# accumulator clears of in-proj/out-proj/down GEMM phases moved from the unit-loop head into the epilogue (issued between the epilogue's stores), prologue clears once
# speedup vs baseline: 1.0381x; 1.0060x over previous
.LBB0_132:
	s_add_u32 s42, s75, 0xf100000
	s_addc_u32 s43, s74, 0
	s_add_u32 s44, s75, 0x2d100000
	s_addc_u32 s45, s74, 0
	s_add_u32 s46, s75, 0x35100000
	s_addc_u32 s47, s74, 0
	s_lshl_b32 s22, s52, 11
	s_lshl_b64 s[12:13], s[22:23], 2
	s_add_u32 s48, s10, s12
	s_addc_u32 s49, s9, s13
	s_add_u32 s50, s75, 0x15100000
	s_addc_u32 s51, s74, 0
	s_add_u32 s52, s75, 0x1b100000
	s_addc_u32 s53, s74, 0
	s_add_u32 s54, s75, 0x21100000
	s_addc_u32 s55, s74, 0
	s_and_b32 s10, s6, 3
	s_add_i32 m0, s93, 0x18000
	v_lshl_add_u64 v[6:7], v[6:7], 0, s[88:89]
	s_lshl_b32 s14, s8, 13
	s_lshl_b32 s16, s10, 12
	s_waitcnt vmcnt(2)
	s_barrier
	global_load_lds_dwordx4 v[6:7], off
	v_lshl_add_u64 v[4:5], v[4:5], 0, s[88:89]
	s_add_i32 m0, s93, 0x1a000
	s_add_i32 s9, s93, 0x8000
	s_add_i32 s97, s93, 0xa000
	global_load_lds_dwordx4 v[4:5], off
	v_lshl_add_u64 v[0:1], v[0:1], 0, s[88:89]
	s_mov_b32 m0, s9
	s_add_u32 s12, s0, 0x8080
	global_load_lds_dwordx4 v[0:1], off
	v_lshl_add_u64 v[0:1], v[2:3], 0, s[88:89]
	s_mov_b32 m0, s97
	s_addc_u32 s13, s1, 0
	global_load_lds_dwordx4 v[0:1], off
	s_add_i32 m0, s93, 0x1c000
	v_lshl_add_u64 v[0:1], s[12:13], 0, v[166:167]
	global_load_lds_dwordx4 v[0:1], off
	v_lshl_add_u64 v[0:1], s[12:13], 0, v[162:163]
	s_add_i32 m0, s93, 0x1e000
	v_lshlrev_b32_e32 v5, 2, v8
	global_load_lds_dwordx4 v[0:1], off
	v_bfe_u32 v1, v8, 4, 2
	v_and_b32_e32 v0, 15, v8
	v_lshlrev_b32_e32 v4, 4, v1
	v_lshl_or_b32 v2, s8, 6, v0
	v_lshl_or_b32 v4, v0, 6, v4
	v_lshlrev_b32_e32 v0, 3, v0
	v_lshlrev_b32_e32 v3, 3, v1
	v_and_b32_e32 v5, 32, v5
	v_lshl_or_b32 v0, v1, 7, v0
	v_and_b32_e32 v1, 1, v8
	s_sext_i32_i16 s6, s36
	v_bitop3_b32 v6, v4, s14, v5 bitop3:0xde
	v_bitop3_b32 v182, v4, s16, v5 bitop3:0xde
	v_cmp_eq_u32_e64 s[36:37], 0, v1
	v_lshlrev_b32_e32 v4, 5, v1
	v_sub_u32_e32 v183, v2, v1
	v_lshlrev_b32_e32 v1, 13, v13
	v_and_b32_e32 v1, 0xffffc000, v1
	v_lshl_add_u32 v1, v12, 10, v1
	v_and_b32_e32 v2, 1, v13
	v_lshl_or_b32 v1, v2, 6, v1
	s_cmpk_lt_u32 s7, 0x100
	v_lshl_add_u32 v170, v14, 1, v1
	v_lshlrev_b32_e32 v1, 13, v9
	s_cselect_b64 s[56:57], -1, 0
	s_lshl_b32 s7, s8, 2
	v_and_b32_e32 v1, 0xffffc000, v1
	s_waitcnt vmcnt(6)
	s_or_b32 s8, s7, s10
	s_lshl_b32 s7, s10, 6
	v_lshl_add_u32 v1, v10, 10, v1
	v_and_b32_e32 v2, 1, v9
	s_add_u32 s58, s48, 0x1000
	v_lshl_or_b32 v1, v2, 6, v1
	s_mov_b32 s22, 0
	s_addc_u32 s59, s49, 0
	v_lshl_or_b32 v184, s10, 5, v3
	v_or3_b32 v185, s7, v4, v3
	v_mov_b32_e32 v171, v49
	v_lshl_add_u32 v172, v11, 1, v1
	v_mov_b32_e32 v173, v49
	v_add_u32_e32 v186, 0, v6
	v_lshlrev_b32_e32 v187, 1, v0
	s_barrier
	v_mov_b32_e32 v32, 0
	v_mov_b32_e32 v33, 0
	v_mov_b32_e32 v34, 0
	v_mov_b32_e32 v35, 0
	v_mov_b32_e32 v36, 0
	v_mov_b32_e32 v37, 0
	v_mov_b32_e32 v38, 0
	v_mov_b32_e32 v39, 0
	v_mov_b32_e32 v40, 0
	v_mov_b32_e32 v41, 0
	v_mov_b32_e32 v42, 0
	v_mov_b32_e32 v43, 0
	v_mov_b32_e32 v44, 0
	v_mov_b32_e32 v45, 0
	v_mov_b32_e32 v46, 0
	v_mov_b32_e32 v47, 0
	v_mov_b32_e32 v50, 0
	v_mov_b32_e32 v51, 0
	v_mov_b32_e32 v52, 0
	v_mov_b32_e32 v53, 0
	v_mov_b32_e32 v54, 0
	v_mov_b32_e32 v55, 0
	v_mov_b32_e32 v56, 0
	v_mov_b32_e32 v57, 0
	v_mov_b32_e32 v58, 0
	v_mov_b32_e32 v59, 0
	v_mov_b32_e32 v60, 0
	v_mov_b32_e32 v61, 0
	v_mov_b32_e32 v62, 0
	v_mov_b32_e32 v63, 0
	v_mov_b32_e32 v64, 0
	v_mov_b32_e32 v65, 0
	v_mov_b32_e32 v66, 0
	v_mov_b32_e32 v67, 0
	v_mov_b32_e32 v68, 0
	v_mov_b32_e32 v69, 0
	v_mov_b32_e32 v70, 0
	v_mov_b32_e32 v71, 0
	v_mov_b32_e32 v72, 0
	v_mov_b32_e32 v73, 0
	v_mov_b32_e32 v74, 0
	v_mov_b32_e32 v75, 0
	v_mov_b32_e32 v76, 0
	v_mov_b32_e32 v77, 0
	v_mov_b32_e32 v78, 0
	v_mov_b32_e32 v79, 0
	v_mov_b32_e32 v80, 0
	v_mov_b32_e32 v81, 0
	v_mov_b32_e32 v82, 0
	v_mov_b32_e32 v83, 0
	v_mov_b32_e32 v84, 0
	v_mov_b32_e32 v85, 0
	v_mov_b32_e32 v86, 0
	v_mov_b32_e32 v87, 0
	v_mov_b32_e32 v88, 0
	v_mov_b32_e32 v89, 0
	v_mov_b32_e32 v90, 0
	v_mov_b32_e32 v91, 0
	v_mov_b32_e32 v92, 0
	v_mov_b32_e32 v93, 0
	v_mov_b32_e32 v94, 0
	v_mov_b32_e32 v95, 0
	v_mov_b32_e32 v96, 0
	v_mov_b32_e32 v97, 0
	v_mov_b32_e32 v98, 0
	v_mov_b32_e32 v99, 0
	v_mov_b32_e32 v100, 0
	v_mov_b32_e32 v101, 0
	v_mov_b32_e32 v102, 0
	v_mov_b32_e32 v103, 0
	v_mov_b32_e32 v104, 0
	v_mov_b32_e32 v105, 0
	v_mov_b32_e32 v106, 0
	v_mov_b32_e32 v107, 0
	v_mov_b32_e32 v108, 0
	v_mov_b32_e32 v109, 0
	v_mov_b32_e32 v110, 0
	v_mov_b32_e32 v111, 0
	v_mov_b32_e32 v112, 0
	v_mov_b32_e32 v113, 0
	v_mov_b32_e32 v114, 0
	v_mov_b32_e32 v115, 0
	v_mov_b32_e32 v116, 0
	v_mov_b32_e32 v117, 0
	v_mov_b32_e32 v118, 0
	v_mov_b32_e32 v119, 0
	v_mov_b32_e32 v120, 0
	v_mov_b32_e32 v121, 0
	v_mov_b32_e32 v122, 0
	v_mov_b32_e32 v123, 0
	v_mov_b32_e32 v124, 0
	v_mov_b32_e32 v125, 0
	v_mov_b32_e32 v126, 0
	v_mov_b32_e32 v127, 0
	v_mov_b32_e32 v128, 0
	v_mov_b32_e32 v129, 0
	v_mov_b32_e32 v130, 0
	v_mov_b32_e32 v131, 0
	v_mov_b32_e32 v132, 0
	v_mov_b32_e32 v133, 0
	v_mov_b32_e32 v134, 0
	v_mov_b32_e32 v135, 0
	v_mov_b32_e32 v136, 0
	v_mov_b32_e32 v137, 0
	v_mov_b32_e32 v138, 0
	v_mov_b32_e32 v139, 0
	v_mov_b32_e32 v140, 0
	v_mov_b32_e32 v141, 0
	v_mov_b32_e32 v142, 0
	v_mov_b32_e32 v143, 0
	v_mov_b32_e32 v144, 0
	v_mov_b32_e32 v145, 0
	v_mov_b32_e32 v146, 0
	v_mov_b32_e32 v147, 0
	v_mov_b32_e32 v148, 0
	v_mov_b32_e32 v149, 0
	v_mov_b32_e32 v150, 0
	v_mov_b32_e32 v151, 0
	v_mov_b32_e32 v152, 0
	v_mov_b32_e32 v153, 0
	v_mov_b32_e32 v154, 0
	v_mov_b32_e32 v155, 0
	v_mov_b32_e32 v156, 0
	v_mov_b32_e32 v157, 0
	v_mov_b32_e32 v158, 0
	v_mov_b32_e32 v159, 0
	v_mov_b32_e32 v160, 0
	v_mov_b32_e32 v161, 0
	s_branch .LBB0_135

.LBB0_137:
	s_ashr_i32 s61, s60, 31
	s_lshl_b64 s[12:13], s[60:61], 18
	s_add_u32 s64, s76, s12
	s_addc_u32 s65, s77, s13
	s_and_b64 s[12:13], s[38:39], exec
	s_cselect_b32 s7, s65, s5
	s_cselect_b32 s10, s64, s4
	s_ashr_i32 s63, s62, 31
	s_lshl_b64 s[12:13], s[62:63], 18
	s_add_u32 s66, s78, s12
	s_addc_u32 s67, s79, s13
	s_and_b64 s[12:13], s[38:39], exec
	s_cselect_b32 s12, s67, s1
	s_cselect_b32 s13, s66, s0
	s_add_u32 s70, s4, 0x20080
	s_addc_u32 s71, s5, 0
	s_add_u32 s4, s0, 0x100
	s_addc_u32 s5, s1, 0
	s_mov_b32 s14, -2

.LBB0_144:
	s_add_i32 s0, s6, -15
	v_lshl_or_b32 v48, s0, 7, v184
	v_lshlrev_b64 v[0:1], 2, v[48:49]
	v_lshl_add_u64 v[4:5], s[48:49], 0, v[0:1]
	v_lshl_add_u64 v[12:13], s[58:59], 0, v[0:1]
	global_load_dwordx4 v[0:3], v[4:5], off offset:16
	global_load_dwordx4 v[8:11], v[4:5], off
	s_nop 0
	global_load_dwordx4 v[4:7], v[12:13], off offset:16
	s_nop 0
	global_load_dwordx4 v[12:15], v[12:13], off
	s_and_b32 s1, s0, 1
	s_lshl_b32 s0, s0, 2
	s_and_b32 s0, s0, 0xffffff8
	s_add_i32 s0, s8, s0
	s_lshl_b32 s4, s68, 9
	s_lshl_b32 s0, s0, 4
	s_add_i32 s0, s0, s4
	s_or_b32 s70, s0, s1
	s_ashr_i32 s71, s70, 31
	s_lshl_b64 s[0:1], s[70:71], 10
	s_waitcnt vmcnt(0)
	v_fmamk_f32 v16, v158, 0x3a800000, v8
	v_med3_f32 v16, v16, s15, v233
	v_mul_f32_e32 v16, 0xbfb8aa3b, v16
	v_exp_f32_e32 v18, v16
	v_fmamk_f32 v17, v150, 0x3a800000, v12
	v_med3_f32 v17, v17, s15, v233
	v_mul_f32_e32 v16, 0xbfb8aa3b, v17
	v_add_f32_e32 v17, 1.0, v18
	v_rcp_f32_e32 v18, v17
	v_fmamk_f32 v17, v159, 0x3a800000, v9
	v_med3_f32 v17, v17, s15, v233
	v_mul_f32_e32 v17, 0xbfb8aa3b, v17
	v_exp_f32_e32 v20, v17
	v_fmamk_f32 v19, v151, 0x3a800000, v13
	v_med3_f32 v19, v19, s15, v233
	v_mul_f32_e32 v17, 0xbfb8aa3b, v19
	v_exp_f32_e32 v16, v16
	v_exp_f32_e32 v17, v17
	v_add_f32_e32 v19, 1.0, v20
	v_rcp_f32_e32 v19, v19
	v_fmamk_f32 v21, v153, 0x3a800000, v15
	v_pk_add_f32 v[16:17], v[16:17], 1.0 op_sel_hi:[1,0]
	v_med3_f32 v21, v21, s15, v233
	v_rcp_f32_e32 v22, v16
	v_rcp_f32_e32 v23, v17
	v_pk_mul_f32 v[16:17], v[16:17], v[18:19]
	v_fmamk_f32 v18, v160, 0x3a800000, v10
	v_med3_f32 v18, v18, s15, v233
	v_mul_f32_e32 v18, 0xbfb8aa3b, v18
	v_exp_f32_e32 v20, v18
	v_fmamk_f32 v19, v152, 0x3a800000, v14
	v_med3_f32 v19, v19, s15, v233
	v_mul_f32_e32 v18, 0xbfb8aa3b, v19
	v_add_f32_e32 v19, 1.0, v20
	v_rcp_f32_e32 v20, v19
	v_fmamk_f32 v19, v161, 0x3a800000, v11
	v_med3_f32 v19, v19, s15, v233
	v_mul_f32_e32 v19, 0xbfb8aa3b, v19
	v_exp_f32_e32 v24, v19
	v_mul_f32_e32 v19, 0xbfb8aa3b, v21
	v_exp_f32_e32 v18, v18
	v_exp_f32_e32 v19, v19
	v_add_f32_e32 v21, 1.0, v24
	v_rcp_f32_e32 v21, v21
	v_fmamk_f32 v25, v147, 0x3a800000, v5
	v_pk_add_f32 v[18:19], v[18:19], 1.0 op_sel_hi:[1,0]
	v_med3_f32 v25, v25, s15, v233
	v_rcp_f32_e32 v28, v18
	v_rcp_f32_e32 v29, v19
	v_pk_mul_f32 v[18:19], v[18:19], v[20:21]
	v_fmamk_f32 v20, v154, 0x3a800000, v0
	v_med3_f32 v20, v20, s15, v233
	v_mul_f32_e32 v20, 0xbfb8aa3b, v20
	v_exp_f32_e32 v24, v20
	v_fmamk_f32 v21, v146, 0x3a800000, v4
	v_med3_f32 v21, v21, s15, v233
	v_mul_f32_e32 v20, 0xbfb8aa3b, v21
	v_add_f32_e32 v21, 1.0, v24
	v_rcp_f32_e32 v24, v21
	v_fmamk_f32 v21, v155, 0x3a800000, v1
	v_med3_f32 v21, v21, s15, v233
	v_mul_f32_e32 v21, 0xbfb8aa3b, v21
	v_exp_f32_e32 v26, v21
	v_mul_f32_e32 v21, 0xbfb8aa3b, v25
	v_exp_f32_e32 v20, v20
	v_exp_f32_e32 v21, v21
	v_add_f32_e32 v25, 1.0, v26
	v_rcp_f32_e32 v25, v25
	v_fmamk_f32 v27, v149, 0x3a800000, v7
	v_pk_add_f32 v[20:21], v[20:21], 1.0 op_sel_hi:[1,0]
	v_med3_f32 v27, v27, s15, v233
	v_rcp_f32_e32 v30, v20
	v_rcp_f32_e32 v31, v21
	v_pk_mul_f32 v[20:21], v[20:21], v[24:25]
	v_fmamk_f32 v24, v156, 0x3a800000, v2
	v_med3_f32 v24, v24, s15, v233
	v_mul_f32_e32 v24, 0xbfb8aa3b, v24
	v_exp_f32_e32 v26, v24
	v_fmamk_f32 v25, v148, 0x3a800000, v6
	v_med3_f32 v25, v25, s15, v233
	v_mul_f32_e32 v24, 0xbfb8aa3b, v25
	v_add_f32_e32 v25, 1.0, v26
	v_rcp_f32_e32 v26, v25
	v_fmamk_f32 v25, v157, 0x3a800000, v3
	v_med3_f32 v25, v25, s15, v233
	v_mul_f32_e32 v25, 0xbfb8aa3b, v25
	v_exp_f32_e32 v48, v25
	v_mul_f32_e32 v25, 0xbfb8aa3b, v27
	v_exp_f32_e32 v24, v24
	v_exp_f32_e32 v25, v25
	v_add_f32_e32 v27, 1.0, v48
	v_rcp_f32_e32 v27, v27
	v_cvt_pk_bf16_f32 v16, v16, v17
	v_pk_add_f32 v[24:25], v[24:25], 1.0 op_sel_hi:[1,0]
	v_cvt_pk_bf16_f32 v17, v18, v19
	v_rcp_f32_e32 v48, v24
	v_rcp_f32_e32 v174, v25
	v_pk_mul_f32 v[26:27], v[24:25], v[26:27]
	v_cvt_pk_bf16_f32 v18, v20, v21
	v_or_b32_e32 v20, s0, v187
	v_mov_b32_e32 v21, s1
	v_cvt_pk_bf16_f32 v19, v26, v27
	v_lshl_add_u64 v[24:25], s[44:45], 0, v[20:21]
	global_store_dwordx4 v[24:25], v[16:19], off nt
	v_mov_b32_e32 v146, 0
	v_mov_b32_e32 v147, 0
	v_mov_b32_e32 v148, 0
	v_mov_b32_e32 v149, 0
	v_mov_b32_e32 v150, 0
	v_mov_b32_e32 v151, 0
	v_mov_b32_e32 v152, 0
	v_mov_b32_e32 v153, 0
	v_mov_b32_e32 v154, 0
	v_mov_b32_e32 v155, 0
	v_mov_b32_e32 v156, 0
	v_mov_b32_e32 v157, 0
	v_mov_b32_e32 v158, 0
	v_mov_b32_e32 v159, 0
	v_mov_b32_e32 v160, 0
	v_mov_b32_e32 v161, 0
	v_lshl_add_u64 v[20:21], s[46:47], 0, v[20:21]
	v_fmamk_f32 v25, v133, 0x3a800000, v7
	v_cvt_pk_bf16_f32 v16, v22, v23
	v_cvt_pk_bf16_f32 v17, v28, v29
	v_cvt_pk_bf16_f32 v18, v30, v31
	v_cvt_pk_bf16_f32 v19, v48, v174
	global_store_dwordx4 v[20:21], v[16:19], off nt
	v_mov_b32_e32 v133, 0
	v_fmamk_f32 v21, v137, 0x3a800000, v15
	v_med3_f32 v21, v21, s15, v233
	v_fmamk_f32 v16, v142, 0x3a800000, v8
	v_med3_f32 v16, v16, s15, v233
	v_mul_f32_e32 v16, 0xbfb8aa3b, v16
	v_exp_f32_e32 v18, v16
	v_fmamk_f32 v17, v134, 0x3a800000, v12
	v_med3_f32 v17, v17, s15, v233
	v_mul_f32_e32 v16, 0xbfb8aa3b, v17
	v_add_f32_e32 v17, 1.0, v18
	v_rcp_f32_e32 v18, v17
	v_fmamk_f32 v17, v143, 0x3a800000, v9
	v_med3_f32 v17, v17, s15, v233
	v_mul_f32_e32 v17, 0xbfb8aa3b, v17
	v_exp_f32_e32 v20, v17
	v_fmamk_f32 v19, v135, 0x3a800000, v13
	v_med3_f32 v19, v19, s15, v233
	v_mul_f32_e32 v17, 0xbfb8aa3b, v19
	v_exp_f32_e32 v16, v16
	v_exp_f32_e32 v17, v17
	v_add_f32_e32 v19, 1.0, v20
	v_rcp_f32_e32 v19, v19
	v_fmamk_f32 v23, v131, 0x3a800000, v5
	v_pk_add_f32 v[16:17], v[16:17], 1.0 op_sel_hi:[1,0]
	v_med3_f32 v23, v23, s15, v233
	v_rcp_f32_e32 v26, v16
	v_pk_mul_f32 v[18:19], v[16:17], v[18:19]
	v_fmamk_f32 v16, v144, 0x3a800000, v10
	v_med3_f32 v16, v16, s15, v233
	v_mul_f32_e32 v16, 0xbfb8aa3b, v16
	v_exp_f32_e32 v20, v16
	v_rcp_f32_e32 v27, v17
	v_fmamk_f32 v17, v136, 0x3a800000, v14
	v_med3_f32 v17, v17, s15, v233
	v_mul_f32_e32 v16, 0xbfb8aa3b, v17
	v_add_f32_e32 v17, 1.0, v20
	v_rcp_f32_e32 v20, v17
	v_fmamk_f32 v17, v145, 0x3a800000, v11
	v_med3_f32 v17, v17, s15, v233
	v_mul_f32_e32 v17, 0xbfb8aa3b, v17
	v_exp_f32_e32 v22, v17
	v_mul_f32_e32 v17, 0xbfb8aa3b, v21
	v_exp_f32_e32 v16, v16
	v_exp_f32_e32 v17, v17
	v_add_f32_e32 v21, 1.0, v22
	v_rcp_f32_e32 v21, v21
	v_med3_f32 v25, v25, s15, v233
	v_pk_add_f32 v[16:17], v[16:17], 1.0 op_sel_hi:[1,0]
	s_or_b32 s0, s70, 2
	v_rcp_f32_e32 v28, v16
	v_pk_mul_f32 v[20:21], v[16:17], v[20:21]
	v_fmamk_f32 v16, v138, 0x3a800000, v0
	v_med3_f32 v16, v16, s15, v233
	v_mul_f32_e32 v16, 0xbfb8aa3b, v16
	v_exp_f32_e32 v22, v16
	v_rcp_f32_e32 v29, v17
	v_fmamk_f32 v17, v130, 0x3a800000, v4
	v_med3_f32 v17, v17, s15, v233
	v_mul_f32_e32 v16, 0xbfb8aa3b, v17
	v_add_f32_e32 v17, 1.0, v22
	v_rcp_f32_e32 v22, v17
	v_fmamk_f32 v17, v139, 0x3a800000, v1
	v_med3_f32 v17, v17, s15, v233
	v_mul_f32_e32 v17, 0xbfb8aa3b, v17
	v_exp_f32_e32 v24, v17
	v_mul_f32_e32 v17, 0xbfb8aa3b, v23
	v_exp_f32_e32 v16, v16
	v_exp_f32_e32 v17, v17
	v_add_f32_e32 v23, 1.0, v24
	v_rcp_f32_e32 v23, v23
	s_ashr_i32 s1, s0, 31
	v_pk_add_f32 v[16:17], v[16:17], 1.0 op_sel_hi:[1,0]
	s_lshl_b64 s[0:1], s[0:1], 10
	v_rcp_f32_e32 v30, v16
	v_pk_mul_f32 v[22:23], v[16:17], v[22:23]
	v_fmamk_f32 v16, v140, 0x3a800000, v2
	v_med3_f32 v16, v16, s15, v233
	v_mul_f32_e32 v16, 0xbfb8aa3b, v16
	v_exp_f32_e32 v24, v16
	v_rcp_f32_e32 v31, v17
	v_fmamk_f32 v17, v132, 0x3a800000, v6
	v_med3_f32 v17, v17, s15, v233
	v_mul_f32_e32 v16, 0xbfb8aa3b, v17
	v_add_f32_e32 v17, 1.0, v24
	v_rcp_f32_e32 v24, v17
	v_fmamk_f32 v17, v141, 0x3a800000, v3
	v_med3_f32 v17, v17, s15, v233
	v_mul_f32_e32 v17, 0xbfb8aa3b, v17
	v_exp_f32_e32 v48, v17
	v_mul_f32_e32 v17, 0xbfb8aa3b, v25
	v_exp_f32_e32 v16, v16
	v_exp_f32_e32 v17, v17
	v_add_f32_e32 v25, 1.0, v48
	v_rcp_f32_e32 v25, v25
	v_pk_add_f32 v[16:17], v[16:17], 1.0 op_sel_hi:[1,0]
	s_nop 0
	v_rcp_f32_e32 v48, v16
	v_rcp_f32_e32 v174, v17
	v_pk_mul_f32 v[24:25], v[16:17], v[24:25]
	v_cvt_pk_bf16_f32 v17, v20, v21
	v_or_b32_e32 v20, s0, v187
	v_mov_b32_e32 v21, s1
	v_cvt_pk_bf16_f32 v16, v18, v19
	v_cvt_pk_bf16_f32 v18, v22, v23
	v_cvt_pk_bf16_f32 v19, v24, v25
	v_lshl_add_u64 v[22:23], s[44:45], 0, v[20:21]
	global_store_dwordx4 v[22:23], v[16:19], off nt
	v_mov_b32_e32 v130, 0
	v_mov_b32_e32 v131, 0
	v_mov_b32_e32 v132, 0
	v_mov_b32_e32 v134, 0
	v_mov_b32_e32 v135, 0
	v_mov_b32_e32 v136, 0
	v_mov_b32_e32 v137, 0
	v_mov_b32_e32 v138, 0
	v_mov_b32_e32 v139, 0
	v_mov_b32_e32 v140, 0
	v_mov_b32_e32 v141, 0
	v_mov_b32_e32 v142, 0
	v_mov_b32_e32 v143, 0
	v_mov_b32_e32 v144, 0
	v_mov_b32_e32 v145, 0
	v_lshl_add_u64 v[20:21], s[46:47], 0, v[20:21]
	v_fmamk_f32 v23, v115, 0x3a800000, v5
	v_cvt_pk_bf16_f32 v16, v26, v27
	v_cvt_pk_bf16_f32 v17, v28, v29
	v_cvt_pk_bf16_f32 v18, v30, v31
	v_cvt_pk_bf16_f32 v19, v48, v174
	global_store_dwordx4 v[20:21], v[16:19], off nt
	v_mov_b32_e32 v115, 0
	v_fmamk_f32 v21, v121, 0x3a800000, v15
	v_med3_f32 v21, v21, s15, v233
	v_fmamk_f32 v16, v126, 0x3a800000, v8
	v_med3_f32 v16, v16, s15, v233
	v_mul_f32_e32 v16, 0xbfb8aa3b, v16
	v_exp_f32_e32 v18, v16
	v_fmamk_f32 v17, v118, 0x3a800000, v12
	v_med3_f32 v17, v17, s15, v233
	v_mul_f32_e32 v16, 0xbfb8aa3b, v17
	v_add_f32_e32 v17, 1.0, v18
	v_rcp_f32_e32 v18, v17
	v_fmamk_f32 v17, v127, 0x3a800000, v9
	v_med3_f32 v17, v17, s15, v233
	v_mul_f32_e32 v17, 0xbfb8aa3b, v17
	v_exp_f32_e32 v20, v17
	v_fmamk_f32 v19, v119, 0x3a800000, v13
	v_med3_f32 v19, v19, s15, v233
	v_mul_f32_e32 v17, 0xbfb8aa3b, v19
	v_exp_f32_e32 v16, v16
	v_exp_f32_e32 v17, v17
	v_add_f32_e32 v19, 1.0, v20
	v_rcp_f32_e32 v19, v19
	v_med3_f32 v23, v23, s15, v233
	v_pk_add_f32 v[16:17], v[16:17], 1.0 op_sel_hi:[1,0]
	v_fmamk_f32 v25, v117, 0x3a800000, v7
	v_rcp_f32_e32 v26, v16
	v_pk_mul_f32 v[18:19], v[16:17], v[18:19]
	v_fmamk_f32 v16, v128, 0x3a800000, v10
	v_med3_f32 v16, v16, s15, v233
	v_mul_f32_e32 v16, 0xbfb8aa3b, v16
	v_exp_f32_e32 v20, v16
	v_rcp_f32_e32 v27, v17
	v_fmamk_f32 v17, v120, 0x3a800000, v14
	v_med3_f32 v17, v17, s15, v233
	v_mul_f32_e32 v16, 0xbfb8aa3b, v17
	v_add_f32_e32 v17, 1.0, v20
	v_rcp_f32_e32 v20, v17
	v_fmamk_f32 v17, v129, 0x3a800000, v11
	v_med3_f32 v17, v17, s15, v233
	v_mul_f32_e32 v17, 0xbfb8aa3b, v17
	v_exp_f32_e32 v22, v17
	v_mul_f32_e32 v17, 0xbfb8aa3b, v21
	v_exp_f32_e32 v16, v16
	v_exp_f32_e32 v17, v17
	v_add_f32_e32 v21, 1.0, v22
	v_rcp_f32_e32 v21, v21
	v_med3_f32 v25, v25, s15, v233
	v_pk_add_f32 v[16:17], v[16:17], 1.0 op_sel_hi:[1,0]
	s_or_b32 s0, s70, 4
	v_rcp_f32_e32 v28, v16
	v_pk_mul_f32 v[20:21], v[16:17], v[20:21]
	v_fmamk_f32 v16, v122, 0x3a800000, v0
	v_med3_f32 v16, v16, s15, v233
	v_mul_f32_e32 v16, 0xbfb8aa3b, v16
	v_exp_f32_e32 v22, v16
	v_rcp_f32_e32 v29, v17
	v_fmamk_f32 v17, v114, 0x3a800000, v4
	v_med3_f32 v17, v17, s15, v233
	v_mul_f32_e32 v16, 0xbfb8aa3b, v17
	v_add_f32_e32 v17, 1.0, v22
	v_rcp_f32_e32 v22, v17
	v_fmamk_f32 v17, v123, 0x3a800000, v1
	v_med3_f32 v17, v17, s15, v233
	v_mul_f32_e32 v17, 0xbfb8aa3b, v17
	v_exp_f32_e32 v24, v17
	v_mul_f32_e32 v17, 0xbfb8aa3b, v23
	v_exp_f32_e32 v16, v16
	v_exp_f32_e32 v17, v17
	v_add_f32_e32 v23, 1.0, v24
	v_rcp_f32_e32 v23, v23
	s_ashr_i32 s1, s0, 31
	v_pk_add_f32 v[16:17], v[16:17], 1.0 op_sel_hi:[1,0]
	s_lshl_b64 s[0:1], s[0:1], 10
	v_rcp_f32_e32 v30, v16
	v_pk_mul_f32 v[22:23], v[16:17], v[22:23]
	v_fmamk_f32 v16, v124, 0x3a800000, v2
	v_med3_f32 v16, v16, s15, v233
	v_mul_f32_e32 v16, 0xbfb8aa3b, v16
	v_exp_f32_e32 v24, v16
	v_rcp_f32_e32 v31, v17
	v_fmamk_f32 v17, v116, 0x3a800000, v6
	v_med3_f32 v17, v17, s15, v233
	v_mul_f32_e32 v16, 0xbfb8aa3b, v17
	v_add_f32_e32 v17, 1.0, v24
	v_rcp_f32_e32 v24, v17
	v_fmamk_f32 v17, v125, 0x3a800000, v3
	v_med3_f32 v17, v17, s15, v233
	v_mul_f32_e32 v17, 0xbfb8aa3b, v17
	v_exp_f32_e32 v48, v17
	v_mul_f32_e32 v17, 0xbfb8aa3b, v25
	v_exp_f32_e32 v16, v16
	v_exp_f32_e32 v17, v17
	v_add_f32_e32 v25, 1.0, v48
	v_rcp_f32_e32 v25, v25
	v_pk_add_f32 v[16:17], v[16:17], 1.0 op_sel_hi:[1,0]
	s_nop 0
	v_rcp_f32_e32 v48, v16
	v_rcp_f32_e32 v174, v17
	v_pk_mul_f32 v[24:25], v[16:17], v[24:25]
	v_cvt_pk_bf16_f32 v17, v20, v21
	v_or_b32_e32 v20, s0, v187
	v_mov_b32_e32 v21, s1
	v_cvt_pk_bf16_f32 v16, v18, v19
	v_cvt_pk_bf16_f32 v18, v22, v23
	v_cvt_pk_bf16_f32 v19, v24, v25
	v_lshl_add_u64 v[22:23], s[44:45], 0, v[20:21]
	global_store_dwordx4 v[22:23], v[16:19], off nt
	v_mov_b32_e32 v114, 0
	v_mov_b32_e32 v116, 0
	v_mov_b32_e32 v117, 0
	v_mov_b32_e32 v118, 0
	v_mov_b32_e32 v119, 0
	v_mov_b32_e32 v120, 0
	v_mov_b32_e32 v121, 0
	v_mov_b32_e32 v122, 0
	v_mov_b32_e32 v123, 0
	v_mov_b32_e32 v124, 0
	v_mov_b32_e32 v125, 0
	v_mov_b32_e32 v126, 0
	v_mov_b32_e32 v127, 0
	v_mov_b32_e32 v128, 0
	v_mov_b32_e32 v129, 0
	v_lshl_add_u64 v[20:21], s[46:47], 0, v[20:21]
	v_fmamk_f32 v23, v99, 0x3a800000, v5
	v_cvt_pk_bf16_f32 v16, v26, v27
	v_cvt_pk_bf16_f32 v17, v28, v29
	v_cvt_pk_bf16_f32 v18, v30, v31
	v_cvt_pk_bf16_f32 v19, v48, v174
	global_store_dwordx4 v[20:21], v[16:19], off nt
	v_mov_b32_e32 v99, 0
	v_fmamk_f32 v21, v105, 0x3a800000, v15
	v_med3_f32 v21, v21, s15, v233
	v_fmamk_f32 v16, v110, 0x3a800000, v8
	v_med3_f32 v16, v16, s15, v233
	v_mul_f32_e32 v16, 0xbfb8aa3b, v16
	v_exp_f32_e32 v18, v16
	v_fmamk_f32 v17, v102, 0x3a800000, v12
	v_med3_f32 v17, v17, s15, v233
	v_mul_f32_e32 v16, 0xbfb8aa3b, v17
	v_add_f32_e32 v17, 1.0, v18
	v_rcp_f32_e32 v18, v17
	v_fmamk_f32 v17, v111, 0x3a800000, v9
	v_med3_f32 v17, v17, s15, v233
	v_mul_f32_e32 v17, 0xbfb8aa3b, v17
	v_exp_f32_e32 v20, v17
	v_fmamk_f32 v19, v103, 0x3a800000, v13
	v_med3_f32 v19, v19, s15, v233
	v_mul_f32_e32 v17, 0xbfb8aa3b, v19
	v_exp_f32_e32 v16, v16
	v_exp_f32_e32 v17, v17
	v_add_f32_e32 v19, 1.0, v20
	v_rcp_f32_e32 v19, v19
	v_med3_f32 v23, v23, s15, v233
	v_pk_add_f32 v[16:17], v[16:17], 1.0 op_sel_hi:[1,0]
	v_fmamk_f32 v25, v101, 0x3a800000, v7
	v_rcp_f32_e32 v26, v16
	v_pk_mul_f32 v[18:19], v[16:17], v[18:19]
	v_fmamk_f32 v16, v112, 0x3a800000, v10
	v_med3_f32 v16, v16, s15, v233
	v_mul_f32_e32 v16, 0xbfb8aa3b, v16
	v_exp_f32_e32 v20, v16
	v_rcp_f32_e32 v27, v17
	v_fmamk_f32 v17, v104, 0x3a800000, v14
	v_med3_f32 v17, v17, s15, v233
	v_mul_f32_e32 v16, 0xbfb8aa3b, v17
	v_add_f32_e32 v17, 1.0, v20
	v_rcp_f32_e32 v20, v17
	v_fmamk_f32 v17, v113, 0x3a800000, v11
	v_med3_f32 v17, v17, s15, v233
	v_mul_f32_e32 v17, 0xbfb8aa3b, v17
	v_exp_f32_e32 v22, v17
	v_mul_f32_e32 v17, 0xbfb8aa3b, v21
	v_exp_f32_e32 v16, v16
	v_exp_f32_e32 v17, v17
	v_add_f32_e32 v21, 1.0, v22
	v_rcp_f32_e32 v21, v21
	v_med3_f32 v25, v25, s15, v233
	v_pk_add_f32 v[16:17], v[16:17], 1.0 op_sel_hi:[1,0]
	s_or_b32 s0, s70, 6
	v_rcp_f32_e32 v28, v16
	v_pk_mul_f32 v[20:21], v[16:17], v[20:21]
	v_fmamk_f32 v16, v106, 0x3a800000, v0
	v_med3_f32 v16, v16, s15, v233
	v_mul_f32_e32 v16, 0xbfb8aa3b, v16
	v_exp_f32_e32 v22, v16
	v_rcp_f32_e32 v29, v17
	v_fmamk_f32 v17, v98, 0x3a800000, v4
	v_med3_f32 v17, v17, s15, v233
	v_mul_f32_e32 v16, 0xbfb8aa3b, v17
	v_add_f32_e32 v17, 1.0, v22
	v_rcp_f32_e32 v22, v17
	v_fmamk_f32 v17, v107, 0x3a800000, v1
	v_med3_f32 v17, v17, s15, v233
	v_mul_f32_e32 v17, 0xbfb8aa3b, v17
	v_exp_f32_e32 v24, v17
	v_mul_f32_e32 v17, 0xbfb8aa3b, v23
	v_exp_f32_e32 v16, v16
	v_exp_f32_e32 v17, v17
	v_add_f32_e32 v23, 1.0, v24
	v_rcp_f32_e32 v23, v23
	s_ashr_i32 s1, s0, 31
	v_pk_add_f32 v[16:17], v[16:17], 1.0 op_sel_hi:[1,0]
	s_lshl_b64 s[0:1], s[0:1], 10
	v_rcp_f32_e32 v30, v16
	v_pk_mul_f32 v[22:23], v[16:17], v[22:23]
	v_fmamk_f32 v16, v108, 0x3a800000, v2
	v_med3_f32 v16, v16, s15, v233
	v_mul_f32_e32 v16, 0xbfb8aa3b, v16
	v_exp_f32_e32 v24, v16
	v_rcp_f32_e32 v31, v17
	v_fmamk_f32 v17, v100, 0x3a800000, v6
	v_med3_f32 v17, v17, s15, v233
	v_mul_f32_e32 v16, 0xbfb8aa3b, v17
	v_add_f32_e32 v17, 1.0, v24
	v_rcp_f32_e32 v24, v17
	v_fmamk_f32 v17, v109, 0x3a800000, v3
	v_med3_f32 v17, v17, s15, v233
	v_mul_f32_e32 v17, 0xbfb8aa3b, v17
	v_exp_f32_e32 v48, v17
	v_mul_f32_e32 v17, 0xbfb8aa3b, v25
	v_exp_f32_e32 v16, v16
	v_exp_f32_e32 v17, v17
	v_add_f32_e32 v25, 1.0, v48
	v_rcp_f32_e32 v25, v25
	v_pk_add_f32 v[16:17], v[16:17], 1.0 op_sel_hi:[1,0]
	s_nop 0
	v_rcp_f32_e32 v48, v16
	v_rcp_f32_e32 v174, v17
	v_pk_mul_f32 v[24:25], v[16:17], v[24:25]
	v_cvt_pk_bf16_f32 v17, v20, v21
	v_or_b32_e32 v20, s0, v187
	v_mov_b32_e32 v21, s1
	v_cvt_pk_bf16_f32 v16, v18, v19
	v_cvt_pk_bf16_f32 v18, v22, v23
	v_cvt_pk_bf16_f32 v19, v24, v25
	v_lshl_add_u64 v[22:23], s[44:45], 0, v[20:21]
	global_store_dwordx4 v[22:23], v[16:19], off nt
	v_mov_b32_e32 v98, 0
	v_mov_b32_e32 v100, 0
	v_mov_b32_e32 v101, 0
	v_mov_b32_e32 v102, 0
	v_mov_b32_e32 v103, 0
	v_mov_b32_e32 v104, 0
	v_mov_b32_e32 v105, 0
	v_mov_b32_e32 v106, 0
	v_mov_b32_e32 v107, 0
	v_mov_b32_e32 v108, 0
	v_mov_b32_e32 v109, 0
	v_mov_b32_e32 v110, 0
	v_mov_b32_e32 v111, 0
	v_mov_b32_e32 v112, 0
	v_mov_b32_e32 v113, 0
	v_lshl_add_u64 v[20:21], s[46:47], 0, v[20:21]
	v_fmamk_f32 v23, v83, 0x3a800000, v5
	v_cvt_pk_bf16_f32 v16, v26, v27
	v_cvt_pk_bf16_f32 v17, v28, v29
	v_cvt_pk_bf16_f32 v18, v30, v31
	v_cvt_pk_bf16_f32 v19, v48, v174
	global_store_dwordx4 v[20:21], v[16:19], off nt
	v_mov_b32_e32 v83, 0
	v_fmamk_f32 v21, v89, 0x3a800000, v15
	v_med3_f32 v21, v21, s15, v233
	v_fmamk_f32 v16, v94, 0x3a800000, v8
	v_med3_f32 v16, v16, s15, v233
	v_mul_f32_e32 v16, 0xbfb8aa3b, v16
	v_exp_f32_e32 v18, v16
	v_fmamk_f32 v17, v86, 0x3a800000, v12
	v_med3_f32 v17, v17, s15, v233
	v_mul_f32_e32 v16, 0xbfb8aa3b, v17
	v_add_f32_e32 v17, 1.0, v18
	v_rcp_f32_e32 v18, v17
	v_fmamk_f32 v17, v95, 0x3a800000, v9
	v_med3_f32 v17, v17, s15, v233
	v_mul_f32_e32 v17, 0xbfb8aa3b, v17
	v_exp_f32_e32 v20, v17
	v_fmamk_f32 v19, v87, 0x3a800000, v13
	v_med3_f32 v19, v19, s15, v233
	v_mul_f32_e32 v17, 0xbfb8aa3b, v19
	v_exp_f32_e32 v16, v16
	v_exp_f32_e32 v17, v17
	v_add_f32_e32 v19, 1.0, v20
	v_rcp_f32_e32 v19, v19
	v_med3_f32 v23, v23, s15, v233
	v_pk_add_f32 v[16:17], v[16:17], 1.0 op_sel_hi:[1,0]
	v_fmamk_f32 v25, v85, 0x3a800000, v7
	v_rcp_f32_e32 v26, v16
	v_pk_mul_f32 v[18:19], v[16:17], v[18:19]
	v_fmamk_f32 v16, v96, 0x3a800000, v10
	v_med3_f32 v16, v16, s15, v233
	v_mul_f32_e32 v16, 0xbfb8aa3b, v16
	v_exp_f32_e32 v20, v16
	v_rcp_f32_e32 v27, v17
	v_fmamk_f32 v17, v88, 0x3a800000, v14
	v_med3_f32 v17, v17, s15, v233
	v_mul_f32_e32 v16, 0xbfb8aa3b, v17
	v_add_f32_e32 v17, 1.0, v20
	v_rcp_f32_e32 v20, v17
	v_fmamk_f32 v17, v97, 0x3a800000, v11
	v_med3_f32 v17, v17, s15, v233
	v_mul_f32_e32 v17, 0xbfb8aa3b, v17
	v_exp_f32_e32 v22, v17
	v_mul_f32_e32 v17, 0xbfb8aa3b, v21
	v_exp_f32_e32 v16, v16
	v_exp_f32_e32 v17, v17
	v_add_f32_e32 v21, 1.0, v22
	v_rcp_f32_e32 v21, v21
	v_med3_f32 v25, v25, s15, v233
	v_pk_add_f32 v[16:17], v[16:17], 1.0 op_sel_hi:[1,0]
	s_or_b32 s0, s70, 8
	v_rcp_f32_e32 v28, v16
	v_pk_mul_f32 v[20:21], v[16:17], v[20:21]
	v_fmamk_f32 v16, v90, 0x3a800000, v0
	v_med3_f32 v16, v16, s15, v233
	v_mul_f32_e32 v16, 0xbfb8aa3b, v16
	v_exp_f32_e32 v22, v16
	v_rcp_f32_e32 v29, v17
	v_fmamk_f32 v17, v82, 0x3a800000, v4
	v_med3_f32 v17, v17, s15, v233
	v_mul_f32_e32 v16, 0xbfb8aa3b, v17
	v_add_f32_e32 v17, 1.0, v22
	v_rcp_f32_e32 v22, v17
	v_fmamk_f32 v17, v91, 0x3a800000, v1
	v_med3_f32 v17, v17, s15, v233
	v_mul_f32_e32 v17, 0xbfb8aa3b, v17
	v_exp_f32_e32 v24, v17
	v_mul_f32_e32 v17, 0xbfb8aa3b, v23
	v_exp_f32_e32 v16, v16
	v_exp_f32_e32 v17, v17
	v_add_f32_e32 v23, 1.0, v24
	v_rcp_f32_e32 v23, v23
	s_ashr_i32 s1, s0, 31
	v_pk_add_f32 v[16:17], v[16:17], 1.0 op_sel_hi:[1,0]
	s_lshl_b64 s[0:1], s[0:1], 10
	v_rcp_f32_e32 v30, v16
	v_pk_mul_f32 v[22:23], v[16:17], v[22:23]
	v_fmamk_f32 v16, v92, 0x3a800000, v2
	v_med3_f32 v16, v16, s15, v233
	v_mul_f32_e32 v16, 0xbfb8aa3b, v16
	v_exp_f32_e32 v24, v16
	v_rcp_f32_e32 v31, v17
	v_fmamk_f32 v17, v84, 0x3a800000, v6
	v_med3_f32 v17, v17, s15, v233
	v_mul_f32_e32 v16, 0xbfb8aa3b, v17
	v_add_f32_e32 v17, 1.0, v24
	v_rcp_f32_e32 v24, v17
	v_fmamk_f32 v17, v93, 0x3a800000, v3
	v_med3_f32 v17, v17, s15, v233
	v_mul_f32_e32 v17, 0xbfb8aa3b, v17
	v_exp_f32_e32 v48, v17
	v_mul_f32_e32 v17, 0xbfb8aa3b, v25
	v_exp_f32_e32 v16, v16
	v_exp_f32_e32 v17, v17
	v_add_f32_e32 v25, 1.0, v48
	v_rcp_f32_e32 v25, v25
	v_pk_add_f32 v[16:17], v[16:17], 1.0 op_sel_hi:[1,0]
	s_nop 0
	v_rcp_f32_e32 v48, v16
	v_rcp_f32_e32 v174, v17
	v_pk_mul_f32 v[24:25], v[16:17], v[24:25]
	v_cvt_pk_bf16_f32 v17, v20, v21
	v_or_b32_e32 v20, s0, v187
	v_mov_b32_e32 v21, s1
	v_cvt_pk_bf16_f32 v16, v18, v19
	v_cvt_pk_bf16_f32 v18, v22, v23
	v_cvt_pk_bf16_f32 v19, v24, v25
	v_lshl_add_u64 v[22:23], s[44:45], 0, v[20:21]
	global_store_dwordx4 v[22:23], v[16:19], off nt
	v_mov_b32_e32 v82, 0
	v_mov_b32_e32 v84, 0
	v_mov_b32_e32 v85, 0
	v_mov_b32_e32 v86, 0
	v_mov_b32_e32 v87, 0
	v_mov_b32_e32 v88, 0
	v_mov_b32_e32 v89, 0
	v_mov_b32_e32 v90, 0
	v_mov_b32_e32 v91, 0
	v_mov_b32_e32 v92, 0
	v_mov_b32_e32 v93, 0
	v_mov_b32_e32 v94, 0
	v_mov_b32_e32 v95, 0
	v_mov_b32_e32 v96, 0
	v_mov_b32_e32 v97, 0
	v_lshl_add_u64 v[20:21], s[46:47], 0, v[20:21]
	v_fmamk_f32 v23, v51, 0x3a800000, v5
	v_cvt_pk_bf16_f32 v16, v26, v27
	v_cvt_pk_bf16_f32 v17, v28, v29
	v_cvt_pk_bf16_f32 v18, v30, v31
	v_cvt_pk_bf16_f32 v19, v48, v174
	global_store_dwordx4 v[20:21], v[16:19], off nt
	v_mov_b32_e32 v51, 0
	v_fmamk_f32 v21, v65, 0x3a800000, v15
	v_med3_f32 v21, v21, s15, v233
	v_fmamk_f32 v16, v70, 0x3a800000, v8
	v_med3_f32 v16, v16, s15, v233
	v_mul_f32_e32 v16, 0xbfb8aa3b, v16
	v_exp_f32_e32 v18, v16
	v_fmamk_f32 v17, v62, 0x3a800000, v12
	v_med3_f32 v17, v17, s15, v233
	v_mul_f32_e32 v16, 0xbfb8aa3b, v17
	v_add_f32_e32 v17, 1.0, v18
	v_rcp_f32_e32 v18, v17
	v_fmamk_f32 v17, v71, 0x3a800000, v9
	v_med3_f32 v17, v17, s15, v233
	v_mul_f32_e32 v17, 0xbfb8aa3b, v17
	v_exp_f32_e32 v20, v17
	v_fmamk_f32 v19, v63, 0x3a800000, v13
	v_med3_f32 v19, v19, s15, v233
	v_mul_f32_e32 v17, 0xbfb8aa3b, v19
	v_exp_f32_e32 v16, v16
	v_exp_f32_e32 v17, v17
	v_add_f32_e32 v19, 1.0, v20
	v_rcp_f32_e32 v19, v19
	v_med3_f32 v23, v23, s15, v233
	v_pk_add_f32 v[16:17], v[16:17], 1.0 op_sel_hi:[1,0]
	v_fmamk_f32 v25, v53, 0x3a800000, v7
	v_rcp_f32_e32 v26, v16
	v_pk_mul_f32 v[18:19], v[16:17], v[18:19]
	v_fmamk_f32 v16, v72, 0x3a800000, v10
	v_med3_f32 v16, v16, s15, v233
	v_mul_f32_e32 v16, 0xbfb8aa3b, v16
	v_exp_f32_e32 v20, v16
	v_rcp_f32_e32 v27, v17
	v_fmamk_f32 v17, v64, 0x3a800000, v14
	v_med3_f32 v17, v17, s15, v233
	v_mul_f32_e32 v16, 0xbfb8aa3b, v17
	v_add_f32_e32 v17, 1.0, v20
	v_rcp_f32_e32 v20, v17
	v_fmamk_f32 v17, v73, 0x3a800000, v11
	v_med3_f32 v17, v17, s15, v233
	v_mul_f32_e32 v17, 0xbfb8aa3b, v17
	v_exp_f32_e32 v22, v17
	v_mul_f32_e32 v17, 0xbfb8aa3b, v21
	v_exp_f32_e32 v16, v16
	v_exp_f32_e32 v17, v17
	v_add_f32_e32 v21, 1.0, v22
	v_rcp_f32_e32 v21, v21
	v_med3_f32 v25, v25, s15, v233
	v_pk_add_f32 v[16:17], v[16:17], 1.0 op_sel_hi:[1,0]
	s_or_b32 s0, s70, 10
	v_rcp_f32_e32 v28, v16
	v_pk_mul_f32 v[20:21], v[16:17], v[20:21]
	v_fmamk_f32 v16, v66, 0x3a800000, v0
	v_med3_f32 v16, v16, s15, v233
	v_mul_f32_e32 v16, 0xbfb8aa3b, v16
	v_exp_f32_e32 v22, v16
	v_rcp_f32_e32 v29, v17
	v_fmamk_f32 v17, v50, 0x3a800000, v4
	v_med3_f32 v17, v17, s15, v233
	v_mul_f32_e32 v16, 0xbfb8aa3b, v17
	v_add_f32_e32 v17, 1.0, v22
	v_rcp_f32_e32 v22, v17
	v_fmamk_f32 v17, v67, 0x3a800000, v1
	v_med3_f32 v17, v17, s15, v233
	v_mul_f32_e32 v17, 0xbfb8aa3b, v17
	v_exp_f32_e32 v24, v17
	v_mul_f32_e32 v17, 0xbfb8aa3b, v23
	v_exp_f32_e32 v16, v16
	v_exp_f32_e32 v17, v17
	v_add_f32_e32 v23, 1.0, v24
	v_rcp_f32_e32 v23, v23
	s_ashr_i32 s1, s0, 31
	v_pk_add_f32 v[16:17], v[16:17], 1.0 op_sel_hi:[1,0]
	s_lshl_b64 s[0:1], s[0:1], 10
	v_rcp_f32_e32 v30, v16
	v_pk_mul_f32 v[22:23], v[16:17], v[22:23]
	v_fmamk_f32 v16, v68, 0x3a800000, v2
	v_med3_f32 v16, v16, s15, v233
	v_mul_f32_e32 v16, 0xbfb8aa3b, v16
	v_exp_f32_e32 v24, v16
	v_rcp_f32_e32 v31, v17
	v_fmamk_f32 v17, v52, 0x3a800000, v6
	v_med3_f32 v17, v17, s15, v233
	v_mul_f32_e32 v16, 0xbfb8aa3b, v17
	v_add_f32_e32 v17, 1.0, v24
	v_rcp_f32_e32 v24, v17
	v_fmamk_f32 v17, v69, 0x3a800000, v3
	v_med3_f32 v17, v17, s15, v233
	v_mul_f32_e32 v17, 0xbfb8aa3b, v17
	v_exp_f32_e32 v48, v17
	v_mul_f32_e32 v17, 0xbfb8aa3b, v25
	v_exp_f32_e32 v16, v16
	v_exp_f32_e32 v17, v17
	v_add_f32_e32 v25, 1.0, v48
	v_rcp_f32_e32 v25, v25
	v_pk_add_f32 v[16:17], v[16:17], 1.0 op_sel_hi:[1,0]
	s_nop 0
	v_rcp_f32_e32 v48, v16
	v_rcp_f32_e32 v174, v17
	v_pk_mul_f32 v[24:25], v[16:17], v[24:25]
	v_cvt_pk_bf16_f32 v17, v20, v21
	v_or_b32_e32 v20, s0, v187
	v_mov_b32_e32 v21, s1
	v_cvt_pk_bf16_f32 v16, v18, v19
	v_cvt_pk_bf16_f32 v18, v22, v23
	v_cvt_pk_bf16_f32 v19, v24, v25
	v_lshl_add_u64 v[22:23], s[44:45], 0, v[20:21]
	global_store_dwordx4 v[22:23], v[16:19], off nt
	v_mov_b32_e32 v50, 0
	v_mov_b32_e32 v52, 0
	v_mov_b32_e32 v53, 0
	v_mov_b32_e32 v62, 0
	v_mov_b32_e32 v63, 0
	v_mov_b32_e32 v64, 0
	v_mov_b32_e32 v65, 0
	v_mov_b32_e32 v66, 0
	v_mov_b32_e32 v67, 0
	v_mov_b32_e32 v68, 0
	v_mov_b32_e32 v69, 0
	v_mov_b32_e32 v70, 0
	v_mov_b32_e32 v71, 0
	v_mov_b32_e32 v72, 0
	v_mov_b32_e32 v73, 0
	v_lshl_add_u64 v[20:21], s[46:47], 0, v[20:21]
	v_fmamk_f32 v23, v75, 0x3a800000, v5
	v_cvt_pk_bf16_f32 v16, v26, v27
	v_cvt_pk_bf16_f32 v17, v28, v29
	v_cvt_pk_bf16_f32 v18, v30, v31
	v_cvt_pk_bf16_f32 v19, v48, v174
	global_store_dwordx4 v[20:21], v[16:19], off nt
	v_mov_b32_e32 v75, 0
	v_fmamk_f32 v21, v81, 0x3a800000, v15
	v_med3_f32 v21, v21, s15, v233
	v_fmamk_f32 v16, v44, 0x3a800000, v8
	v_med3_f32 v16, v16, s15, v233
	v_mul_f32_e32 v16, 0xbfb8aa3b, v16
	v_exp_f32_e32 v18, v16
	v_fmamk_f32 v17, v78, 0x3a800000, v12
	v_med3_f32 v17, v17, s15, v233
	v_mul_f32_e32 v16, 0xbfb8aa3b, v17
	v_add_f32_e32 v17, 1.0, v18
	v_rcp_f32_e32 v18, v17
	v_fmamk_f32 v17, v45, 0x3a800000, v9
	v_med3_f32 v17, v17, s15, v233
	v_mul_f32_e32 v17, 0xbfb8aa3b, v17
	v_exp_f32_e32 v20, v17
	v_fmamk_f32 v19, v79, 0x3a800000, v13
	v_med3_f32 v19, v19, s15, v233
	v_mul_f32_e32 v17, 0xbfb8aa3b, v19
	v_exp_f32_e32 v16, v16
	v_exp_f32_e32 v17, v17
	v_add_f32_e32 v19, 1.0, v20
	v_rcp_f32_e32 v19, v19
	v_med3_f32 v23, v23, s15, v233
	v_pk_add_f32 v[16:17], v[16:17], 1.0 op_sel_hi:[1,0]
	v_fmamk_f32 v25, v77, 0x3a800000, v7
	v_rcp_f32_e32 v26, v16
	v_pk_mul_f32 v[18:19], v[16:17], v[18:19]
	v_fmamk_f32 v16, v46, 0x3a800000, v10
	v_med3_f32 v16, v16, s15, v233
	v_mul_f32_e32 v16, 0xbfb8aa3b, v16
	v_exp_f32_e32 v20, v16
	v_rcp_f32_e32 v27, v17
	v_fmamk_f32 v17, v80, 0x3a800000, v14
	v_med3_f32 v17, v17, s15, v233
	v_mul_f32_e32 v16, 0xbfb8aa3b, v17
	v_add_f32_e32 v17, 1.0, v20
	v_rcp_f32_e32 v20, v17
	v_fmamk_f32 v17, v47, 0x3a800000, v11
	v_med3_f32 v17, v17, s15, v233
	v_mul_f32_e32 v17, 0xbfb8aa3b, v17
	v_exp_f32_e32 v22, v17
	v_mul_f32_e32 v17, 0xbfb8aa3b, v21
	v_exp_f32_e32 v16, v16
	v_exp_f32_e32 v17, v17
	v_add_f32_e32 v21, 1.0, v22
	v_rcp_f32_e32 v21, v21
	v_med3_f32 v25, v25, s15, v233
	v_pk_add_f32 v[16:17], v[16:17], 1.0 op_sel_hi:[1,0]
	s_or_b32 s0, s70, 12
	v_rcp_f32_e32 v28, v16
	v_pk_mul_f32 v[20:21], v[16:17], v[20:21]
	v_fmamk_f32 v16, v40, 0x3a800000, v0
	v_med3_f32 v16, v16, s15, v233
	v_mul_f32_e32 v16, 0xbfb8aa3b, v16
	v_exp_f32_e32 v22, v16
	v_rcp_f32_e32 v29, v17
	v_fmamk_f32 v17, v74, 0x3a800000, v4
	v_med3_f32 v17, v17, s15, v233
	v_mul_f32_e32 v16, 0xbfb8aa3b, v17
	v_add_f32_e32 v17, 1.0, v22
	v_rcp_f32_e32 v22, v17
	v_fmamk_f32 v17, v41, 0x3a800000, v1
	v_med3_f32 v17, v17, s15, v233
	v_mul_f32_e32 v17, 0xbfb8aa3b, v17
	v_exp_f32_e32 v24, v17
	v_mul_f32_e32 v17, 0xbfb8aa3b, v23
	v_exp_f32_e32 v16, v16
	v_exp_f32_e32 v17, v17
	v_add_f32_e32 v23, 1.0, v24
	v_rcp_f32_e32 v23, v23
	s_ashr_i32 s1, s0, 31
	v_pk_add_f32 v[16:17], v[16:17], 1.0 op_sel_hi:[1,0]
	s_lshl_b64 s[0:1], s[0:1], 10
	v_rcp_f32_e32 v30, v16
	v_pk_mul_f32 v[22:23], v[16:17], v[22:23]
	v_fmamk_f32 v16, v42, 0x3a800000, v2
	v_med3_f32 v16, v16, s15, v233
	v_mul_f32_e32 v16, 0xbfb8aa3b, v16
	v_exp_f32_e32 v24, v16
	v_rcp_f32_e32 v31, v17
	v_fmamk_f32 v17, v76, 0x3a800000, v6
	v_med3_f32 v17, v17, s15, v233
	v_mul_f32_e32 v16, 0xbfb8aa3b, v17
	v_add_f32_e32 v17, 1.0, v24
	v_rcp_f32_e32 v24, v17
	v_fmamk_f32 v17, v43, 0x3a800000, v3
	v_med3_f32 v17, v17, s15, v233
	v_mul_f32_e32 v17, 0xbfb8aa3b, v17
	v_exp_f32_e32 v48, v17
	v_mul_f32_e32 v17, 0xbfb8aa3b, v25
	v_exp_f32_e32 v16, v16
	v_exp_f32_e32 v17, v17
	v_add_f32_e32 v25, 1.0, v48
	v_rcp_f32_e32 v25, v25
	v_fmamk_f32 v8, v36, 0x3a800000, v8
	v_pk_add_f32 v[16:17], v[16:17], 1.0 op_sel_hi:[1,0]
	v_med3_f32 v8, v8, s15, v233
	v_rcp_f32_e32 v48, v16
	v_rcp_f32_e32 v174, v17
	v_pk_mul_f32 v[24:25], v[16:17], v[24:25]
	v_cvt_pk_bf16_f32 v17, v20, v21
	v_or_b32_e32 v20, s0, v187
	v_mov_b32_e32 v21, s1
	v_cvt_pk_bf16_f32 v16, v18, v19
	v_cvt_pk_bf16_f32 v18, v22, v23
	v_cvt_pk_bf16_f32 v19, v24, v25
	v_lshl_add_u64 v[22:23], s[44:45], 0, v[20:21]
	global_store_dwordx4 v[22:23], v[16:19], off nt
	v_mov_b32_e32 v36, 0
	v_mov_b32_e32 v40, 0
	v_mov_b32_e32 v41, 0
	v_mov_b32_e32 v42, 0
	v_mov_b32_e32 v43, 0
	v_mov_b32_e32 v44, 0
	v_mov_b32_e32 v45, 0
	v_mov_b32_e32 v46, 0
	v_mov_b32_e32 v47, 0
	v_mov_b32_e32 v74, 0
	v_mov_b32_e32 v76, 0
	v_mov_b32_e32 v77, 0
	v_mov_b32_e32 v78, 0
	v_mov_b32_e32 v79, 0
	v_mov_b32_e32 v80, 0
	v_mov_b32_e32 v81, 0
	v_lshl_add_u64 v[20:21], s[46:47], 0, v[20:21]
	v_mul_f32_e32 v8, 0xbfb8aa3b, v8
	v_cvt_pk_bf16_f32 v16, v26, v27
	v_cvt_pk_bf16_f32 v17, v28, v29
	v_cvt_pk_bf16_f32 v18, v30, v31
	v_cvt_pk_bf16_f32 v19, v48, v174
	global_store_dwordx4 v[20:21], v[16:19], off nt
	v_fmamk_f32 v9, v37, 0x3a800000, v9
	v_fmamk_f32 v12, v58, 0x3a800000, v12
	v_exp_f32_e32 v16, v8
	v_med3_f32 v9, v9, s15, v233
	v_med3_f32 v12, v12, s15, v233
	v_mul_f32_e32 v9, 0xbfb8aa3b, v9
	v_mul_f32_e32 v8, 0xbfb8aa3b, v12
	v_add_f32_e32 v12, 1.0, v16
	v_exp_f32_e32 v16, v9
	v_fmamk_f32 v13, v59, 0x3a800000, v13
	v_med3_f32 v13, v13, s15, v233
	v_mul_f32_e32 v9, 0xbfb8aa3b, v13
	v_exp_f32_e32 v8, v8
	v_exp_f32_e32 v9, v9
	v_add_f32_e32 v13, 1.0, v16
	v_rcp_f32_e32 v12, v12
	v_rcp_f32_e32 v13, v13
	v_pk_add_f32 v[8:9], v[8:9], 1.0 op_sel_hi:[1,0]
	v_fmac_f32_e32 v11, 0x3a800000, v39
	v_rcp_f32_e32 v16, v8
	v_pk_mul_f32 v[12:13], v[8:9], v[12:13]
	v_fmamk_f32 v8, v38, 0x3a800000, v10
	v_med3_f32 v8, v8, s15, v233
	v_mul_f32_e32 v8, 0xbfb8aa3b, v8
	v_exp_f32_e32 v10, v8
	v_rcp_f32_e32 v17, v9
	v_fmamk_f32 v9, v60, 0x3a800000, v14
	v_med3_f32 v9, v9, s15, v233
	v_mul_f32_e32 v8, 0xbfb8aa3b, v9
	v_add_f32_e32 v9, 1.0, v10
	v_rcp_f32_e32 v10, v9
	v_med3_f32 v9, v11, s15, v233
	v_mul_f32_e32 v9, 0xbfb8aa3b, v9
	v_exp_f32_e32 v14, v9
	v_fmac_f32_e32 v15, 0x3a800000, v61
	v_med3_f32 v11, v15, s15, v233
	v_mul_f32_e32 v9, 0xbfb8aa3b, v11
	v_exp_f32_e32 v8, v8
	v_exp_f32_e32 v9, v9
	v_add_f32_e32 v11, 1.0, v14
	v_rcp_f32_e32 v11, v11
	v_fmamk_f32 v0, v32, 0x3a800000, v0
	v_med3_f32 v0, v0, s15, v233
	v_pk_add_f32 v[8:9], v[8:9], 1.0 op_sel_hi:[1,0]
	v_mul_f32_e32 v0, 0xbfb8aa3b, v0
	v_rcp_f32_e32 v14, v8
	v_pk_mul_f32 v[10:11], v[8:9], v[10:11]
	v_rcp_f32_e32 v8, v9
	v_exp_f32_e32 v9, v0
	v_fmamk_f32 v1, v33, 0x3a800000, v1
	v_fmamk_f32 v4, v54, 0x3a800000, v4
	v_med3_f32 v1, v1, s15, v233
	v_med3_f32 v4, v4, s15, v233
	v_mul_f32_e32 v1, 0xbfb8aa3b, v1
	v_mul_f32_e32 v0, 0xbfb8aa3b, v4
	v_add_f32_e32 v4, 1.0, v9
	v_exp_f32_e32 v9, v1
	v_fmamk_f32 v5, v55, 0x3a800000, v5
	v_med3_f32 v5, v5, s15, v233
	v_mul_f32_e32 v1, 0xbfb8aa3b, v5
	v_exp_f32_e32 v0, v0
	v_exp_f32_e32 v1, v1
	v_add_f32_e32 v5, 1.0, v9
	v_rcp_f32_e32 v4, v4
	v_rcp_f32_e32 v5, v5
	v_pk_add_f32 v[0:1], v[0:1], 1.0 op_sel_hi:[1,0]
	v_fmac_f32_e32 v3, 0x3a800000, v35
	v_rcp_f32_e32 v9, v0
	v_pk_mul_f32 v[4:5], v[0:1], v[4:5]
	v_fmamk_f32 v0, v34, 0x3a800000, v2
	v_med3_f32 v0, v0, s15, v233
	v_mul_f32_e32 v0, 0xbfb8aa3b, v0
	v_exp_f32_e32 v2, v0
	v_rcp_f32_e32 v15, v1
	v_fmamk_f32 v1, v56, 0x3a800000, v6
	v_med3_f32 v1, v1, s15, v233
	v_mul_f32_e32 v0, 0xbfb8aa3b, v1
	v_add_f32_e32 v1, 1.0, v2
	v_rcp_f32_e32 v2, v1
	v_med3_f32 v1, v3, s15, v233
	v_fmac_f32_e32 v7, 0x3a800000, v57
	v_mul_f32_e32 v1, 0xbfb8aa3b, v1
	v_med3_f32 v3, v7, s15, v233
	v_exp_f32_e32 v6, v1
	v_mul_f32_e32 v1, 0xbfb8aa3b, v3
	v_exp_f32_e32 v0, v0
	v_exp_f32_e32 v1, v1
	v_add_f32_e32 v3, 1.0, v6
	v_rcp_f32_e32 v3, v3
	s_or_b32 s0, s70, 14
	v_pk_add_f32 v[0:1], v[0:1], 1.0 op_sel_hi:[1,0]
	s_ashr_i32 s1, s0, 31
	v_rcp_f32_e32 v18, v0
	v_rcp_f32_e32 v19, v1
	s_lshl_b64 s[0:1], s[0:1], 10
	v_pk_mul_f32 v[6:7], v[0:1], v[2:3]
	v_cvt_pk_bf16_f32 v2, v4, v5
	v_or_b32_e32 v4, s0, v187
	v_mov_b32_e32 v5, s1
	v_cvt_pk_bf16_f32 v0, v12, v13
	v_cvt_pk_bf16_f32 v1, v10, v11
	v_cvt_pk_bf16_f32 v3, v6, v7
	v_lshl_add_u64 v[6:7], s[44:45], 0, v[4:5]
	global_store_dwordx4 v[6:7], v[0:3], off nt
	v_mov_b32_e32 v32, 0
	v_mov_b32_e32 v33, 0
	v_mov_b32_e32 v34, 0
	v_mov_b32_e32 v35, 0
	v_mov_b32_e32 v37, 0
	v_mov_b32_e32 v38, 0
	v_mov_b32_e32 v39, 0
	v_mov_b32_e32 v54, 0
	v_mov_b32_e32 v55, 0
	v_mov_b32_e32 v56, 0
	v_mov_b32_e32 v57, 0
	v_mov_b32_e32 v58, 0
	v_mov_b32_e32 v59, 0
	v_mov_b32_e32 v60, 0
	v_mov_b32_e32 v61, 0
	v_lshl_add_u64 v[4:5], s[46:47], 0, v[4:5]
	s_nop 0
	v_cvt_pk_bf16_f32 v0, v16, v17
	v_cvt_pk_bf16_f32 v1, v14, v8
	v_cvt_pk_bf16_f32 v2, v9, v15
	v_cvt_pk_bf16_f32 v3, v18, v19
	global_store_dwordx4 v[4:5], v[0:3], off nt
	s_cbranch_execnz .LBB0_143

.LBB0_159:
	v_lshl_or_b32 v0, s6, 8, v185
	v_lshl_add_u32 v12, s68, 8, v183
	v_ashrrev_i32_e32 v1, 31, v0
	v_ashrrev_i32_e32 v2, 31, v12
	v_lshl_add_u64 v[0:1], v[0:1], 1, s[4:5]
	v_mul_lo_u32 v4, s0, v2
	v_mul_lo_u32 v5, s1, v12
	v_mad_u64_u32 v[2:3], s[4:5], s0, v12, 0
	v_add3_u32 v3, v3, v4, v5
	v_lshl_add_u64 v[10:11], v[2:3], 1, v[0:1]
	v_pk_mul_f32 v[2:3], v[160:161], s[70:71] op_sel_hi:[1,0]
	v_pk_mul_f32 v[4:5], v[158:159], s[70:71] op_sel_hi:[1,0]
	v_pk_mul_f32 v[6:7], v[156:157], s[70:71] op_sel_hi:[1,0]
	v_pk_mul_f32 v[8:9], v[154:155], s[70:71] op_sel_hi:[1,0]
	v_cvt_pk_bf16_f32 v13, v4, v5
	v_cvt_pk_bf16_f32 v14, v2, v3
	v_cvt_pk_bf16_f32 v15, v8, v9
	v_cvt_pk_bf16_f32 v16, v6, v7
	v_pk_mul_f32 v[2:3], v[152:153], s[70:71] op_sel_hi:[1,0]
	v_pk_mul_f32 v[4:5], v[150:151], s[70:71] op_sel_hi:[1,0]
	v_pk_mul_f32 v[6:7], v[148:149], s[70:71] op_sel_hi:[1,0]
	v_pk_mul_f32 v[8:9], v[146:147], s[70:71] op_sel_hi:[1,0]
	v_cvt_pk_bf16_f32 v17, v4, v5
	v_cvt_pk_bf16_f32 v18, v2, v3
	v_cvt_pk_bf16_f32 v8, v8, v9
	v_cvt_pk_bf16_f32 v6, v6, v7
	v_cndmask_b32_e64 v2, v16, v6, s[36:37]
	v_cndmask_b32_e64 v3, v14, v18, s[36:37]
	v_cndmask_b32_e64 v4, v15, v8, s[36:37]
	v_cndmask_b32_e64 v5, v13, v17, s[36:37]
	v_mov_b32_dpp v7, v3 quad_perm:[1,0,3,2] row_mask:0xf bank_mask:0xf bound_ctrl:1
	v_mov_b32_dpp v20, v4 quad_perm:[1,0,3,2] row_mask:0xf bank_mask:0xf bound_ctrl:1
	v_mov_b32_dpp v19, v5 quad_perm:[1,0,3,2] row_mask:0xf bank_mask:0xf bound_ctrl:1
	v_mov_b32_dpp v9, v2 quad_perm:[1,0,3,2] row_mask:0xf bank_mask:0xf bound_ctrl:1
	v_cndmask_b32_e64 v5, v9, v16, s[36:37]
	v_cndmask_b32_e64 v3, v7, v14, s[36:37]
	v_cndmask_b32_e64 v4, v20, v15, s[36:37]
	v_cndmask_b32_e64 v2, v19, v13, s[36:37]
	s_lshl_b64 s[68:69], s[0:1], 1
	v_cndmask_b32_e64 v9, v6, v9, s[36:37]
	v_cndmask_b32_e64 v7, v18, v7, s[36:37]
	v_cndmask_b32_e64 v8, v8, v20, s[36:37]
	v_cndmask_b32_e64 v6, v17, v19, s[36:37]
	global_store_dwordx4 v[10:11], v[2:5], off nt
	v_mov_b32_e32 v146, 0
	v_mov_b32_e32 v147, 0
	v_mov_b32_e32 v148, 0
	v_mov_b32_e32 v149, 0
	v_mov_b32_e32 v150, 0
	v_mov_b32_e32 v151, 0
	v_mov_b32_e32 v152, 0
	v_mov_b32_e32 v153, 0
	v_mov_b32_e32 v154, 0
	v_mov_b32_e32 v155, 0
	v_mov_b32_e32 v156, 0
	v_mov_b32_e32 v157, 0
	v_mov_b32_e32 v158, 0
	v_mov_b32_e32 v159, 0
	v_mov_b32_e32 v160, 0
	v_mov_b32_e32 v161, 0
	s_nop 1
	v_lshl_add_u64 v[2:3], v[10:11], 0, s[68:69]
	global_store_dwordx4 v[2:3], v[6:9], off nt
	v_add_u32_e32 v2, 16, v12
	v_ashrrev_i32_e32 v3, 31, v2
	v_mul_lo_u32 v4, s0, v3
	v_mul_lo_u32 v5, s1, v2
	v_mad_u64_u32 v[2:3], s[4:5], s0, v2, 0
	v_add3_u32 v3, v3, v4, v5
	v_lshl_add_u64 v[10:11], v[2:3], 1, v[0:1]
	v_pk_mul_f32 v[2:3], v[144:145], s[70:71] op_sel_hi:[1,0]
	v_pk_mul_f32 v[4:5], v[142:143], s[70:71] op_sel_hi:[1,0]
	v_pk_mul_f32 v[6:7], v[140:141], s[70:71] op_sel_hi:[1,0]
	v_pk_mul_f32 v[8:9], v[138:139], s[70:71] op_sel_hi:[1,0]
	v_cvt_pk_bf16_f32 v13, v4, v5
	v_cvt_pk_bf16_f32 v14, v2, v3
	v_cvt_pk_bf16_f32 v15, v8, v9
	v_cvt_pk_bf16_f32 v16, v6, v7
	v_pk_mul_f32 v[2:3], v[136:137], s[70:71] op_sel_hi:[1,0]
	v_pk_mul_f32 v[4:5], v[134:135], s[70:71] op_sel_hi:[1,0]
	v_pk_mul_f32 v[6:7], v[132:133], s[70:71] op_sel_hi:[1,0]
	v_pk_mul_f32 v[8:9], v[130:131], s[70:71] op_sel_hi:[1,0]
	v_cvt_pk_bf16_f32 v17, v4, v5
	v_cvt_pk_bf16_f32 v18, v2, v3
	v_cvt_pk_bf16_f32 v8, v8, v9
	v_cvt_pk_bf16_f32 v6, v6, v7
	v_cndmask_b32_e64 v2, v16, v6, s[36:37]
	v_cndmask_b32_e64 v3, v14, v18, s[36:37]
	v_cndmask_b32_e64 v4, v15, v8, s[36:37]
	v_cndmask_b32_e64 v5, v13, v17, s[36:37]
	v_mov_b32_dpp v7, v3 quad_perm:[1,0,3,2] row_mask:0xf bank_mask:0xf bound_ctrl:1
	v_mov_b32_dpp v20, v4 quad_perm:[1,0,3,2] row_mask:0xf bank_mask:0xf bound_ctrl:1
	v_mov_b32_dpp v19, v5 quad_perm:[1,0,3,2] row_mask:0xf bank_mask:0xf bound_ctrl:1
	v_mov_b32_dpp v9, v2 quad_perm:[1,0,3,2] row_mask:0xf bank_mask:0xf bound_ctrl:1
	v_cndmask_b32_e64 v5, v9, v16, s[36:37]
	v_cndmask_b32_e64 v3, v7, v14, s[36:37]
	v_cndmask_b32_e64 v4, v20, v15, s[36:37]
	v_cndmask_b32_e64 v2, v19, v13, s[36:37]
	v_cndmask_b32_e64 v9, v6, v9, s[36:37]
	v_cndmask_b32_e64 v7, v18, v7, s[36:37]
	v_cndmask_b32_e64 v8, v8, v20, s[36:37]
	v_cndmask_b32_e64 v6, v17, v19, s[36:37]
	global_store_dwordx4 v[10:11], v[2:5], off nt
	v_mov_b32_e32 v130, 0
	v_mov_b32_e32 v131, 0
	v_mov_b32_e32 v132, 0
	v_mov_b32_e32 v133, 0
	v_mov_b32_e32 v134, 0
	v_mov_b32_e32 v135, 0
	v_mov_b32_e32 v136, 0
	v_mov_b32_e32 v137, 0
	v_mov_b32_e32 v138, 0
	v_mov_b32_e32 v139, 0
	v_mov_b32_e32 v140, 0
	v_mov_b32_e32 v141, 0
	v_mov_b32_e32 v142, 0
	v_mov_b32_e32 v143, 0
	v_mov_b32_e32 v144, 0
	v_mov_b32_e32 v145, 0
	s_nop 1
	v_lshl_add_u64 v[2:3], v[10:11], 0, s[68:69]
	global_store_dwordx4 v[2:3], v[6:9], off nt
	v_add_u32_e32 v2, 32, v12
	v_ashrrev_i32_e32 v3, 31, v2
	v_mul_lo_u32 v4, s0, v3
	v_mul_lo_u32 v5, s1, v2
	v_mad_u64_u32 v[2:3], s[4:5], s0, v2, 0
	v_add3_u32 v3, v3, v4, v5
	v_lshl_add_u64 v[10:11], v[2:3], 1, v[0:1]
	v_pk_mul_f32 v[2:3], v[128:129], s[70:71] op_sel_hi:[1,0]
	v_pk_mul_f32 v[4:5], v[126:127], s[70:71] op_sel_hi:[1,0]
	v_pk_mul_f32 v[6:7], v[124:125], s[70:71] op_sel_hi:[1,0]
	v_pk_mul_f32 v[8:9], v[122:123], s[70:71] op_sel_hi:[1,0]
	v_cvt_pk_bf16_f32 v13, v4, v5
	v_cvt_pk_bf16_f32 v14, v2, v3
	v_cvt_pk_bf16_f32 v15, v8, v9
	v_cvt_pk_bf16_f32 v16, v6, v7
	v_pk_mul_f32 v[2:3], v[120:121], s[70:71] op_sel_hi:[1,0]
	v_pk_mul_f32 v[4:5], v[118:119], s[70:71] op_sel_hi:[1,0]
	v_pk_mul_f32 v[6:7], v[116:117], s[70:71] op_sel_hi:[1,0]
	v_pk_mul_f32 v[8:9], v[114:115], s[70:71] op_sel_hi:[1,0]
	v_cvt_pk_bf16_f32 v17, v4, v5
	v_cvt_pk_bf16_f32 v18, v2, v3
	v_cvt_pk_bf16_f32 v8, v8, v9
	v_cvt_pk_bf16_f32 v6, v6, v7
	v_cndmask_b32_e64 v2, v16, v6, s[36:37]
	v_cndmask_b32_e64 v3, v14, v18, s[36:37]
	v_cndmask_b32_e64 v4, v15, v8, s[36:37]
	v_cndmask_b32_e64 v5, v13, v17, s[36:37]
	v_mov_b32_dpp v7, v3 quad_perm:[1,0,3,2] row_mask:0xf bank_mask:0xf bound_ctrl:1
	v_mov_b32_dpp v20, v4 quad_perm:[1,0,3,2] row_mask:0xf bank_mask:0xf bound_ctrl:1
	v_mov_b32_dpp v19, v5 quad_perm:[1,0,3,2] row_mask:0xf bank_mask:0xf bound_ctrl:1
	v_mov_b32_dpp v9, v2 quad_perm:[1,0,3,2] row_mask:0xf bank_mask:0xf bound_ctrl:1
	v_cndmask_b32_e64 v5, v9, v16, s[36:37]
	v_cndmask_b32_e64 v3, v7, v14, s[36:37]
	v_cndmask_b32_e64 v4, v20, v15, s[36:37]
	v_cndmask_b32_e64 v2, v19, v13, s[36:37]
	v_cndmask_b32_e64 v9, v6, v9, s[36:37]
	v_cndmask_b32_e64 v7, v18, v7, s[36:37]
	v_cndmask_b32_e64 v8, v8, v20, s[36:37]
	v_cndmask_b32_e64 v6, v17, v19, s[36:37]
	global_store_dwordx4 v[10:11], v[2:5], off nt
	v_mov_b32_e32 v114, 0
	v_mov_b32_e32 v115, 0
	v_mov_b32_e32 v116, 0
	v_mov_b32_e32 v117, 0
	v_mov_b32_e32 v118, 0
	v_mov_b32_e32 v119, 0
	v_mov_b32_e32 v120, 0
	v_mov_b32_e32 v121, 0
	v_mov_b32_e32 v122, 0
	v_mov_b32_e32 v123, 0
	v_mov_b32_e32 v124, 0
	v_mov_b32_e32 v125, 0
	v_mov_b32_e32 v126, 0
	v_mov_b32_e32 v127, 0
	v_mov_b32_e32 v128, 0
	v_mov_b32_e32 v129, 0
	s_nop 1
	v_lshl_add_u64 v[2:3], v[10:11], 0, s[68:69]
	global_store_dwordx4 v[2:3], v[6:9], off nt
	v_add_u32_e32 v2, 48, v12
	v_ashrrev_i32_e32 v3, 31, v2
	v_mul_lo_u32 v4, s0, v3
	v_mul_lo_u32 v5, s1, v2
	v_mad_u64_u32 v[2:3], s[4:5], s0, v2, 0
	v_add3_u32 v3, v3, v4, v5
	v_lshl_add_u64 v[10:11], v[2:3], 1, v[0:1]
	v_pk_mul_f32 v[2:3], v[112:113], s[70:71] op_sel_hi:[1,0]
	v_pk_mul_f32 v[4:5], v[110:111], s[70:71] op_sel_hi:[1,0]
	v_pk_mul_f32 v[6:7], v[108:109], s[70:71] op_sel_hi:[1,0]
	v_pk_mul_f32 v[8:9], v[106:107], s[70:71] op_sel_hi:[1,0]
	v_cvt_pk_bf16_f32 v13, v4, v5
	v_cvt_pk_bf16_f32 v14, v2, v3
	v_cvt_pk_bf16_f32 v15, v8, v9
	v_cvt_pk_bf16_f32 v16, v6, v7
	v_pk_mul_f32 v[2:3], v[104:105], s[70:71] op_sel_hi:[1,0]
	v_pk_mul_f32 v[4:5], v[102:103], s[70:71] op_sel_hi:[1,0]
	v_pk_mul_f32 v[6:7], v[100:101], s[70:71] op_sel_hi:[1,0]
	v_pk_mul_f32 v[8:9], v[98:99], s[70:71] op_sel_hi:[1,0]
	v_cvt_pk_bf16_f32 v17, v4, v5
	v_cvt_pk_bf16_f32 v18, v2, v3
	v_cvt_pk_bf16_f32 v8, v8, v9
	v_cvt_pk_bf16_f32 v6, v6, v7
	v_cndmask_b32_e64 v2, v16, v6, s[36:37]
	v_cndmask_b32_e64 v3, v14, v18, s[36:37]
	v_cndmask_b32_e64 v4, v15, v8, s[36:37]
	v_cndmask_b32_e64 v5, v13, v17, s[36:37]
	v_mov_b32_dpp v7, v3 quad_perm:[1,0,3,2] row_mask:0xf bank_mask:0xf bound_ctrl:1
	v_mov_b32_dpp v20, v4 quad_perm:[1,0,3,2] row_mask:0xf bank_mask:0xf bound_ctrl:1
	v_mov_b32_dpp v19, v5 quad_perm:[1,0,3,2] row_mask:0xf bank_mask:0xf bound_ctrl:1
	v_mov_b32_dpp v9, v2 quad_perm:[1,0,3,2] row_mask:0xf bank_mask:0xf bound_ctrl:1
	v_cndmask_b32_e64 v5, v9, v16, s[36:37]
	v_cndmask_b32_e64 v3, v7, v14, s[36:37]
	v_cndmask_b32_e64 v4, v20, v15, s[36:37]
	v_cndmask_b32_e64 v2, v19, v13, s[36:37]
	v_cndmask_b32_e64 v9, v6, v9, s[36:37]
	v_cndmask_b32_e64 v7, v18, v7, s[36:37]
	v_cndmask_b32_e64 v8, v8, v20, s[36:37]
	v_cndmask_b32_e64 v6, v17, v19, s[36:37]
	global_store_dwordx4 v[10:11], v[2:5], off nt
	v_mov_b32_e32 v98, 0
	v_mov_b32_e32 v99, 0
	v_mov_b32_e32 v100, 0
	v_mov_b32_e32 v101, 0
	v_mov_b32_e32 v102, 0
	v_mov_b32_e32 v103, 0
	v_mov_b32_e32 v104, 0
	v_mov_b32_e32 v105, 0
	v_mov_b32_e32 v106, 0
	v_mov_b32_e32 v107, 0
	v_mov_b32_e32 v108, 0
	v_mov_b32_e32 v109, 0
	v_mov_b32_e32 v110, 0
	v_mov_b32_e32 v111, 0
	v_mov_b32_e32 v112, 0
	v_mov_b32_e32 v113, 0
	s_nop 1
	v_lshl_add_u64 v[2:3], v[10:11], 0, s[68:69]
	global_store_dwordx4 v[2:3], v[6:9], off nt
	v_add_u32_e32 v2, 0x80, v12
	v_ashrrev_i32_e32 v3, 31, v2
	v_mul_lo_u32 v4, s0, v3
	v_mul_lo_u32 v5, s1, v2
	v_mad_u64_u32 v[2:3], s[4:5], s0, v2, 0
	v_add3_u32 v3, v3, v4, v5
	v_lshl_add_u64 v[10:11], v[2:3], 1, v[0:1]
	v_pk_mul_f32 v[2:3], v[96:97], s[70:71] op_sel_hi:[1,0]
	v_pk_mul_f32 v[4:5], v[94:95], s[70:71] op_sel_hi:[1,0]
	v_pk_mul_f32 v[6:7], v[92:93], s[70:71] op_sel_hi:[1,0]
	v_pk_mul_f32 v[8:9], v[90:91], s[70:71] op_sel_hi:[1,0]
	v_cvt_pk_bf16_f32 v13, v4, v5
	v_cvt_pk_bf16_f32 v14, v2, v3
	v_cvt_pk_bf16_f32 v15, v8, v9
	v_cvt_pk_bf16_f32 v16, v6, v7
	v_pk_mul_f32 v[2:3], v[88:89], s[70:71] op_sel_hi:[1,0]
	v_pk_mul_f32 v[4:5], v[86:87], s[70:71] op_sel_hi:[1,0]
	v_pk_mul_f32 v[6:7], v[84:85], s[70:71] op_sel_hi:[1,0]
	v_pk_mul_f32 v[8:9], v[82:83], s[70:71] op_sel_hi:[1,0]
	v_cvt_pk_bf16_f32 v17, v4, v5
	v_cvt_pk_bf16_f32 v18, v2, v3
	v_cvt_pk_bf16_f32 v8, v8, v9
	v_cvt_pk_bf16_f32 v6, v6, v7
	v_cndmask_b32_e64 v2, v16, v6, s[36:37]
	v_cndmask_b32_e64 v3, v14, v18, s[36:37]
	v_cndmask_b32_e64 v4, v15, v8, s[36:37]
	v_cndmask_b32_e64 v5, v13, v17, s[36:37]
	v_mov_b32_dpp v7, v3 quad_perm:[1,0,3,2] row_mask:0xf bank_mask:0xf bound_ctrl:1
	v_mov_b32_dpp v20, v4 quad_perm:[1,0,3,2] row_mask:0xf bank_mask:0xf bound_ctrl:1
	v_mov_b32_dpp v19, v5 quad_perm:[1,0,3,2] row_mask:0xf bank_mask:0xf bound_ctrl:1
	v_mov_b32_dpp v9, v2 quad_perm:[1,0,3,2] row_mask:0xf bank_mask:0xf bound_ctrl:1
	v_cndmask_b32_e64 v5, v9, v16, s[36:37]
	v_cndmask_b32_e64 v3, v7, v14, s[36:37]
	v_cndmask_b32_e64 v4, v20, v15, s[36:37]
	v_cndmask_b32_e64 v2, v19, v13, s[36:37]
	v_cndmask_b32_e64 v9, v6, v9, s[36:37]
	v_cndmask_b32_e64 v7, v18, v7, s[36:37]
	v_cndmask_b32_e64 v8, v8, v20, s[36:37]
	v_cndmask_b32_e64 v6, v17, v19, s[36:37]
	global_store_dwordx4 v[10:11], v[2:5], off nt
	v_mov_b32_e32 v82, 0
	v_mov_b32_e32 v83, 0
	v_mov_b32_e32 v84, 0
	v_mov_b32_e32 v85, 0
	v_mov_b32_e32 v86, 0
	v_mov_b32_e32 v87, 0
	v_mov_b32_e32 v88, 0
	v_mov_b32_e32 v89, 0
	v_mov_b32_e32 v90, 0
	v_mov_b32_e32 v91, 0
	v_mov_b32_e32 v92, 0
	v_mov_b32_e32 v93, 0
	v_mov_b32_e32 v94, 0
	v_mov_b32_e32 v95, 0
	v_mov_b32_e32 v96, 0
	v_mov_b32_e32 v97, 0
	s_nop 1
	v_lshl_add_u64 v[2:3], v[10:11], 0, s[68:69]
	global_store_dwordx4 v[2:3], v[6:9], off nt
	v_add_u32_e32 v2, 0x90, v12
	v_ashrrev_i32_e32 v3, 31, v2
	v_mul_lo_u32 v4, s0, v3
	v_mul_lo_u32 v5, s1, v2
	v_mad_u64_u32 v[2:3], s[4:5], s0, v2, 0
	v_add3_u32 v3, v3, v4, v5
	v_lshl_add_u64 v[10:11], v[2:3], 1, v[0:1]
	v_pk_mul_f32 v[2:3], v[72:73], s[70:71] op_sel_hi:[1,0]
	v_pk_mul_f32 v[4:5], v[70:71], s[70:71] op_sel_hi:[1,0]
	v_pk_mul_f32 v[6:7], v[68:69], s[70:71] op_sel_hi:[1,0]
	v_pk_mul_f32 v[8:9], v[66:67], s[70:71] op_sel_hi:[1,0]
	v_cvt_pk_bf16_f32 v13, v4, v5
	v_cvt_pk_bf16_f32 v14, v2, v3
	v_cvt_pk_bf16_f32 v15, v8, v9
	v_cvt_pk_bf16_f32 v16, v6, v7
	v_pk_mul_f32 v[2:3], v[64:65], s[70:71] op_sel_hi:[1,0]
	v_pk_mul_f32 v[4:5], v[62:63], s[70:71] op_sel_hi:[1,0]
	v_pk_mul_f32 v[6:7], v[52:53], s[70:71] op_sel_hi:[1,0]
	v_pk_mul_f32 v[8:9], v[50:51], s[70:71] op_sel_hi:[1,0]
	v_cvt_pk_bf16_f32 v17, v4, v5
	v_cvt_pk_bf16_f32 v18, v2, v3
	v_cvt_pk_bf16_f32 v8, v8, v9
	v_cvt_pk_bf16_f32 v6, v6, v7
	v_cndmask_b32_e64 v2, v16, v6, s[36:37]
	v_cndmask_b32_e64 v3, v14, v18, s[36:37]
	v_cndmask_b32_e64 v4, v15, v8, s[36:37]
	v_cndmask_b32_e64 v5, v13, v17, s[36:37]
	v_mov_b32_dpp v7, v3 quad_perm:[1,0,3,2] row_mask:0xf bank_mask:0xf bound_ctrl:1
	v_mov_b32_dpp v20, v4 quad_perm:[1,0,3,2] row_mask:0xf bank_mask:0xf bound_ctrl:1
	v_mov_b32_dpp v19, v5 quad_perm:[1,0,3,2] row_mask:0xf bank_mask:0xf bound_ctrl:1
	v_mov_b32_dpp v9, v2 quad_perm:[1,0,3,2] row_mask:0xf bank_mask:0xf bound_ctrl:1
	v_cndmask_b32_e64 v5, v9, v16, s[36:37]
	v_cndmask_b32_e64 v3, v7, v14, s[36:37]
	v_cndmask_b32_e64 v4, v20, v15, s[36:37]
	v_cndmask_b32_e64 v2, v19, v13, s[36:37]
	v_cndmask_b32_e64 v9, v6, v9, s[36:37]
	v_cndmask_b32_e64 v7, v18, v7, s[36:37]
	v_cndmask_b32_e64 v8, v8, v20, s[36:37]
	v_cndmask_b32_e64 v6, v17, v19, s[36:37]
	global_store_dwordx4 v[10:11], v[2:5], off nt
	v_mov_b32_e32 v50, 0
	v_mov_b32_e32 v51, 0
	v_mov_b32_e32 v52, 0
	v_mov_b32_e32 v53, 0
	v_mov_b32_e32 v62, 0
	v_mov_b32_e32 v63, 0
	v_mov_b32_e32 v64, 0
	v_mov_b32_e32 v65, 0
	v_mov_b32_e32 v66, 0
	v_mov_b32_e32 v67, 0
	v_mov_b32_e32 v68, 0
	v_mov_b32_e32 v69, 0
	v_mov_b32_e32 v70, 0
	v_mov_b32_e32 v71, 0
	v_mov_b32_e32 v72, 0
	v_mov_b32_e32 v73, 0
	s_nop 1
	v_lshl_add_u64 v[2:3], v[10:11], 0, s[68:69]
	global_store_dwordx4 v[2:3], v[6:9], off nt
	v_add_u32_e32 v2, 0xa0, v12
	v_ashrrev_i32_e32 v3, 31, v2
	v_mul_lo_u32 v4, s0, v3
	v_mul_lo_u32 v5, s1, v2
	v_mad_u64_u32 v[2:3], s[4:5], s0, v2, 0
	v_add3_u32 v3, v3, v4, v5
	v_lshl_add_u64 v[10:11], v[2:3], 1, v[0:1]
	v_pk_mul_f32 v[2:3], v[46:47], s[70:71] op_sel_hi:[1,0]
	v_pk_mul_f32 v[4:5], v[44:45], s[70:71] op_sel_hi:[1,0]
	v_pk_mul_f32 v[6:7], v[42:43], s[70:71] op_sel_hi:[1,0]
	v_pk_mul_f32 v[8:9], v[40:41], s[70:71] op_sel_hi:[1,0]
	v_cvt_pk_bf16_f32 v13, v4, v5
	v_cvt_pk_bf16_f32 v14, v2, v3
	v_cvt_pk_bf16_f32 v15, v8, v9
	v_cvt_pk_bf16_f32 v16, v6, v7
	v_pk_mul_f32 v[2:3], v[80:81], s[70:71] op_sel_hi:[1,0]
	v_pk_mul_f32 v[4:5], v[78:79], s[70:71] op_sel_hi:[1,0]
	v_pk_mul_f32 v[6:7], v[76:77], s[70:71] op_sel_hi:[1,0]
	v_pk_mul_f32 v[8:9], v[74:75], s[70:71] op_sel_hi:[1,0]
	v_cvt_pk_bf16_f32 v17, v4, v5
	v_cvt_pk_bf16_f32 v18, v2, v3
	v_cvt_pk_bf16_f32 v8, v8, v9
	v_cvt_pk_bf16_f32 v6, v6, v7
	v_cndmask_b32_e64 v2, v16, v6, s[36:37]
	v_cndmask_b32_e64 v3, v14, v18, s[36:37]
	v_cndmask_b32_e64 v4, v15, v8, s[36:37]
	v_cndmask_b32_e64 v5, v13, v17, s[36:37]
	v_mov_b32_dpp v7, v3 quad_perm:[1,0,3,2] row_mask:0xf bank_mask:0xf bound_ctrl:1
	v_mov_b32_dpp v20, v4 quad_perm:[1,0,3,2] row_mask:0xf bank_mask:0xf bound_ctrl:1
	v_mov_b32_dpp v19, v5 quad_perm:[1,0,3,2] row_mask:0xf bank_mask:0xf bound_ctrl:1
	v_mov_b32_dpp v9, v2 quad_perm:[1,0,3,2] row_mask:0xf bank_mask:0xf bound_ctrl:1
	v_cndmask_b32_e64 v5, v9, v16, s[36:37]
	v_cndmask_b32_e64 v3, v7, v14, s[36:37]
	v_cndmask_b32_e64 v4, v20, v15, s[36:37]
	v_cndmask_b32_e64 v2, v19, v13, s[36:37]
	v_cndmask_b32_e64 v9, v6, v9, s[36:37]
	v_cndmask_b32_e64 v7, v18, v7, s[36:37]
	v_cndmask_b32_e64 v8, v8, v20, s[36:37]
	v_cndmask_b32_e64 v6, v17, v19, s[36:37]
	global_store_dwordx4 v[10:11], v[2:5], off nt
	v_mov_b32_e32 v40, 0
	v_mov_b32_e32 v41, 0
	v_mov_b32_e32 v42, 0
	v_mov_b32_e32 v43, 0
	v_mov_b32_e32 v44, 0
	v_mov_b32_e32 v45, 0
	v_mov_b32_e32 v46, 0
	v_mov_b32_e32 v47, 0
	v_mov_b32_e32 v74, 0
	v_mov_b32_e32 v75, 0
	v_mov_b32_e32 v76, 0
	v_mov_b32_e32 v77, 0
	v_mov_b32_e32 v78, 0
	v_mov_b32_e32 v79, 0
	v_mov_b32_e32 v80, 0
	v_mov_b32_e32 v81, 0
	s_nop 1
	v_lshl_add_u64 v[2:3], v[10:11], 0, s[68:69]
	global_store_dwordx4 v[2:3], v[6:9], off nt
	v_add_u32_e32 v2, 0xb0, v12
	v_ashrrev_i32_e32 v3, 31, v2
	v_mul_lo_u32 v4, s0, v3
	v_mul_lo_u32 v5, s1, v2
	v_mad_u64_u32 v[2:3], s[0:1], s0, v2, 0
	v_add3_u32 v3, v3, v4, v5
	v_lshl_add_u64 v[8:9], v[2:3], 1, v[0:1]
	v_pk_mul_f32 v[0:1], v[38:39], s[70:71] op_sel_hi:[1,0]
	v_pk_mul_f32 v[2:3], v[36:37], s[70:71] op_sel_hi:[1,0]
	v_pk_mul_f32 v[4:5], v[34:35], s[70:71] op_sel_hi:[1,0]
	v_pk_mul_f32 v[6:7], v[32:33], s[70:71] op_sel_hi:[1,0]
	v_cvt_pk_bf16_f32 v10, v2, v3
	v_cvt_pk_bf16_f32 v11, v0, v1
	v_cvt_pk_bf16_f32 v12, v6, v7
	v_cvt_pk_bf16_f32 v13, v4, v5
	v_pk_mul_f32 v[0:1], v[60:61], s[70:71] op_sel_hi:[1,0]
	v_pk_mul_f32 v[2:3], v[58:59], s[70:71] op_sel_hi:[1,0]
	v_pk_mul_f32 v[4:5], v[56:57], s[70:71] op_sel_hi:[1,0]
	v_pk_mul_f32 v[6:7], v[54:55], s[70:71] op_sel_hi:[1,0]
	v_cvt_pk_bf16_f32 v14, v2, v3
	v_cvt_pk_bf16_f32 v15, v0, v1
	v_cvt_pk_bf16_f32 v6, v6, v7
	v_cvt_pk_bf16_f32 v4, v4, v5
	v_cndmask_b32_e64 v0, v13, v4, s[36:37]
	v_cndmask_b32_e64 v1, v11, v15, s[36:37]
	v_cndmask_b32_e64 v2, v12, v6, s[36:37]
	v_cndmask_b32_e64 v3, v10, v14, s[36:37]
	v_mov_b32_dpp v5, v1 quad_perm:[1,0,3,2] row_mask:0xf bank_mask:0xf bound_ctrl:1
	v_mov_b32_dpp v17, v2 quad_perm:[1,0,3,2] row_mask:0xf bank_mask:0xf bound_ctrl:1
	v_mov_b32_dpp v16, v3 quad_perm:[1,0,3,2] row_mask:0xf bank_mask:0xf bound_ctrl:1
	v_mov_b32_dpp v7, v0 quad_perm:[1,0,3,2] row_mask:0xf bank_mask:0xf bound_ctrl:1
	v_cndmask_b32_e64 v3, v7, v13, s[36:37]
	v_cndmask_b32_e64 v1, v5, v11, s[36:37]
	v_cndmask_b32_e64 v2, v17, v12, s[36:37]
	v_cndmask_b32_e64 v0, v16, v10, s[36:37]
	v_cndmask_b32_e64 v7, v4, v7, s[36:37]
	v_cndmask_b32_e64 v5, v15, v5, s[36:37]
	v_cndmask_b32_e64 v6, v6, v17, s[36:37]
	v_cndmask_b32_e64 v4, v14, v16, s[36:37]
	global_store_dwordx4 v[8:9], v[0:3], off nt
	v_mov_b32_e32 v32, 0
	v_mov_b32_e32 v33, 0
	v_mov_b32_e32 v34, 0
	v_mov_b32_e32 v35, 0
	v_mov_b32_e32 v36, 0
	v_mov_b32_e32 v37, 0
	v_mov_b32_e32 v38, 0
	v_mov_b32_e32 v39, 0
	v_mov_b32_e32 v54, 0
	v_mov_b32_e32 v55, 0
	v_mov_b32_e32 v56, 0
	v_mov_b32_e32 v57, 0
	v_mov_b32_e32 v58, 0
	v_mov_b32_e32 v59, 0
	v_mov_b32_e32 v60, 0
	v_mov_b32_e32 v61, 0
	s_nop 1
	v_lshl_add_u64 v[0:1], v[8:9], 0, s[68:69]
	global_store_dwordx4 v[0:1], v[4:7], off nt
	s_andn2_b64 vcc, exec, s[38:39]
	s_mov_b64 s[0:1], -1
	s_cbranch_vccnz .LBB0_134

.LBB0_513:
	v_lshrrev_b32_e32 v15, 1, v8
	s_add_u32 s44, s20, 0x3fd00000
	v_and_b32_e32 v15, 24, v15
	s_addc_u32 s45, s19, 0
	v_lshlrev_b32_e32 v16, 1, v15
	v_lshlrev_b32_e32 v17, 6, v8
	s_movk_i32 s19, 0x3c0
	v_and_or_b32 v16, v17, s19, v16
	v_lshlrev_b32_e32 v17, 2, v8
	s_sext_i32_i8 s21, s22
	s_and_b32 s22, s33, 3
	s_lshl_b32 s19, s31, 13
	v_and_b32_e32 v17, 32, v17
	v_bitop3_b32 v18, v16, s19, v17 bitop3:0xde
	s_lshl_b32 s19, s22, 12
	s_add_i32 m0, s13, 0x18000
	v_lshl_add_u64 v[6:7], v[6:7], 0, s[88:89]
	v_bitop3_b32 v196, v16, s19, v17 bitop3:0xde
	s_waitcnt vmcnt(2)
	s_barrier
	global_load_lds_dwordx4 v[6:7], off
	v_lshl_add_u64 v[4:5], v[4:5], 0, s[88:89]
	s_add_i32 m0, s13, 0x1a000
	s_add_i32 s19, s13, 0x8000
	s_add_i32 s20, s13, 0xa000
	global_load_lds_dwordx4 v[4:5], off
	v_lshl_add_u64 v[0:1], v[0:1], 0, s[88:89]
	s_mov_b32 m0, s19
	s_add_u32 s36, s0, 0x8080
	global_load_lds_dwordx4 v[0:1], off
	v_lshl_add_u64 v[0:1], v[2:3], 0, s[88:89]
	s_mov_b32 m0, s20
	s_addc_u32 s37, s1, 0
	global_load_lds_dwordx4 v[0:1], off
	s_add_i32 m0, s13, 0x1c000
	v_lshl_add_u64 v[0:1], s[36:37], 0, v[48:49]
	global_load_lds_dwordx4 v[0:1], off
	v_lshl_add_u64 v[0:1], s[36:37], 0, v[174:175]
	s_add_i32 m0, s13, 0x1e000
	s_cmpk_lt_u32 s30, 0x100
	global_load_lds_dwordx4 v[0:1], off
	v_and_b32_e32 v0, 1, v8
	v_and_b32_e32 v1, 14, v8
	v_lshl_or_b32 v197, s31, 6, v1
	v_lshlrev_b32_e32 v1, 5, v0
	v_cmp_eq_u32_e64 s[38:39], 0, v0
	v_lshlrev_b32_e32 v0, 13, v9
	s_cselect_b64 s[46:47], -1, 0
	s_lshl_b32 s30, s22, 6
	v_and_b32_e32 v0, 0xffffc000, v0
	v_or3_b32 v198, s30, v1, v15
	v_lshl_add_u32 v0, v10, 10, v0
	v_and_b32_e32 v1, 1, v9
	v_lshl_or_b32 v0, v1, 6, v0
	v_lshl_add_u32 v176, v11, 1, v0
	v_lshlrev_b32_e32 v0, 13, v12
	v_and_b32_e32 v0, 0xffffc000, v0
	s_waitcnt vmcnt(6)
	v_lshl_add_u32 v0, v13, 10, v0
	v_and_b32_e32 v1, 1, v12
	v_lshl_or_b32 v0, v1, 6, v0
	s_mov_b32 s22, 0
	v_mov_b32_e32 v177, v49
	v_lshl_add_u32 v178, v14, 1, v0
	v_mov_b32_e32 v179, v49
	v_add_u32_e32 v199, 0, v18
	s_barrier
	v_mov_b32_e32 v32, 0
	v_mov_b32_e32 v33, 0
	v_mov_b32_e32 v34, 0
	v_mov_b32_e32 v35, 0
	v_mov_b32_e32 v36, 0
	v_mov_b32_e32 v37, 0
	v_mov_b32_e32 v38, 0
	v_mov_b32_e32 v39, 0
	v_mov_b32_e32 v40, 0
	v_mov_b32_e32 v41, 0
	v_mov_b32_e32 v42, 0
	v_mov_b32_e32 v43, 0
	v_mov_b32_e32 v44, 0
	v_mov_b32_e32 v45, 0
	v_mov_b32_e32 v46, 0
	v_mov_b32_e32 v47, 0
	v_mov_b32_e32 v50, 0
	v_mov_b32_e32 v51, 0
	v_mov_b32_e32 v52, 0
	v_mov_b32_e32 v53, 0
	v_mov_b32_e32 v54, 0
	v_mov_b32_e32 v55, 0
	v_mov_b32_e32 v56, 0
	v_mov_b32_e32 v57, 0
	v_mov_b32_e32 v58, 0
	v_mov_b32_e32 v59, 0
	v_mov_b32_e32 v60, 0
	v_mov_b32_e32 v61, 0
	v_mov_b32_e32 v62, 0
	v_mov_b32_e32 v63, 0
	v_mov_b32_e32 v64, 0
	v_mov_b32_e32 v65, 0
	v_mov_b32_e32 v66, 0
	v_mov_b32_e32 v67, 0
	v_mov_b32_e32 v68, 0
	v_mov_b32_e32 v69, 0
	v_mov_b32_e32 v70, 0
	v_mov_b32_e32 v71, 0
	v_mov_b32_e32 v72, 0
	v_mov_b32_e32 v73, 0
	v_mov_b32_e32 v74, 0
	v_mov_b32_e32 v75, 0
	v_mov_b32_e32 v76, 0
	v_mov_b32_e32 v77, 0
	v_mov_b32_e32 v78, 0
	v_mov_b32_e32 v79, 0
	v_mov_b32_e32 v80, 0
	v_mov_b32_e32 v81, 0
	v_mov_b32_e32 v82, 0
	v_mov_b32_e32 v83, 0
	v_mov_b32_e32 v84, 0
	v_mov_b32_e32 v85, 0
	v_mov_b32_e32 v86, 0
	v_mov_b32_e32 v87, 0
	v_mov_b32_e32 v88, 0
	v_mov_b32_e32 v89, 0
	v_mov_b32_e32 v90, 0
	v_mov_b32_e32 v91, 0
	v_mov_b32_e32 v92, 0
	v_mov_b32_e32 v93, 0
	v_mov_b32_e32 v94, 0
	v_mov_b32_e32 v95, 0
	v_mov_b32_e32 v96, 0
	v_mov_b32_e32 v97, 0
	v_mov_b32_e32 v98, 0
	v_mov_b32_e32 v99, 0
	v_mov_b32_e32 v100, 0
	v_mov_b32_e32 v101, 0
	v_mov_b32_e32 v102, 0
	v_mov_b32_e32 v103, 0
	v_mov_b32_e32 v104, 0
	v_mov_b32_e32 v105, 0
	v_mov_b32_e32 v106, 0
	v_mov_b32_e32 v107, 0
	v_mov_b32_e32 v108, 0
	v_mov_b32_e32 v109, 0
	v_mov_b32_e32 v110, 0
	v_mov_b32_e32 v111, 0
	v_mov_b32_e32 v112, 0
	v_mov_b32_e32 v113, 0
	v_mov_b32_e32 v114, 0
	v_mov_b32_e32 v115, 0
	v_mov_b32_e32 v116, 0
	v_mov_b32_e32 v117, 0
	v_mov_b32_e32 v118, 0
	v_mov_b32_e32 v119, 0
	v_mov_b32_e32 v120, 0
	v_mov_b32_e32 v121, 0
	v_mov_b32_e32 v122, 0
	v_mov_b32_e32 v123, 0
	v_mov_b32_e32 v124, 0
	v_mov_b32_e32 v125, 0
	v_mov_b32_e32 v126, 0
	v_mov_b32_e32 v127, 0
	v_mov_b32_e32 v128, 0
	v_mov_b32_e32 v129, 0
	v_mov_b32_e32 v130, 0
	v_mov_b32_e32 v131, 0
	v_mov_b32_e32 v132, 0
	v_mov_b32_e32 v133, 0
	v_mov_b32_e32 v134, 0
	v_mov_b32_e32 v135, 0
	v_mov_b32_e32 v136, 0
	v_mov_b32_e32 v137, 0
	v_mov_b32_e32 v138, 0
	v_mov_b32_e32 v139, 0
	v_mov_b32_e32 v140, 0
	v_mov_b32_e32 v141, 0
	v_mov_b32_e32 v142, 0
	v_mov_b32_e32 v143, 0
	v_mov_b32_e32 v144, 0
	v_mov_b32_e32 v145, 0
	v_mov_b32_e32 v146, 0
	v_mov_b32_e32 v147, 0
	v_mov_b32_e32 v148, 0
	v_mov_b32_e32 v149, 0
	v_mov_b32_e32 v150, 0
	v_mov_b32_e32 v151, 0
	v_mov_b32_e32 v152, 0
	v_mov_b32_e32 v153, 0
	v_mov_b32_e32 v154, 0
	v_mov_b32_e32 v155, 0
	v_mov_b32_e32 v156, 0
	v_mov_b32_e32 v157, 0
	v_mov_b32_e32 v158, 0
	v_mov_b32_e32 v159, 0
	v_mov_b32_e32 v160, 0
	v_mov_b32_e32 v161, 0
	s_branch .LBB0_516

.LBB0_522:
	s_ashr_i32 s49, s48, 31
	s_lshl_b64 s[30:31], s[48:49], 18
	s_add_u32 s52, s7, s30
	s_addc_u32 s53, s8, s31
	s_and_b64 s[30:31], s[40:41], exec
	s_cselect_b32 s30, s53, s5
	s_cselect_b32 s31, s52, s4
	s_ashr_i32 s51, s50, 31
	s_lshl_b64 s[36:37], s[50:51], 18
	s_add_u32 s54, s9, s36
	s_addc_u32 s55, s10, s37
	s_and_b64 s[36:37], s[40:41], exec
	s_cselect_b32 s33, s55, s1
	s_cselect_b32 s49, s54, s0
	s_add_u32 s58, s4, 0x20080
	s_addc_u32 s59, s5, 0
	s_add_u32 s4, s0, 0x100
	s_addc_u32 s5, s1, 0
	s_mov_b32 s51, -2

.LBB0_526:
	v_lshl_or_b32 v2, s21, 8, v198
	v_lshl_add_u32 v0, s56, 8, v197
	v_ashrrev_i32_e32 v3, 31, v2
	v_lshlrev_b64 v[180:181], 1, v[2:3]
	v_ashrrev_i32_e32 v1, 31, v0
	v_lshl_add_u64 v[2:3], s[44:45], 0, v[180:181]
	v_lshlrev_b64 v[224:225], 11, v[0:1]
	s_nop 15
	s_nop 15
	v_lshl_add_u64 v[4:5], v[2:3], 0, v[224:225]
	global_load_dwordx4 v[200:203], v[4:5], off
	global_load_dwordx4 v[204:207], v[4:5], off offset:2048
	v_or_b32_e32 v4, 16, v0
	v_ashrrev_i32_e32 v5, 31, v4
	v_lshlrev_b64 v[194:195], 11, v[4:5]
	v_lshl_add_u64 v[4:5], v[2:3], 0, v[194:195]
	global_load_dwordx4 v[208:211], v[4:5], off
	global_load_dwordx4 v[212:215], v[4:5], off offset:2048
	s_mov_b64 s[0:1], 0x40000
	v_lshl_add_u64 v[188:189], v[224:225], 0, s[0:1]
	s_mov_b64 s[0:1], 0x48000
	v_or_b32_e32 v4, 32, v0
	v_or_b32_e32 v0, 48, v0
	v_lshl_add_u64 v[186:187], v[224:225], 0, s[0:1]
	s_mov_b64 s[0:1], 0x50000
	v_ashrrev_i32_e32 v5, 31, v4
	v_ashrrev_i32_e32 v1, 31, v0
	v_lshl_add_u64 v[184:185], v[224:225], 0, s[0:1]
	s_mov_b64 s[0:1], 0x58000
	v_lshlrev_b64 v[192:193], 11, v[4:5]
	v_lshlrev_b64 v[190:191], 11, v[0:1]
	v_lshl_add_u64 v[182:183], v[224:225], 0, s[0:1]
	v_lshl_add_u64 v[0:1], v[2:3], 0, v[192:193]
	v_lshl_add_u64 v[4:5], v[2:3], 0, v[190:191]
	v_lshl_add_u64 v[6:7], v[2:3], 0, v[188:189]
	v_lshl_add_u64 v[8:9], v[2:3], 0, v[186:187]
	v_lshl_add_u64 v[10:11], v[2:3], 0, v[184:185]
	v_lshl_add_u64 v[2:3], v[2:3], 0, v[182:183]
	global_load_dwordx4 v[216:219], v[0:1], off
	global_load_dwordx4 v[220:223], v[0:1], off offset:2048
	global_load_dwordx4 v[166:169], v[4:5], off
	global_load_dwordx4 v[162:165], v[4:5], off offset:2048
	global_load_dwordx4 v[28:31], v[6:7], off
	global_load_dwordx4 v[24:27], v[6:7], off offset:2048
	global_load_dwordx4 v[20:23], v[8:9], off
	global_load_dwordx4 v[16:19], v[8:9], off offset:2048
	global_load_dwordx4 v[12:15], v[10:11], off
	s_nop 0
	global_load_dwordx4 v[8:11], v[10:11], off offset:2048
	s_nop 0
	global_load_dwordx4 v[4:7], v[2:3], off
	s_nop 0
	global_load_dwordx4 v[0:3], v[2:3], off offset:2048
	s_andn2_b64 vcc, exec, s[40:41]
	s_mov_b64 s[0:1], -1
	s_waitcnt vmcnt(0)
	v_cndmask_b32_e64 v226, v203, v207, s[38:39]
	v_cndmask_b32_e64 v227, v202, v206, s[38:39]
	v_cndmask_b32_e64 v234, v201, v205, s[38:39]
	v_cndmask_b32_e64 v235, v200, v204, s[38:39]
	v_mov_b32_dpp v227, v227 quad_perm:[1,0,3,2] row_mask:0xf bank_mask:0xf bound_ctrl:1
	v_mov_b32_dpp v234, v234 quad_perm:[1,0,3,2] row_mask:0xf bank_mask:0xf bound_ctrl:1
	v_mov_b32_dpp v235, v235 quad_perm:[1,0,3,2] row_mask:0xf bank_mask:0xf bound_ctrl:1
	v_mov_b32_dpp v226, v226 quad_perm:[1,0,3,2] row_mask:0xf bank_mask:0xf bound_ctrl:1
	v_cndmask_b32_e64 v240, v226, v203, s[38:39]
	v_cndmask_b32_e64 v241, v227, v202, s[38:39]
	v_cndmask_b32_e64 v243, v207, v226, s[38:39]
	v_cndmask_b32_e64 v242, v206, v227, s[38:39]
	v_cndmask_b32_e64 v247, v205, v234, s[38:39]
	v_cndmask_b32_e64 v227, v204, v235, s[38:39]
	v_cndmask_b32_e64 v203, v234, v201, s[38:39]
	v_cndmask_b32_e64 v201, v235, v200, s[38:39]
	v_lshlrev_b32_e32 v204, 16, v241
	v_and_b32_e32 v205, 0xffff0000, v241
	v_lshlrev_b32_e32 v206, 16, v240
	v_and_b32_e32 v207, 0xffff0000, v240
	v_lshlrev_b32_e32 v226, 16, v227
	v_and_b32_e32 v227, 0xffff0000, v227
	v_lshlrev_b32_e32 v234, 16, v247
	v_and_b32_e32 v235, 0xffff0000, v247
	v_lshlrev_b32_e32 v240, 16, v242
	v_and_b32_e32 v241, 0xffff0000, v242
	v_lshlrev_b32_e32 v242, 16, v243
	v_and_b32_e32 v243, 0xffff0000, v243
	v_lshlrev_b32_e32 v200, 16, v201
	v_and_b32_e32 v201, 0xffff0000, v201
	v_lshlrev_b32_e32 v202, 16, v203
	v_and_b32_e32 v203, 0xffff0000, v203
	v_pk_fma_f32 v[156:157], v[156:157], s[90:91], v[206:207] op_sel_hi:[1,0,1]
	v_pk_fma_f32 v[154:155], v[154:155], s[90:91], v[204:205] op_sel_hi:[1,0,1]
	v_pk_fma_f32 v[152:153], v[152:153], s[90:91], v[234:235] op_sel_hi:[1,0,1]
	v_pk_fma_f32 v[150:151], v[150:151], s[90:91], v[226:227] op_sel_hi:[1,0,1]
	v_pk_fma_f32 v[148:149], v[148:149], s[90:91], v[242:243] op_sel_hi:[1,0,1]
	v_pk_fma_f32 v[146:147], v[146:147], s[90:91], v[240:241] op_sel_hi:[1,0,1]
	v_pk_fma_f32 v[160:161], v[160:161], s[90:91], v[202:203] op_sel_hi:[1,0,1]
	v_pk_fma_f32 v[158:159], v[158:159], s[90:91], v[200:201] op_sel_hi:[1,0,1]
	v_cvt_pk_bf16_f32 v154, v154, v155
	v_cvt_pk_bf16_f32 v155, v156, v157
	v_cvt_pk_bf16_f32 v150, v150, v151
	v_cvt_pk_bf16_f32 v151, v152, v153
	v_cvt_pk_bf16_f32 v152, v146, v147
	v_cvt_pk_bf16_f32 v153, v148, v149
	v_cvt_pk_bf16_f32 v158, v158, v159
	v_cvt_pk_bf16_f32 v159, v160, v161
	v_cndmask_b32_e64 v146, v155, v153, s[38:39]
	v_cndmask_b32_e64 v147, v154, v152, s[38:39]
	v_cndmask_b32_e64 v148, v159, v151, s[38:39]
	v_cndmask_b32_e64 v149, v158, v150, s[38:39]
	v_mov_b32_dpp v160, v147 quad_perm:[1,0,3,2] row_mask:0xf bank_mask:0xf bound_ctrl:1
	v_mov_b32_dpp v161, v146 quad_perm:[1,0,3,2] row_mask:0xf bank_mask:0xf bound_ctrl:1
	v_mov_b32_dpp v156, v149 quad_perm:[1,0,3,2] row_mask:0xf bank_mask:0xf bound_ctrl:1
	v_mov_b32_dpp v157, v148 quad_perm:[1,0,3,2] row_mask:0xf bank_mask:0xf bound_ctrl:1
	v_cndmask_b32_e64 v149, v161, v155, s[38:39]
	v_cndmask_b32_e64 v148, v160, v154, s[38:39]
	v_lshl_add_u64 v[154:155], s[44:45], 0, v[224:225]
	v_cndmask_b32_e64 v239, v211, v215, s[38:39]
	v_cndmask_b32_e64 v244, v210, v214, s[38:39]
	v_cndmask_b32_e64 v245, v209, v213, s[38:39]
	v_cndmask_b32_e64 v246, v208, v212, s[38:39]
	v_cndmask_b32_e64 v147, v157, v159, s[38:39]
	v_cndmask_b32_e64 v146, v156, v158, s[38:39]
	v_lshl_add_u64 v[154:155], v[154:155], 0, v[180:181]
	v_cndmask_b32_e64 v153, v153, v161, s[38:39]
	v_cndmask_b32_e64 v152, v152, v160, s[38:39]
	v_cndmask_b32_e64 v151, v151, v157, s[38:39]
	v_cndmask_b32_e64 v150, v150, v156, s[38:39]
	global_store_dwordx4 v[154:155], v[146:149], off
	global_store_dwordx4 v[154:155], v[150:153], off offset:2048
	v_cndmask_b32_e64 v200, v219, v223, s[38:39]
	v_mov_b32_dpp v146, v246 quad_perm:[1,0,3,2] row_mask:0xf bank_mask:0xf bound_ctrl:1
	v_mov_b32_dpp v147, v245 quad_perm:[1,0,3,2] row_mask:0xf bank_mask:0xf bound_ctrl:1
	v_mov_b32_dpp v148, v244 quad_perm:[1,0,3,2] row_mask:0xf bank_mask:0xf bound_ctrl:1
	v_mov_b32_dpp v149, v239 quad_perm:[1,0,3,2] row_mask:0xf bank_mask:0xf bound_ctrl:1
	v_cndmask_b32_e64 v153, v149, v211, s[38:39]
	v_cndmask_b32_e64 v151, v148, v210, s[38:39]
	v_cndmask_b32_e64 v150, v147, v209, s[38:39]
	v_cndmask_b32_e64 v152, v146, v208, s[38:39]
	v_cndmask_b32_e64 v161, v215, v149, s[38:39]
	v_cndmask_b32_e64 v159, v214, v148, s[38:39]
	v_cndmask_b32_e64 v157, v213, v147, s[38:39]
	v_cndmask_b32_e64 v155, v212, v146, s[38:39]
	v_lshlrev_b32_e32 v146, 16, v152
	v_and_b32_e32 v147, 0xffff0000, v152
	v_lshlrev_b32_e32 v148, 16, v150
	v_and_b32_e32 v149, 0xffff0000, v150
	v_lshlrev_b32_e32 v150, 16, v151
	v_and_b32_e32 v151, 0xffff0000, v151
	v_lshlrev_b32_e32 v152, 16, v153
	v_and_b32_e32 v153, 0xffff0000, v153
	v_lshlrev_b32_e32 v154, 16, v155
	v_and_b32_e32 v155, 0xffff0000, v155
	v_lshlrev_b32_e32 v156, 16, v157
	v_and_b32_e32 v157, 0xffff0000, v157
	v_lshlrev_b32_e32 v158, 16, v159
	v_and_b32_e32 v159, 0xffff0000, v159
	v_lshlrev_b32_e32 v160, 16, v161
	v_and_b32_e32 v161, 0xffff0000, v161
	v_pk_fma_f32 v[140:141], v[140:141], s[90:91], v[152:153] op_sel_hi:[1,0,1]
	v_pk_fma_f32 v[138:139], v[138:139], s[90:91], v[150:151] op_sel_hi:[1,0,1]
	v_pk_fma_f32 v[136:137], v[136:137], s[90:91], v[156:157] op_sel_hi:[1,0,1]
	v_pk_fma_f32 v[134:135], v[134:135], s[90:91], v[154:155] op_sel_hi:[1,0,1]
	v_pk_fma_f32 v[132:133], v[132:133], s[90:91], v[160:161] op_sel_hi:[1,0,1]
	v_pk_fma_f32 v[130:131], v[130:131], s[90:91], v[158:159] op_sel_hi:[1,0,1]
	v_pk_fma_f32 v[144:145], v[144:145], s[90:91], v[148:149] op_sel_hi:[1,0,1]
	v_pk_fma_f32 v[142:143], v[142:143], s[90:91], v[146:147] op_sel_hi:[1,0,1]
	v_cvt_pk_bf16_f32 v138, v138, v139
	v_cvt_pk_bf16_f32 v139, v140, v141
	v_cvt_pk_bf16_f32 v134, v134, v135
	v_cvt_pk_bf16_f32 v135, v136, v137
	v_cvt_pk_bf16_f32 v136, v130, v131
	v_cvt_pk_bf16_f32 v137, v132, v133
	v_cvt_pk_bf16_f32 v142, v142, v143
	v_cvt_pk_bf16_f32 v143, v144, v145
	v_cndmask_b32_e64 v130, v139, v137, s[38:39]
	v_cndmask_b32_e64 v131, v138, v136, s[38:39]
	v_cndmask_b32_e64 v132, v143, v135, s[38:39]
	v_cndmask_b32_e64 v133, v142, v134, s[38:39]
	v_mov_b32_dpp v144, v131 quad_perm:[1,0,3,2] row_mask:0xf bank_mask:0xf bound_ctrl:1
	v_mov_b32_dpp v145, v130 quad_perm:[1,0,3,2] row_mask:0xf bank_mask:0xf bound_ctrl:1
	v_mov_b32_dpp v140, v133 quad_perm:[1,0,3,2] row_mask:0xf bank_mask:0xf bound_ctrl:1
	v_mov_b32_dpp v141, v132 quad_perm:[1,0,3,2] row_mask:0xf bank_mask:0xf bound_ctrl:1
	v_cndmask_b32_e64 v133, v145, v139, s[38:39]
	v_cndmask_b32_e64 v132, v144, v138, s[38:39]
	v_lshl_add_u64 v[138:139], s[44:45], 0, v[194:195]
	v_cndmask_b32_e64 v201, v218, v222, s[38:39]
	v_cndmask_b32_e64 v202, v217, v221, s[38:39]
	v_cndmask_b32_e64 v203, v216, v220, s[38:39]
	v_cndmask_b32_e64 v131, v141, v143, s[38:39]
	v_cndmask_b32_e64 v130, v140, v142, s[38:39]
	v_lshl_add_u64 v[138:139], v[138:139], 0, v[180:181]
	v_cndmask_b32_e64 v137, v137, v145, s[38:39]
	v_cndmask_b32_e64 v136, v136, v144, s[38:39]
	v_cndmask_b32_e64 v135, v135, v141, s[38:39]
	v_cndmask_b32_e64 v134, v134, v140, s[38:39]
	global_store_dwordx4 v[138:139], v[130:133], off
	v_mov_b32_e32 v150, 0
	v_mov_b32_e32 v151, 0
	v_mov_b32_e32 v152, 0
	v_mov_b32_e32 v153, 0
	v_mov_b32_e32 v154, 0
	v_mov_b32_e32 v155, 0
	v_mov_b32_e32 v156, 0
	v_mov_b32_e32 v157, 0
	v_mov_b32_e32 v158, 0
	v_mov_b32_e32 v159, 0
	v_mov_b32_e32 v160, 0
	v_mov_b32_e32 v161, 0
	global_store_dwordx4 v[138:139], v[134:137], off offset:2048
	v_cndmask_b32_e64 v146, v169, v165, s[38:39]
	v_mov_b32_dpp v130, v203 quad_perm:[1,0,3,2] row_mask:0xf bank_mask:0xf bound_ctrl:1
	v_mov_b32_dpp v131, v202 quad_perm:[1,0,3,2] row_mask:0xf bank_mask:0xf bound_ctrl:1
	v_mov_b32_dpp v132, v201 quad_perm:[1,0,3,2] row_mask:0xf bank_mask:0xf bound_ctrl:1
	v_mov_b32_dpp v133, v200 quad_perm:[1,0,3,2] row_mask:0xf bank_mask:0xf bound_ctrl:1
	v_cndmask_b32_e64 v137, v133, v219, s[38:39]
	v_cndmask_b32_e64 v135, v132, v218, s[38:39]
	v_cndmask_b32_e64 v134, v131, v217, s[38:39]
	v_cndmask_b32_e64 v136, v130, v216, s[38:39]
	v_cndmask_b32_e64 v145, v223, v133, s[38:39]
	v_cndmask_b32_e64 v143, v222, v132, s[38:39]
	v_cndmask_b32_e64 v141, v221, v131, s[38:39]
	v_cndmask_b32_e64 v139, v220, v130, s[38:39]
	v_lshlrev_b32_e32 v130, 16, v136
	v_and_b32_e32 v131, 0xffff0000, v136
	v_lshlrev_b32_e32 v132, 16, v134
	v_and_b32_e32 v133, 0xffff0000, v134
	v_lshlrev_b32_e32 v134, 16, v135
	v_and_b32_e32 v135, 0xffff0000, v135
	v_lshlrev_b32_e32 v136, 16, v137
	v_and_b32_e32 v137, 0xffff0000, v137
	v_lshlrev_b32_e32 v138, 16, v139
	v_and_b32_e32 v139, 0xffff0000, v139
	v_lshlrev_b32_e32 v140, 16, v141
	v_and_b32_e32 v141, 0xffff0000, v141
	v_lshlrev_b32_e32 v142, 16, v143
	v_and_b32_e32 v143, 0xffff0000, v143
	v_lshlrev_b32_e32 v144, 16, v145
	v_and_b32_e32 v145, 0xffff0000, v145
	v_pk_fma_f32 v[124:125], v[124:125], s[90:91], v[136:137] op_sel_hi:[1,0,1]
	v_pk_fma_f32 v[122:123], v[122:123], s[90:91], v[134:135] op_sel_hi:[1,0,1]
	v_pk_fma_f32 v[120:121], v[120:121], s[90:91], v[140:141] op_sel_hi:[1,0,1]
	v_pk_fma_f32 v[118:119], v[118:119], s[90:91], v[138:139] op_sel_hi:[1,0,1]
	v_pk_fma_f32 v[116:117], v[116:117], s[90:91], v[144:145] op_sel_hi:[1,0,1]
	v_pk_fma_f32 v[114:115], v[114:115], s[90:91], v[142:143] op_sel_hi:[1,0,1]
	v_pk_fma_f32 v[128:129], v[128:129], s[90:91], v[132:133] op_sel_hi:[1,0,1]
	v_pk_fma_f32 v[126:127], v[126:127], s[90:91], v[130:131] op_sel_hi:[1,0,1]
	v_cvt_pk_bf16_f32 v122, v122, v123
	v_cvt_pk_bf16_f32 v123, v124, v125
	v_cvt_pk_bf16_f32 v118, v118, v119
	v_cvt_pk_bf16_f32 v119, v120, v121
	v_cvt_pk_bf16_f32 v120, v114, v115
	v_cvt_pk_bf16_f32 v121, v116, v117
	v_cvt_pk_bf16_f32 v126, v126, v127
	v_cvt_pk_bf16_f32 v127, v128, v129
	v_cndmask_b32_e64 v114, v123, v121, s[38:39]
	v_cndmask_b32_e64 v115, v122, v120, s[38:39]
	v_cndmask_b32_e64 v116, v127, v119, s[38:39]
	v_cndmask_b32_e64 v117, v126, v118, s[38:39]
	v_mov_b32_dpp v128, v115 quad_perm:[1,0,3,2] row_mask:0xf bank_mask:0xf bound_ctrl:1
	v_mov_b32_dpp v129, v114 quad_perm:[1,0,3,2] row_mask:0xf bank_mask:0xf bound_ctrl:1
	v_mov_b32_dpp v124, v117 quad_perm:[1,0,3,2] row_mask:0xf bank_mask:0xf bound_ctrl:1
	v_mov_b32_dpp v125, v116 quad_perm:[1,0,3,2] row_mask:0xf bank_mask:0xf bound_ctrl:1
	v_cndmask_b32_e64 v117, v129, v123, s[38:39]
	v_cndmask_b32_e64 v116, v128, v122, s[38:39]
	v_lshl_add_u64 v[122:123], s[44:45], 0, v[192:193]
	v_cndmask_b32_e64 v147, v168, v164, s[38:39]
	v_cndmask_b32_e64 v148, v167, v163, s[38:39]
	v_cndmask_b32_e64 v149, v166, v162, s[38:39]
	v_cndmask_b32_e64 v115, v125, v127, s[38:39]
	v_cndmask_b32_e64 v114, v124, v126, s[38:39]
	v_lshl_add_u64 v[122:123], v[122:123], 0, v[180:181]
	v_cndmask_b32_e64 v121, v121, v129, s[38:39]
	v_cndmask_b32_e64 v120, v120, v128, s[38:39]
	v_cndmask_b32_e64 v119, v119, v125, s[38:39]
	v_cndmask_b32_e64 v118, v118, v124, s[38:39]
	global_store_dwordx4 v[122:123], v[114:117], off
	v_mov_b32_e32 v134, 0
	v_mov_b32_e32 v135, 0
	v_mov_b32_e32 v136, 0
	v_mov_b32_e32 v137, 0
	v_mov_b32_e32 v138, 0
	v_mov_b32_e32 v139, 0
	v_mov_b32_e32 v140, 0
	v_mov_b32_e32 v141, 0
	v_mov_b32_e32 v142, 0
	v_mov_b32_e32 v143, 0
	v_mov_b32_e32 v144, 0
	v_mov_b32_e32 v145, 0
	global_store_dwordx4 v[122:123], v[118:121], off offset:2048
	v_cndmask_b32_e64 v131, v30, v26, s[38:39]
	v_mov_b32_dpp v114, v149 quad_perm:[1,0,3,2] row_mask:0xf bank_mask:0xf bound_ctrl:1
	v_mov_b32_dpp v115, v148 quad_perm:[1,0,3,2] row_mask:0xf bank_mask:0xf bound_ctrl:1
	v_mov_b32_dpp v116, v147 quad_perm:[1,0,3,2] row_mask:0xf bank_mask:0xf bound_ctrl:1
	v_mov_b32_dpp v117, v146 quad_perm:[1,0,3,2] row_mask:0xf bank_mask:0xf bound_ctrl:1
	v_cndmask_b32_e64 v121, v117, v169, s[38:39]
	v_cndmask_b32_e64 v119, v116, v168, s[38:39]
	v_cndmask_b32_e64 v118, v115, v167, s[38:39]
	v_cndmask_b32_e64 v120, v114, v166, s[38:39]
	v_cndmask_b32_e64 v129, v165, v117, s[38:39]
	v_cndmask_b32_e64 v127, v164, v116, s[38:39]
	v_cndmask_b32_e64 v125, v163, v115, s[38:39]
	v_cndmask_b32_e64 v123, v162, v114, s[38:39]
	v_lshlrev_b32_e32 v114, 16, v120
	v_and_b32_e32 v115, 0xffff0000, v120
	v_lshlrev_b32_e32 v116, 16, v118
	v_and_b32_e32 v117, 0xffff0000, v118
	v_lshlrev_b32_e32 v118, 16, v119
	v_and_b32_e32 v119, 0xffff0000, v119
	v_lshlrev_b32_e32 v120, 16, v121
	v_and_b32_e32 v121, 0xffff0000, v121
	v_lshlrev_b32_e32 v122, 16, v123
	v_and_b32_e32 v123, 0xffff0000, v123
	v_lshlrev_b32_e32 v124, 16, v125
	v_and_b32_e32 v125, 0xffff0000, v125
	v_lshlrev_b32_e32 v126, 16, v127
	v_and_b32_e32 v127, 0xffff0000, v127
	v_lshlrev_b32_e32 v128, 16, v129
	v_and_b32_e32 v129, 0xffff0000, v129
	v_pk_fma_f32 v[108:109], v[108:109], s[90:91], v[120:121] op_sel_hi:[1,0,1]
	v_pk_fma_f32 v[106:107], v[106:107], s[90:91], v[118:119] op_sel_hi:[1,0,1]
	v_pk_fma_f32 v[104:105], v[104:105], s[90:91], v[124:125] op_sel_hi:[1,0,1]
	v_pk_fma_f32 v[102:103], v[102:103], s[90:91], v[122:123] op_sel_hi:[1,0,1]
	v_pk_fma_f32 v[100:101], v[100:101], s[90:91], v[128:129] op_sel_hi:[1,0,1]
	v_pk_fma_f32 v[98:99], v[98:99], s[90:91], v[126:127] op_sel_hi:[1,0,1]
	v_pk_fma_f32 v[112:113], v[112:113], s[90:91], v[116:117] op_sel_hi:[1,0,1]
	v_pk_fma_f32 v[110:111], v[110:111], s[90:91], v[114:115] op_sel_hi:[1,0,1]
	v_cvt_pk_bf16_f32 v106, v106, v107
	v_cvt_pk_bf16_f32 v107, v108, v109
	v_cvt_pk_bf16_f32 v102, v102, v103
	v_cvt_pk_bf16_f32 v103, v104, v105
	v_cvt_pk_bf16_f32 v104, v98, v99
	v_cvt_pk_bf16_f32 v105, v100, v101
	v_cvt_pk_bf16_f32 v110, v110, v111
	v_cvt_pk_bf16_f32 v111, v112, v113
	v_cndmask_b32_e64 v98, v107, v105, s[38:39]
	v_cndmask_b32_e64 v99, v106, v104, s[38:39]
	v_cndmask_b32_e64 v100, v111, v103, s[38:39]
	v_cndmask_b32_e64 v101, v110, v102, s[38:39]
	v_mov_b32_dpp v112, v99 quad_perm:[1,0,3,2] row_mask:0xf bank_mask:0xf bound_ctrl:1
	v_mov_b32_dpp v113, v98 quad_perm:[1,0,3,2] row_mask:0xf bank_mask:0xf bound_ctrl:1
	v_mov_b32_dpp v108, v101 quad_perm:[1,0,3,2] row_mask:0xf bank_mask:0xf bound_ctrl:1
	v_mov_b32_dpp v109, v100 quad_perm:[1,0,3,2] row_mask:0xf bank_mask:0xf bound_ctrl:1
	v_cndmask_b32_e64 v101, v113, v107, s[38:39]
	v_cndmask_b32_e64 v100, v112, v106, s[38:39]
	v_lshl_add_u64 v[106:107], s[44:45], 0, v[190:191]
	v_cndmask_b32_e64 v132, v29, v25, s[38:39]
	v_cndmask_b32_e64 v133, v28, v24, s[38:39]
	v_cndmask_b32_e64 v99, v109, v111, s[38:39]
	v_cndmask_b32_e64 v98, v108, v110, s[38:39]
	v_lshl_add_u64 v[106:107], v[106:107], 0, v[180:181]
	v_cndmask_b32_e64 v130, v31, v27, s[38:39]
	v_cndmask_b32_e64 v105, v105, v113, s[38:39]
	v_cndmask_b32_e64 v104, v104, v112, s[38:39]
	v_cndmask_b32_e64 v103, v103, v109, s[38:39]
	v_cndmask_b32_e64 v102, v102, v108, s[38:39]
	global_store_dwordx4 v[106:107], v[98:101], off
	v_mov_b32_e32 v110, 0
	v_mov_b32_e32 v111, 0
	v_mov_b32_e32 v112, 0
	v_mov_b32_e32 v113, 0
	v_mov_b32_e32 v114, 0
	v_mov_b32_e32 v115, 0
	v_mov_b32_e32 v116, 0
	v_mov_b32_e32 v117, 0
	v_mov_b32_e32 v118, 0
	v_mov_b32_e32 v119, 0
	v_mov_b32_e32 v120, 0
	v_mov_b32_e32 v121, 0
	v_mov_b32_e32 v122, 0
	v_mov_b32_e32 v123, 0
	v_mov_b32_e32 v124, 0
	v_mov_b32_e32 v125, 0
	v_mov_b32_e32 v126, 0
	v_mov_b32_e32 v127, 0
	v_mov_b32_e32 v128, 0
	v_mov_b32_e32 v129, 0
	v_mov_b32_e32 v146, 0
	v_mov_b32_e32 v147, 0
	v_mov_b32_e32 v148, 0
	v_mov_b32_e32 v149, 0
	global_store_dwordx4 v[106:107], v[102:105], off offset:2048
	v_cndmask_b32_e64 v107, v22, v18, s[38:39]
	v_mov_b32_dpp v98, v133 quad_perm:[1,0,3,2] row_mask:0xf bank_mask:0xf bound_ctrl:1
	v_mov_b32_dpp v99, v132 quad_perm:[1,0,3,2] row_mask:0xf bank_mask:0xf bound_ctrl:1
	v_mov_b32_dpp v100, v131 quad_perm:[1,0,3,2] row_mask:0xf bank_mask:0xf bound_ctrl:1
	v_mov_b32_dpp v101, v130 quad_perm:[1,0,3,2] row_mask:0xf bank_mask:0xf bound_ctrl:1
	v_cndmask_b32_e64 v30, v100, v30, s[38:39]
	v_cndmask_b32_e64 v29, v99, v29, s[38:39]
	v_cndmask_b32_e64 v28, v98, v28, s[38:39]
	v_cndmask_b32_e64 v31, v101, v31, s[38:39]
	v_cndmask_b32_e64 v105, v27, v101, s[38:39]
	v_cndmask_b32_e64 v103, v26, v100, s[38:39]
	v_cndmask_b32_e64 v101, v25, v99, s[38:39]
	v_cndmask_b32_e64 v99, v24, v98, s[38:39]
	v_lshlrev_b32_e32 v24, 16, v28
	v_and_b32_e32 v25, 0xffff0000, v28
	v_lshlrev_b32_e32 v26, 16, v29
	v_and_b32_e32 v27, 0xffff0000, v29
	v_lshlrev_b32_e32 v28, 16, v30
	v_and_b32_e32 v29, 0xffff0000, v30
	v_lshlrev_b32_e32 v30, 16, v31
	v_and_b32_e32 v31, 0xffff0000, v31
	v_lshlrev_b32_e32 v98, 16, v99
	v_and_b32_e32 v99, 0xffff0000, v99
	v_lshlrev_b32_e32 v100, 16, v101
	v_and_b32_e32 v101, 0xffff0000, v101
	v_lshlrev_b32_e32 v104, 16, v105
	v_and_b32_e32 v105, 0xffff0000, v105
	v_pk_fma_f32 v[26:27], v[96:97], s[90:91], v[26:27] op_sel_hi:[1,0,1]
	v_pk_fma_f32 v[24:25], v[94:95], s[90:91], v[24:25] op_sel_hi:[1,0,1]
	v_pk_fma_f32 v[28:29], v[90:91], s[90:91], v[28:29] op_sel_hi:[1,0,1]
	v_lshlrev_b32_e32 v102, 16, v103
	v_and_b32_e32 v103, 0xffff0000, v103
	v_pk_fma_f32 v[30:31], v[92:93], s[90:91], v[30:31] op_sel_hi:[1,0,1]
	v_cvt_pk_bf16_f32 v90, v24, v25
	v_cvt_pk_bf16_f32 v91, v26, v27
	v_cvt_pk_bf16_f32 v92, v28, v29
	v_pk_fma_f32 v[24:25], v[88:89], s[90:91], v[100:101] op_sel_hi:[1,0,1]
	v_pk_fma_f32 v[26:27], v[86:87], s[90:91], v[98:99] op_sel_hi:[1,0,1]
	v_pk_fma_f32 v[28:29], v[84:85], s[90:91], v[104:105] op_sel_hi:[1,0,1]
	v_cvt_pk_bf16_f32 v93, v30, v31
	v_pk_fma_f32 v[30:31], v[82:83], s[90:91], v[102:103] op_sel_hi:[1,0,1]
	v_cvt_pk_bf16_f32 v82, v26, v27
	v_cvt_pk_bf16_f32 v83, v24, v25
	v_cvt_pk_bf16_f32 v28, v28, v29
	v_cvt_pk_bf16_f32 v30, v30, v31
	v_cndmask_b32_e64 v24, v93, v28, s[38:39]
	v_cndmask_b32_e64 v26, v91, v83, s[38:39]
	v_cndmask_b32_e64 v27, v90, v82, s[38:39]
	v_cndmask_b32_e64 v25, v92, v30, s[38:39]
	v_mov_b32_dpp v29, v26 quad_perm:[1,0,3,2] row_mask:0xf bank_mask:0xf bound_ctrl:1
	v_mov_b32_dpp v84, v27 quad_perm:[1,0,3,2] row_mask:0xf bank_mask:0xf bound_ctrl:1
	v_mov_b32_dpp v31, v24 quad_perm:[1,0,3,2] row_mask:0xf bank_mask:0xf bound_ctrl:1
	v_mov_b32_dpp v85, v25 quad_perm:[1,0,3,2] row_mask:0xf bank_mask:0xf bound_ctrl:1
	v_cndmask_b32_e64 v27, v31, v93, s[38:39]
	v_cndmask_b32_e64 v25, v29, v91, s[38:39]
	v_cndmask_b32_e64 v31, v28, v31, s[38:39]
	v_cndmask_b32_e64 v29, v83, v29, s[38:39]
	v_cndmask_b32_e64 v28, v82, v84, s[38:39]
	v_lshl_add_u64 v[82:83], s[44:45], 0, v[188:189]
	v_cndmask_b32_e64 v108, v21, v17, s[38:39]
	v_cndmask_b32_e64 v109, v20, v16, s[38:39]
	v_cndmask_b32_e64 v26, v85, v92, s[38:39]
	v_cndmask_b32_e64 v24, v84, v90, s[38:39]
	v_lshl_add_u64 v[82:83], v[82:83], 0, v[180:181]
	v_cndmask_b32_e64 v106, v23, v19, s[38:39]
	v_cndmask_b32_e64 v30, v30, v85, s[38:39]
	global_store_dwordx4 v[82:83], v[24:27], off
	v_mov_b32_e32 v86, 0
	v_mov_b32_e32 v87, 0
	v_mov_b32_e32 v88, 0
	v_mov_b32_e32 v89, 0
	v_mov_b32_e32 v90, 0
	v_mov_b32_e32 v91, 0
	v_mov_b32_e32 v92, 0
	v_mov_b32_e32 v93, 0
	v_mov_b32_e32 v94, 0
	v_mov_b32_e32 v95, 0
	v_mov_b32_e32 v96, 0
	v_mov_b32_e32 v97, 0
	v_mov_b32_e32 v98, 0
	v_mov_b32_e32 v99, 0
	v_mov_b32_e32 v100, 0
	v_mov_b32_e32 v101, 0
	v_mov_b32_e32 v102, 0
	v_mov_b32_e32 v103, 0
	v_mov_b32_e32 v104, 0
	v_mov_b32_e32 v105, 0
	v_mov_b32_e32 v130, 0
	v_mov_b32_e32 v131, 0
	v_mov_b32_e32 v132, 0
	v_mov_b32_e32 v133, 0
	global_store_dwordx4 v[82:83], v[28:31], off offset:2048
	v_cndmask_b32_e64 v83, v14, v10, s[38:39]
	v_mov_b32_dpp v24, v109 quad_perm:[1,0,3,2] row_mask:0xf bank_mask:0xf bound_ctrl:1
	v_mov_b32_dpp v25, v108 quad_perm:[1,0,3,2] row_mask:0xf bank_mask:0xf bound_ctrl:1
	v_mov_b32_dpp v26, v107 quad_perm:[1,0,3,2] row_mask:0xf bank_mask:0xf bound_ctrl:1
	v_mov_b32_dpp v27, v106 quad_perm:[1,0,3,2] row_mask:0xf bank_mask:0xf bound_ctrl:1
	v_cndmask_b32_e64 v22, v26, v22, s[38:39]
	v_cndmask_b32_e64 v21, v25, v21, s[38:39]
	v_cndmask_b32_e64 v20, v24, v20, s[38:39]
	v_cndmask_b32_e64 v23, v27, v23, s[38:39]
	v_cndmask_b32_e64 v31, v19, v27, s[38:39]
	v_cndmask_b32_e64 v29, v18, v26, s[38:39]
	v_cndmask_b32_e64 v27, v17, v25, s[38:39]
	v_cndmask_b32_e64 v25, v16, v24, s[38:39]
	v_lshlrev_b32_e32 v16, 16, v20
	v_and_b32_e32 v17, 0xffff0000, v20
	v_lshlrev_b32_e32 v18, 16, v21
	v_and_b32_e32 v19, 0xffff0000, v21
	v_lshlrev_b32_e32 v20, 16, v22
	v_and_b32_e32 v21, 0xffff0000, v22
	v_lshlrev_b32_e32 v22, 16, v23
	v_and_b32_e32 v23, 0xffff0000, v23
	v_lshlrev_b32_e32 v24, 16, v25
	v_and_b32_e32 v25, 0xffff0000, v25
	v_lshlrev_b32_e32 v26, 16, v27
	v_and_b32_e32 v27, 0xffff0000, v27
	v_lshlrev_b32_e32 v30, 16, v31
	v_and_b32_e32 v31, 0xffff0000, v31
	v_pk_fma_f32 v[18:19], v[80:81], s[90:91], v[18:19] op_sel_hi:[1,0,1]
	v_pk_fma_f32 v[16:17], v[78:79], s[90:91], v[16:17] op_sel_hi:[1,0,1]
	v_pk_fma_f32 v[20:21], v[74:75], s[90:91], v[20:21] op_sel_hi:[1,0,1]
	v_lshlrev_b32_e32 v28, 16, v29
	v_and_b32_e32 v29, 0xffff0000, v29
	v_pk_fma_f32 v[22:23], v[76:77], s[90:91], v[22:23] op_sel_hi:[1,0,1]
	v_cvt_pk_bf16_f32 v74, v16, v17
	v_cvt_pk_bf16_f32 v75, v18, v19
	v_cvt_pk_bf16_f32 v76, v20, v21
	v_pk_fma_f32 v[16:17], v[64:65], s[90:91], v[26:27] op_sel_hi:[1,0,1]
	v_pk_fma_f32 v[18:19], v[62:63], s[90:91], v[24:25] op_sel_hi:[1,0,1]
	v_pk_fma_f32 v[20:21], v[60:61], s[90:91], v[30:31] op_sel_hi:[1,0,1]
	v_cvt_pk_bf16_f32 v77, v22, v23
	v_pk_fma_f32 v[22:23], v[58:59], s[90:91], v[28:29] op_sel_hi:[1,0,1]
	v_cvt_pk_bf16_f32 v24, v18, v19
	v_cvt_pk_bf16_f32 v25, v16, v17
	v_cvt_pk_bf16_f32 v20, v20, v21
	v_cvt_pk_bf16_f32 v22, v22, v23
	v_cndmask_b32_e64 v16, v77, v20, s[38:39]
	v_cndmask_b32_e64 v18, v75, v25, s[38:39]
	v_cndmask_b32_e64 v19, v74, v24, s[38:39]
	v_cndmask_b32_e64 v17, v76, v22, s[38:39]
	v_mov_b32_dpp v21, v18 quad_perm:[1,0,3,2] row_mask:0xf bank_mask:0xf bound_ctrl:1
	v_mov_b32_dpp v26, v19 quad_perm:[1,0,3,2] row_mask:0xf bank_mask:0xf bound_ctrl:1
	v_mov_b32_dpp v23, v16 quad_perm:[1,0,3,2] row_mask:0xf bank_mask:0xf bound_ctrl:1
	v_mov_b32_dpp v27, v17 quad_perm:[1,0,3,2] row_mask:0xf bank_mask:0xf bound_ctrl:1
	v_cndmask_b32_e64 v19, v23, v77, s[38:39]
	v_cndmask_b32_e64 v17, v21, v75, s[38:39]
	v_cndmask_b32_e64 v23, v20, v23, s[38:39]
	v_cndmask_b32_e64 v21, v25, v21, s[38:39]
	v_cndmask_b32_e64 v20, v24, v26, s[38:39]
	v_lshl_add_u64 v[24:25], s[44:45], 0, v[186:187]
	v_cndmask_b32_e64 v84, v13, v9, s[38:39]
	v_cndmask_b32_e64 v85, v12, v8, s[38:39]
	v_cndmask_b32_e64 v18, v27, v76, s[38:39]
	v_cndmask_b32_e64 v16, v26, v74, s[38:39]
	v_lshl_add_u64 v[24:25], v[24:25], 0, v[180:181]
	v_cndmask_b32_e64 v82, v15, v11, s[38:39]
	v_cndmask_b32_e64 v22, v22, v27, s[38:39]
	global_store_dwordx4 v[24:25], v[16:19], off
	v_mov_b32_e32 v58, 0
	v_mov_b32_e32 v59, 0
	v_mov_b32_e32 v60, 0
	v_mov_b32_e32 v61, 0
	v_mov_b32_e32 v62, 0
	v_mov_b32_e32 v63, 0
	v_mov_b32_e32 v64, 0
	v_mov_b32_e32 v65, 0
	v_mov_b32_e32 v74, 0
	v_mov_b32_e32 v75, 0
	v_mov_b32_e32 v76, 0
	v_mov_b32_e32 v77, 0
	v_mov_b32_e32 v78, 0
	v_mov_b32_e32 v79, 0
	v_mov_b32_e32 v80, 0
	v_mov_b32_e32 v81, 0
	v_mov_b32_e32 v106, 0
	v_mov_b32_e32 v107, 0
	v_mov_b32_e32 v108, 0
	v_mov_b32_e32 v109, 0
	global_store_dwordx4 v[24:25], v[20:23], off offset:2048
	v_cndmask_b32_e64 v25, v6, v2, s[38:39]
	v_mov_b32_dpp v16, v85 quad_perm:[1,0,3,2] row_mask:0xf bank_mask:0xf bound_ctrl:1
	v_mov_b32_dpp v17, v84 quad_perm:[1,0,3,2] row_mask:0xf bank_mask:0xf bound_ctrl:1
	v_mov_b32_dpp v18, v83 quad_perm:[1,0,3,2] row_mask:0xf bank_mask:0xf bound_ctrl:1
	v_mov_b32_dpp v19, v82 quad_perm:[1,0,3,2] row_mask:0xf bank_mask:0xf bound_ctrl:1
	v_cndmask_b32_e64 v14, v18, v14, s[38:39]
	v_cndmask_b32_e64 v13, v17, v13, s[38:39]
	v_cndmask_b32_e64 v12, v16, v12, s[38:39]
	v_cndmask_b32_e64 v15, v19, v15, s[38:39]
	v_cndmask_b32_e64 v23, v11, v19, s[38:39]
	v_cndmask_b32_e64 v21, v10, v18, s[38:39]
	v_cndmask_b32_e64 v19, v9, v17, s[38:39]
	v_cndmask_b32_e64 v17, v8, v16, s[38:39]
	v_lshlrev_b32_e32 v8, 16, v12
	v_and_b32_e32 v9, 0xffff0000, v12
	v_lshlrev_b32_e32 v10, 16, v13
	v_and_b32_e32 v11, 0xffff0000, v13
	v_lshlrev_b32_e32 v12, 16, v14
	v_and_b32_e32 v13, 0xffff0000, v14
	v_lshlrev_b32_e32 v14, 16, v15
	v_and_b32_e32 v15, 0xffff0000, v15
	v_lshlrev_b32_e32 v16, 16, v17
	v_and_b32_e32 v17, 0xffff0000, v17
	v_lshlrev_b32_e32 v18, 16, v19
	v_and_b32_e32 v19, 0xffff0000, v19
	v_lshlrev_b32_e32 v22, 16, v23
	v_and_b32_e32 v23, 0xffff0000, v23
	v_pk_fma_f32 v[10:11], v[56:57], s[90:91], v[10:11] op_sel_hi:[1,0,1]
	v_pk_fma_f32 v[8:9], v[54:55], s[90:91], v[8:9] op_sel_hi:[1,0,1]
	v_pk_fma_f32 v[12:13], v[50:51], s[90:91], v[12:13] op_sel_hi:[1,0,1]
	v_lshlrev_b32_e32 v20, 16, v21
	v_and_b32_e32 v21, 0xffff0000, v21
	v_pk_fma_f32 v[14:15], v[52:53], s[90:91], v[14:15] op_sel_hi:[1,0,1]
	v_cvt_pk_bf16_f32 v28, v8, v9
	v_cvt_pk_bf16_f32 v29, v10, v11
	v_cvt_pk_bf16_f32 v30, v12, v13
	v_pk_fma_f32 v[8:9], v[72:73], s[90:91], v[18:19] op_sel_hi:[1,0,1]
	v_pk_fma_f32 v[10:11], v[70:71], s[90:91], v[16:17] op_sel_hi:[1,0,1]
	v_pk_fma_f32 v[12:13], v[68:69], s[90:91], v[22:23] op_sel_hi:[1,0,1]
	v_cvt_pk_bf16_f32 v31, v14, v15
	v_pk_fma_f32 v[14:15], v[66:67], s[90:91], v[20:21] op_sel_hi:[1,0,1]
	v_cvt_pk_bf16_f32 v16, v10, v11
	v_cvt_pk_bf16_f32 v17, v8, v9
	v_cvt_pk_bf16_f32 v12, v12, v13
	v_cvt_pk_bf16_f32 v14, v14, v15
	v_cndmask_b32_e64 v8, v31, v12, s[38:39]
	v_cndmask_b32_e64 v10, v29, v17, s[38:39]
	v_cndmask_b32_e64 v11, v28, v16, s[38:39]
	v_cndmask_b32_e64 v9, v30, v14, s[38:39]
	v_mov_b32_dpp v13, v10 quad_perm:[1,0,3,2] row_mask:0xf bank_mask:0xf bound_ctrl:1
	v_mov_b32_dpp v18, v11 quad_perm:[1,0,3,2] row_mask:0xf bank_mask:0xf bound_ctrl:1
	v_mov_b32_dpp v15, v8 quad_perm:[1,0,3,2] row_mask:0xf bank_mask:0xf bound_ctrl:1
	v_mov_b32_dpp v19, v9 quad_perm:[1,0,3,2] row_mask:0xf bank_mask:0xf bound_ctrl:1
	v_cndmask_b32_e64 v11, v15, v31, s[38:39]
	v_cndmask_b32_e64 v9, v13, v29, s[38:39]
	v_cndmask_b32_e64 v15, v12, v15, s[38:39]
	v_cndmask_b32_e64 v13, v17, v13, s[38:39]
	v_cndmask_b32_e64 v12, v16, v18, s[38:39]
	v_lshl_add_u64 v[16:17], s[44:45], 0, v[184:185]
	v_cndmask_b32_e64 v26, v5, v1, s[38:39]
	v_cndmask_b32_e64 v27, v4, v0, s[38:39]
	v_cndmask_b32_e64 v10, v19, v30, s[38:39]
	v_cndmask_b32_e64 v8, v18, v28, s[38:39]
	v_lshl_add_u64 v[16:17], v[16:17], 0, v[180:181]
	v_cndmask_b32_e64 v24, v7, v3, s[38:39]
	v_cndmask_b32_e64 v14, v14, v19, s[38:39]
	global_store_dwordx4 v[16:17], v[8:11], off
	v_mov_b32_e32 v50, 0
	v_mov_b32_e32 v51, 0
	v_mov_b32_e32 v52, 0
	v_mov_b32_e32 v53, 0
	v_mov_b32_e32 v54, 0
	v_mov_b32_e32 v55, 0
	v_mov_b32_e32 v56, 0
	v_mov_b32_e32 v57, 0
	v_mov_b32_e32 v66, 0
	v_mov_b32_e32 v67, 0
	v_mov_b32_e32 v68, 0
	v_mov_b32_e32 v69, 0
	v_mov_b32_e32 v70, 0
	v_mov_b32_e32 v71, 0
	v_mov_b32_e32 v72, 0
	v_mov_b32_e32 v73, 0
	v_mov_b32_e32 v82, 0
	v_mov_b32_e32 v83, 0
	v_mov_b32_e32 v84, 0
	v_mov_b32_e32 v85, 0
	global_store_dwordx4 v[16:17], v[12:15], off offset:2048
	s_nop 0
	v_mov_b32_dpp v8, v27 quad_perm:[1,0,3,2] row_mask:0xf bank_mask:0xf bound_ctrl:1
	v_mov_b32_dpp v9, v26 quad_perm:[1,0,3,2] row_mask:0xf bank_mask:0xf bound_ctrl:1
	v_mov_b32_dpp v10, v25 quad_perm:[1,0,3,2] row_mask:0xf bank_mask:0xf bound_ctrl:1
	v_mov_b32_dpp v11, v24 quad_perm:[1,0,3,2] row_mask:0xf bank_mask:0xf bound_ctrl:1
	v_cndmask_b32_e64 v6, v10, v6, s[38:39]
	v_cndmask_b32_e64 v5, v9, v5, s[38:39]
	v_cndmask_b32_e64 v4, v8, v4, s[38:39]
	v_cndmask_b32_e64 v7, v11, v7, s[38:39]
	v_cndmask_b32_e64 v15, v3, v11, s[38:39]
	v_cndmask_b32_e64 v13, v2, v10, s[38:39]
	v_cndmask_b32_e64 v11, v1, v9, s[38:39]
	v_cndmask_b32_e64 v9, v0, v8, s[38:39]
	v_lshlrev_b32_e32 v0, 16, v4
	v_and_b32_e32 v1, 0xffff0000, v4
	v_lshlrev_b32_e32 v2, 16, v5
	v_and_b32_e32 v3, 0xffff0000, v5
	v_lshlrev_b32_e32 v4, 16, v6
	v_and_b32_e32 v5, 0xffff0000, v6
	v_lshlrev_b32_e32 v6, 16, v7
	v_and_b32_e32 v7, 0xffff0000, v7
	v_lshlrev_b32_e32 v8, 16, v9
	v_and_b32_e32 v9, 0xffff0000, v9
	v_lshlrev_b32_e32 v10, 16, v11
	v_and_b32_e32 v11, 0xffff0000, v11
	v_lshlrev_b32_e32 v14, 16, v15
	v_and_b32_e32 v15, 0xffff0000, v15
	v_pk_fma_f32 v[2:3], v[38:39], s[90:91], v[2:3] op_sel_hi:[1,0,1]
	v_pk_fma_f32 v[0:1], v[36:37], s[90:91], v[0:1] op_sel_hi:[1,0,1]
	v_pk_fma_f32 v[4:5], v[32:33], s[90:91], v[4:5] op_sel_hi:[1,0,1]
	v_lshlrev_b32_e32 v12, 16, v13
	v_and_b32_e32 v13, 0xffff0000, v13
	v_pk_fma_f32 v[6:7], v[34:35], s[90:91], v[6:7] op_sel_hi:[1,0,1]
	v_cvt_pk_bf16_f32 v16, v0, v1
	v_cvt_pk_bf16_f32 v17, v2, v3
	v_cvt_pk_bf16_f32 v18, v4, v5
	v_pk_fma_f32 v[0:1], v[46:47], s[90:91], v[10:11] op_sel_hi:[1,0,1]
	v_pk_fma_f32 v[2:3], v[44:45], s[90:91], v[8:9] op_sel_hi:[1,0,1]
	v_pk_fma_f32 v[4:5], v[42:43], s[90:91], v[14:15] op_sel_hi:[1,0,1]
	v_cvt_pk_bf16_f32 v19, v6, v7
	v_pk_fma_f32 v[6:7], v[40:41], s[90:91], v[12:13] op_sel_hi:[1,0,1]
	v_cvt_pk_bf16_f32 v8, v2, v3
	v_cvt_pk_bf16_f32 v9, v0, v1
	v_cvt_pk_bf16_f32 v4, v4, v5
	v_cvt_pk_bf16_f32 v6, v6, v7
	v_cndmask_b32_e64 v0, v19, v4, s[38:39]
	v_cndmask_b32_e64 v2, v17, v9, s[38:39]
	v_cndmask_b32_e64 v3, v16, v8, s[38:39]
	v_cndmask_b32_e64 v1, v18, v6, s[38:39]
	v_mov_b32_dpp v5, v2 quad_perm:[1,0,3,2] row_mask:0xf bank_mask:0xf bound_ctrl:1
	v_mov_b32_dpp v10, v3 quad_perm:[1,0,3,2] row_mask:0xf bank_mask:0xf bound_ctrl:1
	v_mov_b32_dpp v7, v0 quad_perm:[1,0,3,2] row_mask:0xf bank_mask:0xf bound_ctrl:1
	v_mov_b32_dpp v11, v1 quad_perm:[1,0,3,2] row_mask:0xf bank_mask:0xf bound_ctrl:1
	v_cndmask_b32_e64 v3, v7, v19, s[38:39]
	v_cndmask_b32_e64 v1, v5, v17, s[38:39]
	v_cndmask_b32_e64 v7, v4, v7, s[38:39]
	v_cndmask_b32_e64 v5, v9, v5, s[38:39]
	v_cndmask_b32_e64 v4, v8, v10, s[38:39]
	v_lshl_add_u64 v[8:9], s[44:45], 0, v[182:183]
	v_cndmask_b32_e64 v2, v11, v18, s[38:39]
	v_cndmask_b32_e64 v0, v10, v16, s[38:39]
	v_lshl_add_u64 v[8:9], v[8:9], 0, v[180:181]
	v_cndmask_b32_e64 v6, v6, v11, s[38:39]
	global_store_dwordx4 v[8:9], v[0:3], off
	v_mov_b32_e32 v32, 0
	v_mov_b32_e32 v33, 0
	v_mov_b32_e32 v34, 0
	v_mov_b32_e32 v35, 0
	v_mov_b32_e32 v36, 0
	v_mov_b32_e32 v37, 0
	v_mov_b32_e32 v38, 0
	v_mov_b32_e32 v39, 0
	v_mov_b32_e32 v40, 0
	v_mov_b32_e32 v41, 0
	v_mov_b32_e32 v42, 0
	v_mov_b32_e32 v43, 0
	v_mov_b32_e32 v44, 0
	v_mov_b32_e32 v45, 0
	v_mov_b32_e32 v46, 0
	v_mov_b32_e32 v47, 0
	global_store_dwordx4 v[8:9], v[4:7], off offset:2048
	s_cbranch_vccnz .LBB0_515
	s_andn2_b64 vcc, exec, s[42:43]
	s_cbranch_vccnz .LBB0_514
	s_barrier
	s_branch .LBB0_514

.LBB0_977:
	v_and_b32_e32 v15, 15, v8
	v_and_b32_e32 v17, 48, v8
	s_add_u32 s40, s56, 0x2f100000
	v_lshl_or_b32 v17, v15, 6, v17
	v_lshlrev_b32_e32 v15, 2, v15
	s_addc_u32 s41, s57, 0
	s_and_b32 s22, s18, 3
	s_lshl_b32 s18, s21, 13
	v_and_b32_e32 v18, 32, v15
	v_bitop3_b32 v19, v17, s18, v18 bitop3:0xde
	s_lshl_b32 s18, s22, 12
	s_add_i32 m0, s12, 0x18000
	v_lshl_add_u64 v[6:7], v[6:7], 0, s[88:89]
	s_lshl_b32 s33, s21, 6
	v_bitop3_b32 v182, v17, s18, v18 bitop3:0xde
	s_waitcnt vmcnt(2)
	s_barrier
	global_load_lds_dwordx4 v[6:7], off
	v_lshl_add_u64 v[4:5], v[4:5], 0, s[88:89]
	s_add_i32 m0, s12, 0x1a000
	s_add_i32 s18, s12, 0x8000
	s_add_i32 s19, s12, 0xa000
	global_load_lds_dwordx4 v[4:5], off
	v_lshl_add_u64 v[0:1], v[0:1], 0, s[88:89]
	s_mov_b32 m0, s18
	s_add_u32 s30, s0, 0x8080
	global_load_lds_dwordx4 v[0:1], off
	v_lshl_add_u64 v[0:1], v[2:3], 0, s[88:89]
	s_mov_b32 m0, s19
	s_addc_u32 s31, s1, 0
	global_load_lds_dwordx4 v[0:1], off
	s_add_i32 m0, s12, 0x1c000
	v_lshl_add_u64 v[0:1], s[30:31], 0, v[164:165]
	global_load_lds_dwordx4 v[0:1], off
	v_lshl_add_u64 v[0:1], s[30:31], 0, v[168:169]
	s_add_i32 m0, s12, 0x1e000
	v_lshrrev_b32_e32 v16, 1, v8
	global_load_lds_dwordx4 v[0:1], off
	v_and_b32_e32 v0, 16, v16
	v_lshl_or_b32 v183, s22, 6, v0
	v_lshlrev_b32_e32 v0, 13, v9
	v_and_b32_e32 v0, 0xffffc000, v0
	v_lshl_add_u32 v0, v10, 10, v0
	v_and_b32_e32 v1, 1, v9
	v_lshl_or_b32 v0, v1, 6, v0
	s_cmpk_lt_u32 s20, 0x100
	v_lshl_add_u32 v170, v11, 1, v0
	v_lshlrev_b32_e32 v0, 13, v12
	s_cselect_b64 s[42:43], -1, 0
	s_lshl_b32 s20, s21, 8
	v_and_b32_e32 v0, 0xffffc000, v0
	s_waitcnt vmcnt(6)
	s_add_i32 s20, s20, 0
	v_lshl_add_u32 v0, v13, 10, v0
	v_and_b32_e32 v1, 1, v12
	s_add_i32 s20, s20, 0x20000
	v_lshl_or_b32 v0, v1, 6, v0
	v_and_or_b32 v184, v8, 31, s33
	v_add_u32_e32 v185, s20, v15
	v_mov_b32_e32 v171, v49
	v_lshl_add_u32 v172, v14, 1, v0
	v_mov_b32_e32 v173, v49
	s_mov_b32 s20, 0
	v_add_u32_e32 v186, 0, v19
	s_barrier
	v_mov_b32_e32 v32, 0
	v_mov_b32_e32 v33, 0
	v_mov_b32_e32 v34, 0
	v_mov_b32_e32 v35, 0
	v_mov_b32_e32 v36, 0
	v_mov_b32_e32 v37, 0
	v_mov_b32_e32 v38, 0
	v_mov_b32_e32 v39, 0
	v_mov_b32_e32 v40, 0
	v_mov_b32_e32 v41, 0
	v_mov_b32_e32 v42, 0
	v_mov_b32_e32 v43, 0
	v_mov_b32_e32 v44, 0
	v_mov_b32_e32 v45, 0
	v_mov_b32_e32 v46, 0
	v_mov_b32_e32 v47, 0
	v_mov_b32_e32 v50, 0
	v_mov_b32_e32 v51, 0
	v_mov_b32_e32 v52, 0
	v_mov_b32_e32 v53, 0
	v_mov_b32_e32 v54, 0
	v_mov_b32_e32 v55, 0
	v_mov_b32_e32 v56, 0
	v_mov_b32_e32 v57, 0
	v_mov_b32_e32 v58, 0
	v_mov_b32_e32 v59, 0
	v_mov_b32_e32 v60, 0
	v_mov_b32_e32 v61, 0
	v_mov_b32_e32 v62, 0
	v_mov_b32_e32 v63, 0
	v_mov_b32_e32 v64, 0
	v_mov_b32_e32 v65, 0
	v_mov_b32_e32 v66, 0
	v_mov_b32_e32 v67, 0
	v_mov_b32_e32 v68, 0
	v_mov_b32_e32 v69, 0
	v_mov_b32_e32 v70, 0
	v_mov_b32_e32 v71, 0
	v_mov_b32_e32 v72, 0
	v_mov_b32_e32 v73, 0
	v_mov_b32_e32 v74, 0
	v_mov_b32_e32 v75, 0
	v_mov_b32_e32 v76, 0
	v_mov_b32_e32 v77, 0
	v_mov_b32_e32 v78, 0
	v_mov_b32_e32 v79, 0
	v_mov_b32_e32 v80, 0
	v_mov_b32_e32 v81, 0
	v_mov_b32_e32 v82, 0
	v_mov_b32_e32 v83, 0
	v_mov_b32_e32 v84, 0
	v_mov_b32_e32 v85, 0
	v_mov_b32_e32 v86, 0
	v_mov_b32_e32 v87, 0
	v_mov_b32_e32 v88, 0
	v_mov_b32_e32 v89, 0
	v_mov_b32_e32 v90, 0
	v_mov_b32_e32 v91, 0
	v_mov_b32_e32 v92, 0
	v_mov_b32_e32 v93, 0
	v_mov_b32_e32 v94, 0
	v_mov_b32_e32 v95, 0
	v_mov_b32_e32 v96, 0
	v_mov_b32_e32 v97, 0
	v_mov_b32_e32 v98, 0
	v_mov_b32_e32 v99, 0
	v_mov_b32_e32 v100, 0
	v_mov_b32_e32 v101, 0
	v_mov_b32_e32 v102, 0
	v_mov_b32_e32 v103, 0
	v_mov_b32_e32 v104, 0
	v_mov_b32_e32 v105, 0
	v_mov_b32_e32 v106, 0
	v_mov_b32_e32 v107, 0
	v_mov_b32_e32 v108, 0
	v_mov_b32_e32 v109, 0
	v_mov_b32_e32 v110, 0
	v_mov_b32_e32 v111, 0
	v_mov_b32_e32 v112, 0
	v_mov_b32_e32 v113, 0
	v_mov_b32_e32 v114, 0
	v_mov_b32_e32 v115, 0
	v_mov_b32_e32 v116, 0
	v_mov_b32_e32 v117, 0
	v_mov_b32_e32 v118, 0
	v_mov_b32_e32 v119, 0
	v_mov_b32_e32 v120, 0
	v_mov_b32_e32 v121, 0
	v_mov_b32_e32 v122, 0
	v_mov_b32_e32 v123, 0
	v_mov_b32_e32 v124, 0
	v_mov_b32_e32 v125, 0
	v_mov_b32_e32 v126, 0
	v_mov_b32_e32 v127, 0
	v_mov_b32_e32 v128, 0
	v_mov_b32_e32 v129, 0
	v_mov_b32_e32 v130, 0
	v_mov_b32_e32 v131, 0
	v_mov_b32_e32 v132, 0
	v_mov_b32_e32 v133, 0
	v_mov_b32_e32 v134, 0
	v_mov_b32_e32 v135, 0
	v_mov_b32_e32 v136, 0
	v_mov_b32_e32 v137, 0
	v_mov_b32_e32 v138, 0
	v_mov_b32_e32 v139, 0
	v_mov_b32_e32 v140, 0
	v_mov_b32_e32 v141, 0
	v_mov_b32_e32 v142, 0
	v_mov_b32_e32 v143, 0
	v_mov_b32_e32 v144, 0
	v_mov_b32_e32 v145, 0
	v_mov_b32_e32 v146, 0
	v_mov_b32_e32 v147, 0
	v_mov_b32_e32 v148, 0
	v_mov_b32_e32 v149, 0
	v_mov_b32_e32 v150, 0
	v_mov_b32_e32 v151, 0
	v_mov_b32_e32 v152, 0
	v_mov_b32_e32 v153, 0
	v_mov_b32_e32 v154, 0
	v_mov_b32_e32 v155, 0
	v_mov_b32_e32 v156, 0
	v_mov_b32_e32 v157, 0
	v_mov_b32_e32 v158, 0
	v_mov_b32_e32 v159, 0
	v_mov_b32_e32 v160, 0
	v_mov_b32_e32 v161, 0
	s_branch .LBB0_980

.LBB0_986:
	s_ashr_i32 s45, s44, 31
	s_lshl_b64 s[30:31], s[44:45], 18
	s_add_u32 s48, s7, s30
	s_addc_u32 s49, s8, s31
	s_and_b64 s[30:31], s[36:37], exec
	s_cselect_b32 s21, s49, s5
	s_cselect_b32 s30, s48, s4
	s_ashr_i32 s47, s46, 31
	s_lshl_b64 s[50:51], s[46:47], 18
	s_add_u32 s50, s9, s50
	s_addc_u32 s51, s10, s51
	s_and_b64 s[56:57], s[36:37], exec
	s_cselect_b32 s31, s51, s1
	s_cselect_b32 s33, s50, s0
	s_add_u32 s56, s4, 0x20080
	s_addc_u32 s57, s5, 0
	s_add_u32 s4, s0, 0x100
	s_addc_u32 s5, s1, 0
	s_mov_b32 s45, -2

.LBB0_990:
	s_nop 15
	s_nop 15
	v_lshl_add_u32 v8, s20, 10, v185
	ds_read2_b32 v[2:3], v8 offset1:16
	v_lshl_add_u32 v6, s52, 8, v184
	s_lshl_b32 s0, s54, 8
	s_and_b32 s0, s0, 0x300
	v_or_b32_e32 v48, s0, v183
	s_waitcnt lgkmcnt(0)
	v_mul_f32_e32 v2, 0x3e800000, v2
	v_pk_mul_f32 v[0:1], v[160:161], v[2:3] op_sel_hi:[1,0]
	v_pk_mul_f32 v[4:5], v[158:159], v[2:3] op_sel_hi:[1,0]
	v_med3_f32 v7, v0, s11, v232
	v_med3_f32 v4, v4, s11, v232
	v_med3_f32 v5, v5, s11, v232
	v_mov_b32_e32 v0, v49
	v_cvt_pk_fp8_f32 v0, v4, v5
	v_med3_f32 v1, v1, s11, v232
	v_pk_mul_f32 v[10:11], v[154:155], v[2:3] op_sel_hi:[1,0]
	v_pk_mul_f32 v[4:5], v[156:157], v[2:3] op_sel_hi:[1,0]
	v_cvt_pk_fp8_f32 v0, v7, v1 op_sel:[0,0,1]
	v_med3_f32 v7, v10, s11, v232
	v_med3_f32 v9, v11, s11, v232
	v_mov_b32_e32 v1, v49
	v_cvt_pk_fp8_f32 v1, v7, v9
	v_pk_mul_f32 v[10:11], v[150:151], v[2:3] op_sel_hi:[1,0]
	v_med3_f32 v4, v4, s11, v232
	v_med3_f32 v7, v10, s11, v232
	v_med3_f32 v9, v11, s11, v232
	v_mov_b32_e32 v10, v49
	v_cvt_pk_fp8_f32 v10, v7, v9
	v_med3_f32 v5, v5, s11, v232
	v_cvt_pk_fp8_f32 v1, v4, v5 op_sel:[0,0,1]
	v_pk_mul_f32 v[4:5], v[152:153], v[2:3] op_sel_hi:[1,0]
	v_pk_mul_f32 v[12:13], v[146:147], v[2:3] op_sel_hi:[1,0]
	v_med3_f32 v4, v4, s11, v232
	v_med3_f32 v5, v5, s11, v232
	v_cvt_pk_fp8_f32 v10, v4, v5 op_sel:[0,0,1]
	v_pk_mul_f32 v[4:5], v[148:149], v[2:3] op_sel_hi:[1,0]
	v_med3_f32 v2, v12, s11, v232
	v_med3_f32 v7, v13, s11, v232
	v_mov_b32_e32 v11, v49
	v_cvt_pk_fp8_f32 v11, v2, v7
	v_med3_f32 v4, v4, s11, v232
	v_med3_f32 v5, v5, s11, v232
	s_mov_b64 s[0:1], 0x20000
	v_cvt_pk_fp8_f32 v11, v4, v5 op_sel:[0,0,1]
	v_mul_f32_e32 v4, 0x3e800000, v3
	v_pk_mul_f32 v[2:3], v[144:145], v[4:5] op_sel_hi:[1,0]
	v_pk_mul_f32 v[12:13], v[142:143], v[4:5] op_sel_hi:[1,0]
	v_med3_f32 v9, v2, s11, v232
	v_med3_f32 v5, v12, s11, v232
	v_med3_f32 v7, v13, s11, v232
	v_mov_b32_e32 v2, v49
	v_cvt_pk_fp8_f32 v2, v5, v7
	v_med3_f32 v3, v3, s11, v232
	v_pk_mul_f32 v[14:15], v[138:139], v[4:5] op_sel_hi:[1,0]
	v_pk_mul_f32 v[12:13], v[140:141], v[4:5] op_sel_hi:[1,0]
	v_cvt_pk_fp8_f32 v2, v9, v3 op_sel:[0,0,1]
	v_med3_f32 v5, v14, s11, v232
	v_med3_f32 v7, v15, s11, v232
	v_mov_b32_e32 v3, v49
	v_cvt_pk_fp8_f32 v3, v5, v7
	v_med3_f32 v9, v12, s11, v232
	v_med3_f32 v12, v13, s11, v232
	v_pk_mul_f32 v[14:15], v[134:135], v[4:5] op_sel_hi:[1,0]
	v_cvt_pk_fp8_f32 v3, v9, v12 op_sel:[0,0,1]
	v_pk_mul_f32 v[12:13], v[136:137], v[4:5] op_sel_hi:[1,0]
	v_med3_f32 v5, v14, s11, v232
	v_med3_f32 v7, v15, s11, v232
	v_med3_f32 v9, v12, s11, v232
	v_mov_b32_e32 v12, v49
	v_cvt_pk_fp8_f32 v12, v5, v7
	v_med3_f32 v13, v13, s11, v232
	v_pk_mul_f32 v[14:15], v[132:133], v[4:5] op_sel_hi:[1,0]
	v_pk_mul_f32 v[4:5], v[130:131], v[4:5] op_sel_hi:[1,0]
	v_cvt_pk_fp8_f32 v12, v9, v13 op_sel:[0,0,1]
	v_med3_f32 v4, v4, s11, v232
	v_med3_f32 v5, v5, s11, v232
	v_mov_b32_e32 v13, v49
	v_cvt_pk_fp8_f32 v13, v4, v5
	v_med3_f32 v7, v14, s11, v232
	v_med3_f32 v9, v15, s11, v232
	v_permlane16_swap_b32_e32 v0, v2
	v_cvt_pk_fp8_f32 v13, v7, v9 op_sel:[0,0,1]
	v_ashrrev_i32_e32 v7, 31, v6
	v_lshlrev_b64 v[4:5], 10, v[6:7]
	v_lshl_add_u64 v[4:5], s[40:41], 0, v[4:5]
	v_lshl_add_u64 v[4:5], v[4:5], 0, v[48:49]
	v_permlane16_swap_b32_e32 v1, v3
	global_store_dwordx4 v[4:5], v[0:3], off
	v_mov_b32_e32 v130, 0
	v_mov_b32_e32 v131, 0
	v_mov_b32_e32 v132, 0
	v_mov_b32_e32 v133, 0
	v_mov_b32_e32 v134, 0
	v_mov_b32_e32 v135, 0
	v_mov_b32_e32 v136, 0
	v_mov_b32_e32 v137, 0
	v_mov_b32_e32 v138, 0
	v_mov_b32_e32 v139, 0
	v_mov_b32_e32 v140, 0
	v_mov_b32_e32 v141, 0
	v_mov_b32_e32 v142, 0
	v_mov_b32_e32 v143, 0
	v_mov_b32_e32 v144, 0
	v_mov_b32_e32 v145, 0
	v_mov_b32_e32 v146, 0
	v_mov_b32_e32 v147, 0
	v_mov_b32_e32 v148, 0
	v_mov_b32_e32 v149, 0
	v_mov_b32_e32 v150, 0
	v_mov_b32_e32 v151, 0
	v_mov_b32_e32 v152, 0
	v_mov_b32_e32 v153, 0
	v_mov_b32_e32 v154, 0
	v_mov_b32_e32 v155, 0
	v_mov_b32_e32 v156, 0
	v_mov_b32_e32 v157, 0
	v_mov_b32_e32 v158, 0
	v_mov_b32_e32 v159, 0
	v_mov_b32_e32 v160, 0
	v_mov_b32_e32 v161, 0
	ds_read2_b32 v[2:3], v8 offset0:32 offset1:48
	v_permlane16_swap_b32_e32 v10, v12
	v_permlane16_swap_b32_e32 v11, v13
	s_waitcnt lgkmcnt(0)
	v_mul_f32_e32 v2, 0x3e800000, v2
	global_store_dwordx4 v[4:5], v[10:13], off offset:32
	v_pk_mul_f32 v[0:1], v[128:129], v[2:3] op_sel_hi:[1,0]
	v_pk_mul_f32 v[14:15], v[114:115], v[2:3] op_sel_hi:[1,0]
	v_pk_mul_f32 v[10:11], v[126:127], v[2:3] op_sel_hi:[1,0]
	v_med3_f32 v1, v1, s11, v232
	v_med3_f32 v7, v10, s11, v232
	v_med3_f32 v9, v11, s11, v232
	v_med3_f32 v10, v0, s11, v232
	v_mov_b32_e32 v0, v49
	v_cvt_pk_fp8_f32 v0, v7, v9
	v_pk_mul_f32 v[12:13], v[122:123], v[2:3] op_sel_hi:[1,0]
	v_or_b32_e32 v6, 32, v6
	v_med3_f32 v7, v12, s11, v232
	v_cvt_pk_fp8_f32 v0, v10, v1 op_sel:[0,0,1]
	v_med3_f32 v9, v13, s11, v232
	v_mov_b32_e32 v1, v49
	v_cvt_pk_fp8_f32 v1, v7, v9
	v_pk_mul_f32 v[10:11], v[124:125], v[2:3] op_sel_hi:[1,0]
	v_pk_mul_f32 v[12:13], v[118:119], v[2:3] op_sel_hi:[1,0]
	v_med3_f32 v10, v10, s11, v232
	v_med3_f32 v11, v11, s11, v232
	v_cvt_pk_fp8_f32 v1, v10, v11 op_sel:[0,0,1]
	v_pk_mul_f32 v[10:11], v[120:121], v[2:3] op_sel_hi:[1,0]
	v_med3_f32 v7, v12, s11, v232
	v_med3_f32 v9, v13, s11, v232
	v_med3_f32 v12, v10, s11, v232
	v_mov_b32_e32 v10, v49
	v_cvt_pk_fp8_f32 v10, v7, v9
	v_med3_f32 v11, v11, s11, v232
	v_med3_f32 v7, v15, s11, v232
	v_cvt_pk_fp8_f32 v10, v12, v11 op_sel:[0,0,1]
	v_pk_mul_f32 v[12:13], v[116:117], v[2:3] op_sel_hi:[1,0]
	v_med3_f32 v2, v14, s11, v232
	v_mov_b32_e32 v11, v49
	v_cvt_pk_fp8_f32 v11, v2, v7
	v_med3_f32 v9, v12, s11, v232
	v_med3_f32 v12, v13, s11, v232
	v_mul_f32_e32 v14, 0x3e800000, v3
	v_cvt_pk_fp8_f32 v11, v9, v12 op_sel:[0,0,1]
	v_pk_mul_f32 v[2:3], v[112:113], v[14:15] op_sel_hi:[1,0]
	v_pk_mul_f32 v[12:13], v[110:111], v[14:15] op_sel_hi:[1,0]
	v_med3_f32 v3, v3, s11, v232
	v_med3_f32 v7, v12, s11, v232
	v_med3_f32 v9, v13, s11, v232
	v_med3_f32 v12, v2, s11, v232
	v_mov_b32_e32 v2, v49
	v_cvt_pk_fp8_f32 v2, v7, v9
	v_pk_mul_f32 v[16:17], v[106:107], v[14:15] op_sel_hi:[1,0]
	v_cvt_pk_fp8_f32 v2, v12, v3 op_sel:[0,0,1]
	v_med3_f32 v7, v16, s11, v232
	v_med3_f32 v9, v17, s11, v232
	v_mov_b32_e32 v3, v49
	v_cvt_pk_fp8_f32 v3, v7, v9
	v_pk_mul_f32 v[12:13], v[108:109], v[14:15] op_sel_hi:[1,0]
	v_pk_mul_f32 v[16:17], v[102:103], v[14:15] op_sel_hi:[1,0]
	v_med3_f32 v12, v12, s11, v232
	v_med3_f32 v13, v13, s11, v232
	v_cvt_pk_fp8_f32 v3, v12, v13 op_sel:[0,0,1]
	v_pk_mul_f32 v[12:13], v[104:105], v[14:15] op_sel_hi:[1,0]
	v_med3_f32 v7, v16, s11, v232
	v_med3_f32 v9, v17, s11, v232
	v_med3_f32 v15, v12, s11, v232
	v_mov_b32_e32 v12, v49
	v_cvt_pk_fp8_f32 v12, v7, v9
	v_med3_f32 v13, v13, s11, v232
	v_pk_mul_f32 v[16:17], v[100:101], v[14:15] op_sel_hi:[1,0]
	v_permlane16_swap_b32_e32 v0, v2
	v_cvt_pk_fp8_f32 v12, v15, v13 op_sel:[0,0,1]
	v_pk_mul_f32 v[14:15], v[98:99], v[14:15] op_sel_hi:[1,0]
	v_mov_b32_e32 v13, v49
	v_med3_f32 v7, v14, s11, v232
	v_med3_f32 v9, v15, s11, v232
	v_cvt_pk_fp8_f32 v13, v7, v9
	v_ashrrev_i32_e32 v7, 31, v6
	v_lshlrev_b64 v[6:7], 10, v[6:7]
	v_lshl_add_u64 v[6:7], s[40:41], 0, v[6:7]
	v_lshl_add_u64 v[6:7], v[6:7], 0, v[48:49]
	v_permlane16_swap_b32_e32 v1, v3
	v_med3_f32 v14, v16, s11, v232
	v_med3_f32 v15, v17, s11, v232
	global_store_dwordx4 v[6:7], v[0:3], off
	v_mov_b32_e32 v98, 0
	v_mov_b32_e32 v99, 0
	v_mov_b32_e32 v100, 0
	v_mov_b32_e32 v101, 0
	v_mov_b32_e32 v102, 0
	v_mov_b32_e32 v103, 0
	v_mov_b32_e32 v104, 0
	v_mov_b32_e32 v105, 0
	v_mov_b32_e32 v106, 0
	v_mov_b32_e32 v107, 0
	v_mov_b32_e32 v108, 0
	v_mov_b32_e32 v109, 0
	v_mov_b32_e32 v110, 0
	v_mov_b32_e32 v111, 0
	v_mov_b32_e32 v112, 0
	v_mov_b32_e32 v113, 0
	v_mov_b32_e32 v114, 0
	v_mov_b32_e32 v115, 0
	v_mov_b32_e32 v116, 0
	v_mov_b32_e32 v117, 0
	v_mov_b32_e32 v118, 0
	v_mov_b32_e32 v119, 0
	v_mov_b32_e32 v120, 0
	v_mov_b32_e32 v121, 0
	v_mov_b32_e32 v122, 0
	v_mov_b32_e32 v123, 0
	v_mov_b32_e32 v124, 0
	v_mov_b32_e32 v125, 0
	v_mov_b32_e32 v126, 0
	v_mov_b32_e32 v127, 0
	v_mov_b32_e32 v128, 0
	v_mov_b32_e32 v129, 0
	ds_read2_b32 v[2:3], v8 offset0:128 offset1:144
	v_cvt_pk_fp8_f32 v13, v14, v15 op_sel:[0,0,1]
	v_permlane16_swap_b32_e32 v10, v12
	s_nop 0
	v_permlane16_swap_b32_e32 v11, v13
	s_waitcnt lgkmcnt(0)
	v_mul_f32_e32 v2, 0x3e800000, v2
	global_store_dwordx4 v[6:7], v[10:13], off offset:32
	v_pk_mul_f32 v[0:1], v[96:97], v[2:3] op_sel_hi:[1,0]
	v_pk_mul_f32 v[6:7], v[94:95], v[2:3] op_sel_hi:[1,0]
	v_med3_f32 v9, v0, s11, v232
	v_med3_f32 v6, v6, s11, v232
	v_med3_f32 v7, v7, s11, v232
	v_mov_b32_e32 v0, v49
	v_cvt_pk_fp8_f32 v0, v6, v7
	v_med3_f32 v1, v1, s11, v232
	v_pk_mul_f32 v[10:11], v[90:91], v[2:3] op_sel_hi:[1,0]
	v_pk_mul_f32 v[6:7], v[92:93], v[2:3] op_sel_hi:[1,0]
	v_cvt_pk_fp8_f32 v0, v9, v1 op_sel:[0,0,1]
	v_med3_f32 v9, v10, s11, v232
	v_med3_f32 v10, v11, s11, v232
	v_mov_b32_e32 v1, v49
	v_cvt_pk_fp8_f32 v1, v9, v10
	v_pk_mul_f32 v[10:11], v[86:87], v[2:3] op_sel_hi:[1,0]
	v_med3_f32 v6, v6, s11, v232
	v_med3_f32 v9, v10, s11, v232
	v_med3_f32 v11, v11, s11, v232
	v_mov_b32_e32 v10, v49
	v_cvt_pk_fp8_f32 v10, v9, v11
	v_med3_f32 v7, v7, s11, v232
	v_cvt_pk_fp8_f32 v1, v6, v7 op_sel:[0,0,1]
	v_pk_mul_f32 v[6:7], v[88:89], v[2:3] op_sel_hi:[1,0]
	v_pk_mul_f32 v[12:13], v[82:83], v[2:3] op_sel_hi:[1,0]
	v_med3_f32 v6, v6, s11, v232
	v_med3_f32 v7, v7, s11, v232
	v_cvt_pk_fp8_f32 v10, v6, v7 op_sel:[0,0,1]
	v_pk_mul_f32 v[6:7], v[84:85], v[2:3] op_sel_hi:[1,0]
	v_med3_f32 v2, v12, s11, v232
	v_med3_f32 v9, v13, s11, v232
	v_mov_b32_e32 v11, v49
	v_cvt_pk_fp8_f32 v11, v2, v9
	v_med3_f32 v6, v6, s11, v232
	v_med3_f32 v7, v7, s11, v232
	v_cvt_pk_fp8_f32 v11, v6, v7 op_sel:[0,0,1]
	v_mul_f32_e32 v6, 0x3e800000, v3
	v_pk_mul_f32 v[2:3], v[80:81], v[6:7] op_sel_hi:[1,0]
	v_pk_mul_f32 v[12:13], v[78:79], v[6:7] op_sel_hi:[1,0]
	v_med3_f32 v3, v3, s11, v232
	v_med3_f32 v7, v12, s11, v232
	v_med3_f32 v9, v13, s11, v232
	v_med3_f32 v12, v2, s11, v232
	v_mov_b32_e32 v2, v49
	v_cvt_pk_fp8_f32 v2, v7, v9
	v_pk_mul_f32 v[14:15], v[74:75], v[6:7] op_sel_hi:[1,0]
	v_cvt_pk_fp8_f32 v2, v12, v3 op_sel:[0,0,1]
	v_pk_mul_f32 v[12:13], v[76:77], v[6:7] op_sel_hi:[1,0]
	v_med3_f32 v7, v14, s11, v232
	v_med3_f32 v9, v15, s11, v232
	v_mov_b32_e32 v3, v49
	v_cvt_pk_fp8_f32 v3, v7, v9
	v_med3_f32 v12, v12, s11, v232
	v_med3_f32 v13, v13, s11, v232
	v_pk_mul_f32 v[14:15], v[70:71], v[6:7] op_sel_hi:[1,0]
	v_cvt_pk_fp8_f32 v3, v12, v13 op_sel:[0,0,1]
	v_pk_mul_f32 v[12:13], v[72:73], v[6:7] op_sel_hi:[1,0]
	v_med3_f32 v7, v14, s11, v232
	v_med3_f32 v9, v15, s11, v232
	v_med3_f32 v14, v12, s11, v232
	v_mov_b32_e32 v12, v49
	v_cvt_pk_fp8_f32 v12, v7, v9
	v_med3_f32 v13, v13, s11, v232
	v_permlane16_swap_b32_e32 v0, v2
	v_cvt_pk_fp8_f32 v12, v14, v13 op_sel:[0,0,1]
	v_pk_mul_f32 v[14:15], v[68:69], v[6:7] op_sel_hi:[1,0]
	v_pk_mul_f32 v[6:7], v[66:67], v[6:7] op_sel_hi:[1,0]
	v_mov_b32_e32 v13, v49
	v_med3_f32 v6, v6, s11, v232
	v_med3_f32 v7, v7, s11, v232
	v_cvt_pk_fp8_f32 v13, v6, v7
	v_med3_f32 v9, v14, s11, v232
	v_med3_f32 v14, v15, s11, v232
	v_lshl_add_u64 v[6:7], v[4:5], 0, s[0:1]
	s_mov_b32 s0, 0x20000
	v_cvt_pk_fp8_f32 v13, v9, v14 op_sel:[0,0,1]
	v_add_co_u32_e32 v14, vcc, s0, v4
	v_permlane16_swap_b32_e32 v1, v3
	s_nop 0
	v_addc_co_u32_e32 v15, vcc, 0, v5, vcc
	global_store_dwordx4 v[14:15], v[0:3], off
	v_mov_b32_e32 v66, 0
	v_mov_b32_e32 v67, 0
	v_mov_b32_e32 v68, 0
	v_mov_b32_e32 v69, 0
	v_mov_b32_e32 v70, 0
	v_mov_b32_e32 v71, 0
	v_mov_b32_e32 v72, 0
	v_mov_b32_e32 v73, 0
	v_mov_b32_e32 v74, 0
	v_mov_b32_e32 v75, 0
	v_mov_b32_e32 v76, 0
	v_mov_b32_e32 v77, 0
	v_mov_b32_e32 v78, 0
	v_mov_b32_e32 v79, 0
	v_mov_b32_e32 v80, 0
	v_mov_b32_e32 v81, 0
	v_mov_b32_e32 v82, 0
	v_mov_b32_e32 v83, 0
	v_mov_b32_e32 v84, 0
	v_mov_b32_e32 v85, 0
	v_mov_b32_e32 v86, 0
	v_mov_b32_e32 v87, 0
	v_mov_b32_e32 v88, 0
	v_mov_b32_e32 v89, 0
	v_mov_b32_e32 v90, 0
	v_mov_b32_e32 v91, 0
	v_mov_b32_e32 v92, 0
	v_mov_b32_e32 v93, 0
	v_mov_b32_e32 v94, 0
	v_mov_b32_e32 v95, 0
	v_mov_b32_e32 v96, 0
	v_mov_b32_e32 v97, 0
	ds_read2_b32 v[2:3], v8 offset0:160 offset1:176
	v_permlane16_swap_b32_e32 v10, v12
	v_permlane16_swap_b32_e32 v11, v13
	s_waitcnt lgkmcnt(0)
	v_mul_f32_e32 v2, 0x3e800000, v2
	global_store_dwordx4 v[6:7], v[10:13], off offset:32
	v_pk_mul_f32 v[0:1], v[60:61], v[2:3] op_sel_hi:[1,0]
	v_pk_mul_f32 v[6:7], v[58:59], v[2:3] op_sel_hi:[1,0]
	v_med3_f32 v8, v0, s11, v232
	v_med3_f32 v6, v6, s11, v232
	v_med3_f32 v7, v7, s11, v232
	v_mov_b32_e32 v0, v49
	v_cvt_pk_fp8_f32 v0, v6, v7
	v_med3_f32 v1, v1, s11, v232
	v_pk_mul_f32 v[6:7], v[52:53], v[2:3] op_sel_hi:[1,0]
	s_mov_b64 s[0:1], 0x28000
	v_cvt_pk_fp8_f32 v0, v8, v1 op_sel:[0,0,1]
	v_pk_mul_f32 v[8:9], v[50:51], v[2:3] op_sel_hi:[1,0]
	v_mov_b32_e32 v1, v49
	v_med3_f32 v8, v8, s11, v232
	v_med3_f32 v9, v9, s11, v232
	v_cvt_pk_fp8_f32 v1, v8, v9
	v_med3_f32 v6, v6, s11, v232
	v_med3_f32 v7, v7, s11, v232
	v_pk_mul_f32 v[8:9], v[62:63], v[2:3] op_sel_hi:[1,0]
	v_cvt_pk_fp8_f32 v1, v6, v7 op_sel:[0,0,1]
	v_pk_mul_f32 v[6:7], v[64:65], v[2:3] op_sel_hi:[1,0]
	v_med3_f32 v8, v8, s11, v232
	v_med3_f32 v9, v9, s11, v232
	v_med3_f32 v10, v6, s11, v232
	v_mov_b32_e32 v6, v49
	v_cvt_pk_fp8_f32 v6, v8, v9
	v_med3_f32 v7, v7, s11, v232
	v_pk_mul_f32 v[8:9], v[56:57], v[2:3] op_sel_hi:[1,0]
	v_cvt_pk_fp8_f32 v6, v10, v7 op_sel:[0,0,1]
	v_pk_mul_f32 v[10:11], v[54:55], v[2:3] op_sel_hi:[1,0]
	v_mov_b32_e32 v7, v49
	v_med3_f32 v2, v10, s11, v232
	v_med3_f32 v10, v11, s11, v232
	v_cvt_pk_fp8_f32 v7, v2, v10
	v_med3_f32 v8, v8, s11, v232
	v_med3_f32 v9, v9, s11, v232
	v_mul_f32_e32 v10, 0x3e800000, v3
	v_cvt_pk_fp8_f32 v7, v8, v9 op_sel:[0,0,1]
	v_pk_mul_f32 v[2:3], v[42:43], v[10:11] op_sel_hi:[1,0]
	v_pk_mul_f32 v[8:9], v[40:41], v[10:11] op_sel_hi:[1,0]
	v_med3_f32 v11, v2, s11, v232
	v_med3_f32 v8, v8, s11, v232
	v_med3_f32 v9, v9, s11, v232
	v_mov_b32_e32 v2, v49
	v_cvt_pk_fp8_f32 v2, v8, v9
	v_med3_f32 v3, v3, s11, v232
	v_pk_mul_f32 v[12:13], v[32:33], v[10:11] op_sel_hi:[1,0]
	v_pk_mul_f32 v[8:9], v[34:35], v[10:11] op_sel_hi:[1,0]
	v_cvt_pk_fp8_f32 v2, v11, v3 op_sel:[0,0,1]
	v_med3_f32 v11, v12, s11, v232
	v_med3_f32 v12, v13, s11, v232
	v_mov_b32_e32 v3, v49
	v_cvt_pk_fp8_f32 v3, v11, v12
	v_med3_f32 v8, v8, s11, v232
	v_med3_f32 v9, v9, s11, v232
	v_pk_mul_f32 v[12:13], v[44:45], v[10:11] op_sel_hi:[1,0]
	v_cvt_pk_fp8_f32 v3, v8, v9 op_sel:[0,0,1]
	v_pk_mul_f32 v[8:9], v[46:47], v[10:11] op_sel_hi:[1,0]
	v_med3_f32 v11, v12, s11, v232
	v_med3_f32 v12, v13, s11, v232
	v_med3_f32 v13, v8, s11, v232
	v_mov_b32_e32 v8, v49
	v_cvt_pk_fp8_f32 v8, v11, v12
	v_med3_f32 v9, v9, s11, v232
	v_permlane16_swap_b32_e32 v0, v2
	v_cvt_pk_fp8_f32 v8, v13, v9 op_sel:[0,0,1]
	v_pk_mul_f32 v[12:13], v[38:39], v[10:11] op_sel_hi:[1,0]
	v_pk_mul_f32 v[10:11], v[36:37], v[10:11] op_sel_hi:[1,0]
	v_mov_b32_e32 v9, v49
	v_med3_f32 v10, v10, s11, v232
	v_med3_f32 v11, v11, s11, v232
	v_cvt_pk_fp8_f32 v9, v10, v11
	v_med3_f32 v12, v12, s11, v232
	v_med3_f32 v13, v13, s11, v232
	v_lshl_add_u64 v[10:11], v[4:5], 0, s[0:1]
	v_cvt_pk_fp8_f32 v9, v12, v13 op_sel:[0,0,1]
	v_add_co_u32_e32 v4, vcc, 0x28000, v4
	v_permlane16_swap_b32_e32 v1, v3
	s_nop 0
	v_addc_co_u32_e32 v5, vcc, 0, v5, vcc
	v_permlane16_swap_b32_e32 v6, v8
	v_permlane16_swap_b32_e32 v7, v9
	s_mov_b64 s[0:1], -1
	s_andn2_b64 vcc, exec, s[36:37]
	global_store_dwordx4 v[4:5], v[0:3], off
	v_mov_b32_e32 v32, 0
	v_mov_b32_e32 v33, 0
	v_mov_b32_e32 v34, 0
	v_mov_b32_e32 v35, 0
	v_mov_b32_e32 v36, 0
	v_mov_b32_e32 v37, 0
	v_mov_b32_e32 v38, 0
	v_mov_b32_e32 v39, 0
	v_mov_b32_e32 v40, 0
	v_mov_b32_e32 v41, 0
	v_mov_b32_e32 v42, 0
	v_mov_b32_e32 v43, 0
	v_mov_b32_e32 v44, 0
	v_mov_b32_e32 v45, 0
	v_mov_b32_e32 v46, 0
	v_mov_b32_e32 v47, 0
	v_mov_b32_e32 v50, 0
	v_mov_b32_e32 v51, 0
	v_mov_b32_e32 v52, 0
	v_mov_b32_e32 v53, 0
	v_mov_b32_e32 v54, 0
	v_mov_b32_e32 v55, 0
	v_mov_b32_e32 v56, 0
	v_mov_b32_e32 v57, 0
	v_mov_b32_e32 v58, 0
	v_mov_b32_e32 v59, 0
	v_mov_b32_e32 v60, 0
	v_mov_b32_e32 v61, 0
	v_mov_b32_e32 v62, 0
	v_mov_b32_e32 v63, 0
	v_mov_b32_e32 v64, 0
	v_mov_b32_e32 v65, 0
	global_store_dwordx4 v[10:11], v[6:9], off offset:32
	s_cbranch_vccnz .LBB0_979
	s_andn2_b64 vcc, exec, s[38:39]
	s_cbranch_vccnz .LBB0_978
	s_barrier
	s_branch .LBB0_978
